# non-temporal (nt) policy on read-once streaming loads in P0 P1 P4 P5 P9 and hgrn prefetch, on top of v12
# speedup vs baseline: 1.0168x; 1.0102x over previous
.LBB0_13:
	v_lshl_add_u64 v[38:39], v[36:37], 0, s[4:5]
	v_add_co_u32_e32 v110, vcc, s2, v38
	global_load_dwordx4 v[42:45], v[38:39], off nt
	s_nop 0
	v_addc_co_u32_e32 v111, vcc, 0, v39, vcc
	v_add_co_u32_e32 v114, vcc, s3, v38
	v_mov_b32_e32 v106, s15
	s_nop 0
	v_addc_co_u32_e32 v115, vcc, 0, v39, vcc
	v_add_co_u32_e32 v118, vcc, s6, v38
	ds_read_b128 v[46:49], v106
	ds_read_b128 v[50:53], v106 offset:16
	ds_read_b128 v[54:57], v106 offset:256
	ds_read_b128 v[58:61], v106 offset:272
	ds_read_b128 v[62:65], v106 offset:512
	ds_read_b128 v[66:69], v106 offset:528
	ds_read_b128 v[70:73], v106 offset:768
	ds_read_b128 v[74:77], v106 offset:784
	ds_read_b128 v[78:81], v106 offset:1024
	ds_read_b128 v[82:85], v106 offset:1040
	ds_read_b128 v[86:89], v106 offset:1280
	ds_read_b128 v[90:93], v106 offset:1296
	ds_read_b128 v[94:97], v106 offset:1536
	ds_read_b128 v[98:101], v106 offset:1552
	ds_read_b128 v[102:105], v106 offset:1792
	ds_read_b128 v[106:109], v106 offset:1808
	v_addc_co_u32_e32 v119, vcc, 0, v39, vcc
	v_add_co_u32_e32 v122, vcc, s7, v38
	s_waitcnt lgkmcnt(13)
	v_mov_b32_e32 v138, v57
	v_addc_co_u32_e32 v123, vcc, 0, v39, vcc
	v_add_co_u32_e32 v126, vcc, s10, v38
	s_waitcnt lgkmcnt(11)
	v_mov_b32_e32 v140, v65
	v_addc_co_u32_e32 v127, vcc, 0, v39, vcc
	v_add_co_u32_e32 v130, vcc, s11, v38
	s_waitcnt lgkmcnt(9)
	v_mov_b32_e32 v142, v73
	v_addc_co_u32_e32 v131, vcc, 0, v39, vcc
	v_add_co_u32_e32 v38, vcc, s12, v38
	s_waitcnt lgkmcnt(7)
	v_mov_b32_e32 v144, v81
	v_addc_co_u32_e32 v39, vcc, 0, v39, vcc
	global_load_dwordx4 v[110:113], v[110:111], off nt
	s_nop 0
	global_load_dwordx4 v[114:117], v[114:115], off nt
	s_nop 0
	global_load_dwordx4 v[118:121], v[118:119], off nt
	s_nop 0
	global_load_dwordx4 v[122:125], v[122:123], off nt
	s_nop 0
	global_load_dwordx4 v[126:129], v[126:127], off nt
	s_nop 0
	global_load_dwordx4 v[130:133], v[130:131], off nt
	s_nop 0
	global_load_dwordx4 v[134:137], v[38:39], off nt
	v_mov_b32_e32 v38, v49
	s_waitcnt lgkmcnt(5)
	v_mov_b32_e32 v146, v89
	s_waitcnt lgkmcnt(3)
	v_mov_b32_e32 v148, v97
	s_waitcnt lgkmcnt(1)
	v_mov_b32_e32 v150, v105
	s_add_u32 s4, s4, 0x60000
	s_addc_u32 s5, s5, 0
	s_add_i32 s15, s15, 32
	v_mov_b32_e32 v152, v53
	v_mov_b32_e32 v154, v61
	v_mov_b32_e32 v156, v69
	v_mov_b32_e32 v158, v77
	v_mov_b32_e32 v160, v85
	v_mov_b32_e32 v162, v93
	v_mov_b32_e32 v164, v101
	s_waitcnt lgkmcnt(0)
	v_mov_b32_e32 v166, v109
	s_cmp_eq_u32 s4, 0x300000
	s_waitcnt vmcnt(7)
	v_pk_fma_f32 v[32:33], v[44:45], v[46:47], v[32:33] op_sel_hi:[1,0,1]
	v_pk_fma_f32 v[30:31], v[42:43], v[46:47], v[30:31] op_sel_hi:[1,0,1]
	v_pk_fma_f32 v[28:29], v[44:45], v[54:55], v[28:29] op_sel_hi:[1,0,1]
	v_pk_fma_f32 v[26:27], v[42:43], v[54:55], v[26:27] op_sel_hi:[1,0,1]
	v_pk_fma_f32 v[24:25], v[44:45], v[62:63], v[24:25] op_sel_hi:[1,0,1]
	v_pk_fma_f32 v[22:23], v[42:43], v[62:63], v[22:23] op_sel_hi:[1,0,1]
	v_pk_fma_f32 v[20:21], v[44:45], v[70:71], v[20:21] op_sel_hi:[1,0,1]
	v_pk_fma_f32 v[18:19], v[42:43], v[70:71], v[18:19] op_sel_hi:[1,0,1]
	v_pk_fma_f32 v[16:17], v[44:45], v[78:79], v[16:17] op_sel_hi:[1,0,1]
	v_pk_fma_f32 v[14:15], v[42:43], v[78:79], v[14:15] op_sel_hi:[1,0,1]
	v_pk_fma_f32 v[12:13], v[44:45], v[86:87], v[12:13] op_sel_hi:[1,0,1]
	v_pk_fma_f32 v[10:11], v[42:43], v[86:87], v[10:11] op_sel_hi:[1,0,1]
	v_pk_fma_f32 v[8:9], v[44:45], v[94:95], v[8:9] op_sel_hi:[1,0,1]
	v_pk_fma_f32 v[6:7], v[42:43], v[94:95], v[6:7] op_sel_hi:[1,0,1]
	v_pk_fma_f32 v[4:5], v[44:45], v[102:103], v[4:5] op_sel_hi:[1,0,1]
	v_pk_fma_f32 v[2:3], v[42:43], v[102:103], v[2:3] op_sel_hi:[1,0,1]
	s_waitcnt vmcnt(6)
	v_pk_fma_f32 v[30:31], v[110:111], v[46:47], v[30:31] op_sel:[0,1,0]
	v_pk_fma_f32 v[32:33], v[112:113], v[46:47], v[32:33] op_sel:[0,1,0]
	v_pk_fma_f32 v[26:27], v[110:111], v[54:55], v[26:27] op_sel:[0,1,0]
	v_pk_fma_f32 v[28:29], v[112:113], v[54:55], v[28:29] op_sel:[0,1,0]
	v_pk_fma_f32 v[22:23], v[110:111], v[62:63], v[22:23] op_sel:[0,1,0]
	v_pk_fma_f32 v[24:25], v[112:113], v[62:63], v[24:25] op_sel:[0,1,0]
	v_pk_fma_f32 v[18:19], v[110:111], v[70:71], v[18:19] op_sel:[0,1,0]
	v_pk_fma_f32 v[20:21], v[112:113], v[70:71], v[20:21] op_sel:[0,1,0]
	v_pk_fma_f32 v[14:15], v[110:111], v[78:79], v[14:15] op_sel:[0,1,0]
	v_pk_fma_f32 v[16:17], v[112:113], v[78:79], v[16:17] op_sel:[0,1,0]
	v_pk_fma_f32 v[10:11], v[110:111], v[86:87], v[10:11] op_sel:[0,1,0]
	v_pk_fma_f32 v[12:13], v[112:113], v[86:87], v[12:13] op_sel:[0,1,0]
	v_pk_fma_f32 v[6:7], v[110:111], v[94:95], v[6:7] op_sel:[0,1,0]
	v_pk_fma_f32 v[8:9], v[112:113], v[94:95], v[8:9] op_sel:[0,1,0]
	v_pk_fma_f32 v[2:3], v[110:111], v[102:103], v[2:3] op_sel:[0,1,0]
	v_pk_fma_f32 v[4:5], v[112:113], v[102:103], v[4:5] op_sel:[0,1,0]
	s_waitcnt vmcnt(5)
	v_pk_fma_f32 v[32:33], v[116:117], v[48:49], v[32:33] op_sel_hi:[1,0,1]
	v_pk_fma_f32 v[30:31], v[114:115], v[48:49], v[30:31] op_sel_hi:[1,0,1]
	v_pk_fma_f32 v[28:29], v[116:117], v[56:57], v[28:29] op_sel_hi:[1,0,1]
	v_pk_fma_f32 v[26:27], v[114:115], v[56:57], v[26:27] op_sel_hi:[1,0,1]
	v_pk_fma_f32 v[24:25], v[116:117], v[64:65], v[24:25] op_sel_hi:[1,0,1]
	v_pk_fma_f32 v[22:23], v[114:115], v[64:65], v[22:23] op_sel_hi:[1,0,1]
	v_pk_fma_f32 v[20:21], v[116:117], v[72:73], v[20:21] op_sel_hi:[1,0,1]
	v_pk_fma_f32 v[18:19], v[114:115], v[72:73], v[18:19] op_sel_hi:[1,0,1]
	v_pk_fma_f32 v[16:17], v[116:117], v[80:81], v[16:17] op_sel_hi:[1,0,1]
	v_pk_fma_f32 v[14:15], v[114:115], v[80:81], v[14:15] op_sel_hi:[1,0,1]
	v_pk_fma_f32 v[12:13], v[116:117], v[88:89], v[12:13] op_sel_hi:[1,0,1]
	v_pk_fma_f32 v[10:11], v[114:115], v[88:89], v[10:11] op_sel_hi:[1,0,1]
	v_pk_fma_f32 v[8:9], v[116:117], v[96:97], v[8:9] op_sel_hi:[1,0,1]
	v_pk_fma_f32 v[6:7], v[114:115], v[96:97], v[6:7] op_sel_hi:[1,0,1]
	v_pk_fma_f32 v[4:5], v[116:117], v[104:105], v[4:5] op_sel_hi:[1,0,1]
	v_pk_fma_f32 v[2:3], v[114:115], v[104:105], v[2:3] op_sel_hi:[1,0,1]
	s_waitcnt vmcnt(4)
	v_pk_fma_f32 v[32:33], v[120:121], v[38:39], v[32:33] op_sel_hi:[1,0,1]
	v_pk_fma_f32 v[30:31], v[118:119], v[38:39], v[30:31] op_sel_hi:[1,0,1]
	v_pk_fma_f32 v[28:29], v[120:121], v[138:139], v[28:29] op_sel_hi:[1,0,1]
	v_pk_fma_f32 v[26:27], v[118:119], v[138:139], v[26:27] op_sel_hi:[1,0,1]
	v_pk_fma_f32 v[24:25], v[120:121], v[140:141], v[24:25] op_sel_hi:[1,0,1]
	v_pk_fma_f32 v[22:23], v[118:119], v[140:141], v[22:23] op_sel_hi:[1,0,1]
	v_pk_fma_f32 v[20:21], v[120:121], v[142:143], v[20:21] op_sel_hi:[1,0,1]
	v_pk_fma_f32 v[18:19], v[118:119], v[142:143], v[18:19] op_sel_hi:[1,0,1]
	v_pk_fma_f32 v[16:17], v[120:121], v[144:145], v[16:17] op_sel_hi:[1,0,1]
	v_pk_fma_f32 v[14:15], v[118:119], v[144:145], v[14:15] op_sel_hi:[1,0,1]
	v_pk_fma_f32 v[12:13], v[120:121], v[146:147], v[12:13] op_sel_hi:[1,0,1]
	v_pk_fma_f32 v[10:11], v[118:119], v[146:147], v[10:11] op_sel_hi:[1,0,1]
	v_pk_fma_f32 v[8:9], v[120:121], v[148:149], v[8:9] op_sel_hi:[1,0,1]
	v_pk_fma_f32 v[6:7], v[118:119], v[148:149], v[6:7] op_sel_hi:[1,0,1]
	v_pk_fma_f32 v[4:5], v[120:121], v[150:151], v[4:5] op_sel_hi:[1,0,1]
	v_pk_fma_f32 v[2:3], v[118:119], v[150:151], v[2:3] op_sel_hi:[1,0,1]
	s_waitcnt vmcnt(3)
	v_pk_fma_f32 v[32:33], v[124:125], v[50:51], v[32:33] op_sel_hi:[1,0,1]
	v_pk_fma_f32 v[30:31], v[122:123], v[50:51], v[30:31] op_sel_hi:[1,0,1]
	v_pk_fma_f32 v[28:29], v[124:125], v[58:59], v[28:29] op_sel_hi:[1,0,1]
	v_pk_fma_f32 v[26:27], v[122:123], v[58:59], v[26:27] op_sel_hi:[1,0,1]
	v_pk_fma_f32 v[24:25], v[124:125], v[66:67], v[24:25] op_sel_hi:[1,0,1]
	v_pk_fma_f32 v[22:23], v[122:123], v[66:67], v[22:23] op_sel_hi:[1,0,1]
	v_pk_fma_f32 v[20:21], v[124:125], v[74:75], v[20:21] op_sel_hi:[1,0,1]
	v_pk_fma_f32 v[18:19], v[122:123], v[74:75], v[18:19] op_sel_hi:[1,0,1]
	v_pk_fma_f32 v[16:17], v[124:125], v[82:83], v[16:17] op_sel_hi:[1,0,1]
	v_pk_fma_f32 v[14:15], v[122:123], v[82:83], v[14:15] op_sel_hi:[1,0,1]
	v_pk_fma_f32 v[12:13], v[124:125], v[90:91], v[12:13] op_sel_hi:[1,0,1]
	v_pk_fma_f32 v[10:11], v[122:123], v[90:91], v[10:11] op_sel_hi:[1,0,1]
	v_pk_fma_f32 v[8:9], v[124:125], v[98:99], v[8:9] op_sel_hi:[1,0,1]
	v_pk_fma_f32 v[6:7], v[122:123], v[98:99], v[6:7] op_sel_hi:[1,0,1]
	v_pk_fma_f32 v[4:5], v[124:125], v[106:107], v[4:5] op_sel_hi:[1,0,1]
	v_pk_fma_f32 v[2:3], v[122:123], v[106:107], v[2:3] op_sel_hi:[1,0,1]
	s_waitcnt vmcnt(2)
	v_pk_fma_f32 v[32:33], v[128:129], v[50:51], v[32:33] op_sel:[0,1,0]
	v_pk_fma_f32 v[30:31], v[126:127], v[50:51], v[30:31] op_sel:[0,1,0]
	v_pk_fma_f32 v[28:29], v[128:129], v[58:59], v[28:29] op_sel:[0,1,0]
	v_pk_fma_f32 v[26:27], v[126:127], v[58:59], v[26:27] op_sel:[0,1,0]
	v_pk_fma_f32 v[24:25], v[128:129], v[66:67], v[24:25] op_sel:[0,1,0]
	v_pk_fma_f32 v[22:23], v[126:127], v[66:67], v[22:23] op_sel:[0,1,0]
	v_pk_fma_f32 v[20:21], v[128:129], v[74:75], v[20:21] op_sel:[0,1,0]
	v_pk_fma_f32 v[18:19], v[126:127], v[74:75], v[18:19] op_sel:[0,1,0]
	v_pk_fma_f32 v[16:17], v[128:129], v[82:83], v[16:17] op_sel:[0,1,0]
	v_pk_fma_f32 v[14:15], v[126:127], v[82:83], v[14:15] op_sel:[0,1,0]
	v_pk_fma_f32 v[12:13], v[128:129], v[90:91], v[12:13] op_sel:[0,1,0]
	v_pk_fma_f32 v[10:11], v[126:127], v[90:91], v[10:11] op_sel:[0,1,0]
	v_pk_fma_f32 v[8:9], v[128:129], v[98:99], v[8:9] op_sel:[0,1,0]
	v_pk_fma_f32 v[6:7], v[126:127], v[98:99], v[6:7] op_sel:[0,1,0]
	v_pk_fma_f32 v[4:5], v[128:129], v[106:107], v[4:5] op_sel:[0,1,0]
	v_pk_fma_f32 v[2:3], v[126:127], v[106:107], v[2:3] op_sel:[0,1,0]
	s_waitcnt vmcnt(1)
	v_pk_fma_f32 v[32:33], v[132:133], v[52:53], v[32:33] op_sel_hi:[1,0,1]
	v_pk_fma_f32 v[30:31], v[130:131], v[52:53], v[30:31] op_sel_hi:[1,0,1]
	v_pk_fma_f32 v[28:29], v[132:133], v[60:61], v[28:29] op_sel_hi:[1,0,1]
	v_pk_fma_f32 v[26:27], v[130:131], v[60:61], v[26:27] op_sel_hi:[1,0,1]
	v_pk_fma_f32 v[24:25], v[132:133], v[68:69], v[24:25] op_sel_hi:[1,0,1]
	v_pk_fma_f32 v[22:23], v[130:131], v[68:69], v[22:23] op_sel_hi:[1,0,1]
	v_pk_fma_f32 v[20:21], v[132:133], v[76:77], v[20:21] op_sel_hi:[1,0,1]
	v_pk_fma_f32 v[18:19], v[130:131], v[76:77], v[18:19] op_sel_hi:[1,0,1]
	v_pk_fma_f32 v[16:17], v[132:133], v[84:85], v[16:17] op_sel_hi:[1,0,1]
	v_pk_fma_f32 v[14:15], v[130:131], v[84:85], v[14:15] op_sel_hi:[1,0,1]
	v_pk_fma_f32 v[12:13], v[132:133], v[92:93], v[12:13] op_sel_hi:[1,0,1]
	v_pk_fma_f32 v[10:11], v[130:131], v[92:93], v[10:11] op_sel_hi:[1,0,1]
	v_pk_fma_f32 v[8:9], v[132:133], v[100:101], v[8:9] op_sel_hi:[1,0,1]
	v_pk_fma_f32 v[6:7], v[130:131], v[100:101], v[6:7] op_sel_hi:[1,0,1]
	v_pk_fma_f32 v[4:5], v[132:133], v[108:109], v[4:5] op_sel_hi:[1,0,1]
	v_pk_fma_f32 v[2:3], v[130:131], v[108:109], v[2:3] op_sel_hi:[1,0,1]
	s_waitcnt vmcnt(0)
	v_pk_fma_f32 v[32:33], v[136:137], v[152:153], v[32:33] op_sel_hi:[1,0,1]
	v_pk_fma_f32 v[30:31], v[134:135], v[152:153], v[30:31] op_sel_hi:[1,0,1]
	v_pk_fma_f32 v[28:29], v[136:137], v[154:155], v[28:29] op_sel_hi:[1,0,1]
	v_pk_fma_f32 v[26:27], v[134:135], v[154:155], v[26:27] op_sel_hi:[1,0,1]
	v_pk_fma_f32 v[24:25], v[136:137], v[156:157], v[24:25] op_sel_hi:[1,0,1]
	v_pk_fma_f32 v[22:23], v[134:135], v[156:157], v[22:23] op_sel_hi:[1,0,1]
	v_pk_fma_f32 v[20:21], v[136:137], v[158:159], v[20:21] op_sel_hi:[1,0,1]
	v_pk_fma_f32 v[18:19], v[134:135], v[158:159], v[18:19] op_sel_hi:[1,0,1]
	v_pk_fma_f32 v[16:17], v[136:137], v[160:161], v[16:17] op_sel_hi:[1,0,1]
	v_pk_fma_f32 v[14:15], v[134:135], v[160:161], v[14:15] op_sel_hi:[1,0,1]
	v_pk_fma_f32 v[12:13], v[136:137], v[162:163], v[12:13] op_sel_hi:[1,0,1]
	v_pk_fma_f32 v[10:11], v[134:135], v[162:163], v[10:11] op_sel_hi:[1,0,1]
	v_pk_fma_f32 v[8:9], v[136:137], v[164:165], v[8:9] op_sel_hi:[1,0,1]
	v_pk_fma_f32 v[6:7], v[134:135], v[164:165], v[6:7] op_sel_hi:[1,0,1]
	v_pk_fma_f32 v[4:5], v[136:137], v[166:167], v[4:5] op_sel_hi:[1,0,1]
	v_pk_fma_f32 v[2:3], v[134:135], v[166:167], v[2:3] op_sel_hi:[1,0,1]
	s_cbranch_scc0 .LBB0_13
	s_lshl_b32 s15, s14, 3
	s_mul_i32 s14, s14, 0x60000
	s_mul_hi_i32 s4, s15, 0xc000
	s_add_u32 s5, s8, s14
	s_addc_u32 s14, s9, s4
	s_add_u32 s4, s5, s0
	s_addc_u32 s5, s14, s1
	global_store_dwordx4 v34, v[30:33], s[4:5]
	s_or_b32 s4, s15, 1
	s_mul_hi_i32 s5, s4, 0xc000
	s_mul_i32 s4, s4, 0xc000
	s_add_u32 s4, s8, s4
	s_addc_u32 s5, s9, s5
	s_add_u32 s4, s4, s0
	s_addc_u32 s5, s5, s1
	global_store_dwordx4 v34, v[26:29], s[4:5]
	s_or_b32 s4, s15, 2
	s_mul_hi_i32 s5, s4, 0xc000
	s_mul_i32 s4, s4, 0xc000
	s_add_u32 s4, s8, s4
	s_addc_u32 s5, s9, s5
	s_add_u32 s4, s4, s0
	s_addc_u32 s5, s5, s1
	global_store_dwordx4 v34, v[22:25], s[4:5]
	s_or_b32 s4, s15, 3
	s_mul_hi_i32 s5, s4, 0xc000
	s_mul_i32 s4, s4, 0xc000
	s_add_u32 s4, s8, s4
	s_addc_u32 s5, s9, s5
	s_add_u32 s4, s4, s0
	s_addc_u32 s5, s5, s1
	global_store_dwordx4 v34, v[18:21], s[4:5]
	s_or_b32 s4, s15, 4
	s_mul_hi_i32 s5, s4, 0xc000
	s_mul_i32 s4, s4, 0xc000
	s_add_u32 s4, s8, s4
	s_addc_u32 s5, s9, s5
	s_add_u32 s4, s4, s0
	s_addc_u32 s5, s5, s1
	global_store_dwordx4 v34, v[14:17], s[4:5]
	s_or_b32 s4, s15, 5
	s_mul_hi_i32 s5, s4, 0xc000
	s_mul_i32 s4, s4, 0xc000
	s_add_u32 s4, s8, s4
	s_addc_u32 s5, s9, s5
	s_add_u32 s4, s4, s0
	s_addc_u32 s5, s5, s1
	global_store_dwordx4 v34, v[10:13], s[4:5]
	s_or_b32 s4, s15, 6
	s_mul_hi_i32 s5, s4, 0xc000
	s_mul_i32 s4, s4, 0xc000
	s_add_u32 s4, s8, s4
	s_addc_u32 s5, s9, s5
	s_add_u32 s4, s4, s0
	s_addc_u32 s5, s5, s1
	global_store_dwordx4 v34, v[6:9], s[4:5]
	s_or_b32 s4, s15, 7
	s_mul_hi_i32 s5, s4, 0xc000
	s_mul_i32 s4, s4, 0xc000
	s_add_u32 s4, s8, s4
	s_addc_u32 s5, s9, s5
	s_add_u32 s0, s4, s0
	s_addc_u32 s1, s5, s1
	s_add_i32 s13, s13, s72
	s_cmpk_gt_i32 s13, 0xbf
	global_store_dwordx4 v34, v[2:5], s[0:1]
	s_barrier
	s_cbranch_scc0 .LBB0_12

.LBB0_18:
	s_mul_hi_i32 s0, s20, 0x38e38e39
	s_lshr_b32 s1, s0, 31
	s_ashr_i32 s0, s0, 7
	s_add_i32 s0, s0, s1
	v_readlane_b32 s52, v254, 7
	s_lshl_b32 s10, s0, 6
	s_mul_i32 s1, s0, 0x480000
	v_readlane_b32 s64, v254, 19
	s_mul_hi_i32 s4, s10, 0x12000
	v_readlane_b32 s65, v254, 20
	s_add_u32 s5, s64, s1
	s_mulk_i32 s0, 0xb800
	s_addc_u32 s4, s65, s4
	s_add_i32 s12, s16, s0
	s_ashr_i32 s13, s12, 31
	s_lshl_b64 s[0:1], s[12:13], 2
	s_add_u32 s0, s5, s0
	s_addc_u32 s1, s4, s1
	v_lshl_add_u64 v[34:35], s[0:1], 0, v[86:87]
	v_lshl_add_u64 v[58:59], v[34:35], 0, v[68:69]
	v_add_co_u32_e32 v46, vcc, s18, v58
	v_lshl_add_u64 v[36:37], v[34:35], 0, v[70:71]
	s_nop 0
	v_addc_co_u32_e32 v47, vcc, 0, v59, vcc
	v_add_co_u32_e32 v48, vcc, s19, v58
	global_load_dwordx4 v[50:53], v[58:59], off nt
	global_load_dwordx4 v[38:41], v[36:37], off nt
	v_addc_co_u32_e32 v49, vcc, 0, v59, vcc
	v_add_co_u32_e32 v60, vcc, 0x360000, v58
	v_lshl_add_u64 v[36:37], v[34:35], 0, v[72:73]
	s_nop 0
	v_addc_co_u32_e32 v61, vcc, 0, v59, vcc
	v_add_co_u32_e32 v58, vcc, 0x3f0000, v58
	v_lshl_add_u64 v[34:35], v[34:35], 0, v[74:75]
	s_nop 0
	v_addc_co_u32_e32 v59, vcc, 0, v59, vcc
	global_load_dwordx4 v[42:45], v[36:37], off nt
	s_nop 0
	global_load_dwordx4 v[34:37], v[34:35], off nt
	s_nop 0
	global_load_dwordx4 v[54:57], v[46:47], off nt
	s_nop 0
	global_load_dwordx4 v[46:49], v[48:49], off nt
	s_nop 0
	global_load_dwordx4 v[62:65], v[60:61], off nt
	s_nop 0
	global_load_dwordx4 v[58:61], v[58:59], off nt
	s_add_i32 s11, s2, s20
	s_cmpk_lt_i32 s11, 0x4800
	s_mov_b64 s[0:1], 0
	s_cselect_b64 s[4:5], -1, 0
	s_cmpk_gt_i32 s11, 0x47ff
	s_mov_b64 s[6:7], 0
	v_readlane_b32 s53, v254, 8
	v_readlane_b32 s54, v254, 9
	v_readlane_b32 s55, v254, 10
	v_readlane_b32 s56, v254, 11
	v_readlane_b32 s57, v254, 12
	v_readlane_b32 s58, v254, 13
	v_readlane_b32 s59, v254, 14
	v_readlane_b32 s60, v254, 15
	v_readlane_b32 s61, v254, 16
	v_readlane_b32 s62, v254, 17
	v_readlane_b32 s63, v254, 18
	v_readlane_b32 s66, v254, 21
	v_readlane_b32 s67, v254, 22
	s_cbranch_scc1 .LBB0_20
	s_mul_hi_i32 s0, s11, 0x38e38e39
	s_lshr_b32 s1, s0, 31
	s_ashr_i32 s0, s0, 7
	s_add_i32 s6, s0, s1
	s_mul_i32 s0, s6, 0x240
	s_sub_i32 s7, s11, s0
	s_lshl_b32 s0, s6, 6
	v_readlane_b32 s52, v254, 7
	s_ashr_i32 s1, s0, 31
	s_mul_i32 s6, s6, 0x480000
	v_readlane_b32 s64, v254, 19
	s_mul_hi_i32 s11, s0, 0x12000
	v_readlane_b32 s65, v254, 20
	s_add_u32 s21, s64, s6
	s_addc_u32 s11, s65, s11
	s_lshl_b32 s6, s7, 5
	s_ashr_i32 s7, s6, 31
	s_lshl_b64 s[22:23], s[6:7], 2
	s_add_u32 s22, s21, s22
	s_addc_u32 s23, s11, s23
	v_mov_b32_e32 v85, v67
	v_lshl_add_u64 v[10:11], s[22:23], 0, v[84:85]
	v_lshl_add_u64 v[26:27], v[10:11], 0, v[68:69]
	v_add_co_u32_e32 v18, vcc, s18, v26
	v_lshl_add_u64 v[6:7], v[10:11], 0, v[70:71]
	s_nop 0
	v_addc_co_u32_e32 v19, vcc, 0, v27, vcc
	v_add_co_u32_e32 v22, vcc, 0x2d0000, v26
	v_lshl_add_u64 v[12:13], v[10:11], 0, v[72:73]
	s_nop 0
	v_addc_co_u32_e32 v23, vcc, 0, v27, vcc
	v_add_co_u32_e32 v28, vcc, 0x360000, v26
	v_lshl_add_u64 v[14:15], v[10:11], 0, v[74:75]
	s_nop 0
	v_addc_co_u32_e32 v29, vcc, 0, v27, vcc
	v_add_co_u32_e32 v30, vcc, 0x3f0000, v26
	global_load_dwordx4 v[2:5], v[26:27], off nt
	s_nop 0
	global_load_dwordx4 v[6:9], v[6:7], off nt
	v_addc_co_u32_e32 v31, vcc, 0, v27, vcc
	global_load_dwordx4 v[10:13], v[12:13], off nt
	s_nop 0
	global_load_dwordx4 v[14:17], v[14:15], off nt
	s_nop 0
	global_load_dwordx4 v[18:21], v[18:19], off nt
	s_nop 0
	global_load_dwordx4 v[22:25], v[22:23], off nt
	s_nop 0
	global_load_dwordx4 v[26:29], v[28:29], off nt
	s_nop 0
	global_load_dwordx4 v[30:33], v[30:31], off nt
	s_lshl_b64 s[6:7], s[6:7], 12
	s_add_u32 s6, s50, s6
	s_addc_u32 s7, s51, s7
	s_lshl_b64 s[0:1], s[0:1], 1
	s_add_u32 s6, s6, s0
	s_addc_u32 s7, s7, s1
	s_mov_b64 s[0:1], 0x800
	v_readlane_b32 s53, v254, 8
	v_readlane_b32 s54, v254, 9
	v_readlane_b32 s55, v254, 10
	v_readlane_b32 s56, v254, 11
	v_readlane_b32 s57, v254, 12
	v_readlane_b32 s58, v254, 13
	v_readlane_b32 s59, v254, 14
	v_readlane_b32 s60, v254, 15
	v_readlane_b32 s61, v254, 16
	v_readlane_b32 s62, v254, 17
	v_readlane_b32 s63, v254, 18
	v_readlane_b32 s66, v254, 21
	v_readlane_b32 s67, v254, 22

.LBB0_37:
	v_mul_u32_u24_e32 v36, s6, v82
	v_lshl_add_u64 v[34:35], s[4:5], 0, v[80:81]
	v_lshlrev_b32_e32 v66, 2, v36
	v_mul_u32_u24_e32 v38, s6, v83
	v_lshl_add_u64 v[36:37], v[34:35], 0, v[66:67]
	v_lshlrev_b32_e32 v66, 2, v38
	v_lshl_add_u64 v[38:39], v[34:35], 0, v[66:67]
	global_load_dwordx4 v[62:65], v[36:37], off nt
	global_load_dwordx4 v[50:53], v[38:39], off nt
	v_mul_u32_u24_e32 v36, s6, v84
	v_lshlrev_b32_e32 v66, 2, v36
	v_mul_u32_u24_e32 v38, s6, v85
	v_lshl_add_u64 v[36:37], v[34:35], 0, v[66:67]
	v_lshlrev_b32_e32 v66, 2, v38
	v_lshl_add_u64 v[38:39], v[34:35], 0, v[66:67]
	global_load_dwordx4 v[58:61], v[36:37], off nt
	global_load_dwordx4 v[42:45], v[38:39], off nt
	v_mul_u32_u24_e32 v36, s6, v86
	v_lshlrev_b32_e32 v66, 2, v36
	v_mul_u32_u24_e32 v38, s6, v87
	v_lshl_add_u64 v[36:37], v[34:35], 0, v[66:67]
	v_lshlrev_b32_e32 v66, 2, v38
	v_lshl_add_u64 v[38:39], v[34:35], 0, v[66:67]
	global_load_dwordx4 v[54:57], v[36:37], off nt
	s_nop 0
	global_load_dwordx4 v[38:41], v[38:39], off nt
	v_mul_u32_u24_e32 v36, s6, v88
	v_lshlrev_b32_e32 v66, 2, v36
	v_mul_u32_u24_e32 v46, s6, v89
	v_lshl_add_u64 v[36:37], v[34:35], 0, v[66:67]
	v_lshlrev_b32_e32 v66, 2, v46
	v_lshl_add_u64 v[34:35], v[34:35], 0, v[66:67]
	global_load_dwordx4 v[46:49], v[36:37], off nt
	s_nop 0
	global_load_dwordx4 v[34:37], v[34:35], off nt
	s_add_i32 s21, s2, s1
	s_cmpk_lt_i32 s21, 0x6000
	s_mov_b64 s[4:5], 0
	s_cselect_b64 s[12:13], -1, 0
	s_cmpk_gt_i32 s21, 0x5fff
	s_mov_b64 s[6:7], 0
	s_cbranch_scc1 .LBB0_51
	s_cmpk_gt_i32 s21, 0x47ff
	s_mov_b64 s[16:17], -1
	s_cbranch_scc0 .LBB0_48
	s_and_b32 s4, s21, 0x7c0
	s_add_i32 s6, s20, s18
	s_lshl_b32 s5, s4, 11
	s_and_b32 s6, s6, 0x7e0
	s_or_b32 s17, s5, s6
	s_lshl_b32 s5, s6, 11
	s_add_i32 s22, s21, 0xffffb800
	s_or_b32 s16, s5, s4
	s_cmpk_gt_u32 s22, 0x7ff
	s_mov_b64 s[4:5], -1
	s_cbranch_scc0 .LBB0_45
	s_and_b32 s4, s22, 0xfffff800
	s_cmpk_lg_i32 s4, 0x800
	s_mov_b64 s[4:5], -1
	s_cbranch_scc0 .LBB0_42
	v_readlane_b32 s52, v254, 23
	s_lshl_b32 s4, s17, 2
	v_readlane_b32 s54, v254, 25
	v_readlane_b32 s55, v254, 26
	s_add_u32 s14, s54, s4
	s_addc_u32 s15, s55, 0
	s_lshl_b32 s4, s16, 1
	s_add_u32 s6, s80, s4
	v_readlane_b32 s4, v254, 41
	v_readlane_b32 s53, v254, 24
	v_readlane_b32 s56, v254, 27
	v_readlane_b32 s57, v254, 28
	v_readlane_b32 s58, v254, 29
	v_readlane_b32 s59, v254, 30
	v_readlane_b32 s60, v254, 31
	v_readlane_b32 s61, v254, 32
	v_readlane_b32 s62, v254, 33
	v_readlane_b32 s63, v254, 34
	v_readlane_b32 s64, v254, 35
	v_readlane_b32 s65, v254, 36
	v_readlane_b32 s66, v254, 37
	v_readlane_b32 s67, v254, 38
	s_addc_u32 s7, s4, 0
	s_mov_b64 s[4:5], 0

.LBB0_50:
	v_mov_b32_e32 v79, v67
	v_mul_u32_u24_e32 v2, s16, v82
	v_lshl_add_u64 v[26:27], s[14:15], 0, v[78:79]
	v_lshlrev_b32_e32 v66, 2, v2
	v_mul_u32_u24_e32 v4, s16, v83
	v_lshl_add_u64 v[2:3], v[26:27], 0, v[66:67]
	v_lshlrev_b32_e32 v66, 2, v4
	v_mul_u32_u24_e32 v10, s16, v84
	v_lshl_add_u64 v[6:7], v[26:27], 0, v[66:67]
	v_lshlrev_b32_e32 v66, 2, v10
	v_mul_u32_u24_e32 v12, s16, v85
	v_lshl_add_u64 v[10:11], v[26:27], 0, v[66:67]
	v_lshlrev_b32_e32 v66, 2, v12
	v_mul_u32_u24_e32 v18, s16, v86
	v_lshl_add_u64 v[14:15], v[26:27], 0, v[66:67]
	v_lshlrev_b32_e32 v66, 2, v18
	v_mul_u32_u24_e32 v20, s16, v87
	v_lshl_add_u64 v[18:19], v[26:27], 0, v[66:67]
	v_lshlrev_b32_e32 v66, 2, v20
	v_mul_u32_u24_e32 v28, s16, v88
	v_lshl_add_u64 v[22:23], v[26:27], 0, v[66:67]
	v_lshlrev_b32_e32 v66, 2, v28
	v_mul_u32_u24_e32 v30, s16, v89
	v_lshl_add_u64 v[28:29], v[26:27], 0, v[66:67]
	v_lshlrev_b32_e32 v66, 2, v30
	v_lshl_add_u64 v[30:31], v[26:27], 0, v[66:67]
	global_load_dwordx4 v[2:5], v[2:3], off nt
	s_nop 0
	global_load_dwordx4 v[6:9], v[6:7], off nt
	s_nop 0
	global_load_dwordx4 v[10:13], v[10:11], off nt
	s_nop 0
	global_load_dwordx4 v[14:17], v[14:15], off nt
	s_nop 0
	global_load_dwordx4 v[18:21], v[18:19], off nt
	s_nop 0
	global_load_dwordx4 v[22:25], v[22:23], off nt
	s_nop 0
	global_load_dwordx4 v[26:29], v[28:29], off nt
	s_nop 0
	global_load_dwordx4 v[30:33], v[30:31], off nt

.LBB0_128:
	v_lshl_add_u64 v[66:67], s[96:97], 0, v[94:95]
	v_add_co_u32_e32 v66, vcc, 0x1400000, v66
	s_add_i32 s14, s2, s5
	s_nop 0
	v_addc_co_u32_e32 v67, vcc, 0, v67, vcc
	global_load_dwordx4 v[78:81], v[66:67], off nt
	global_load_dwordx4 v[74:77], v[66:67], off offset:1024 nt
	global_load_dwordx4 v[70:73], v[66:67], off offset:2048 nt
	s_nop 0
	global_load_dwordx4 v[66:69], v[66:67], off offset:3072 nt
	s_cmpk_lt_i32 s14, 0x4800
	s_cselect_b64 s[26:27], -1, 0
	s_cmpk_gt_i32 s14, 0x47ff
	s_cbranch_scc1 .LBB0_130
	v_lshl_add_u64 v[2:3], s[96:97], 0, v[90:91]
	v_add_co_u32_e32 v22, vcc, 0x1400000, v2
	s_nop 1
	v_addc_co_u32_e32 v23, vcc, 0, v3, vcc
	global_load_dwordx4 v[2:5], v[22:23], off nt
	global_load_dwordx4 v[6:9], v[22:23], off offset:1024 nt
	global_load_dwordx4 v[14:17], v[22:23], off offset:2048 nt
	s_nop 0
	global_load_dwordx4 v[22:25], v[22:23], off offset:3072 nt
.LBB0_130:
	s_add_i32 s22, s2, s35
	s_add_i32 s14, s3, s14
	s_cmpk_lt_i32 s14, 0x4800
	s_cselect_b64 s[24:25], -1, 0
	s_cmpk_gt_i32 s14, 0x47ff
	s_cbranch_scc1 .LBB0_132
	s_ashr_i32 s23, s22, 31
	s_lshl_b64 s[16:17], s[22:23], 12
	v_lshl_add_u64 v[34:35], v[84:85], 0, s[16:17]
	global_load_dwordx4 v[10:13], v[34:35], off nt
	global_load_dwordx4 v[18:21], v[34:35], off offset:1024 nt
	global_load_dwordx4 v[26:29], v[34:35], off offset:2048 nt
	s_nop 0
	global_load_dwordx4 v[34:37], v[34:35], off offset:3072 nt
.LBB0_132:
	s_add_i32 s18, s2, s36
	s_add_i32 s15, s3, s14
	s_cmpk_lt_i32 s15, 0x4800
	s_cselect_b64 s[20:21], -1, 0
	s_cmpk_gt_i32 s15, 0x47ff
	s_cbranch_scc1 .LBB0_134
	s_ashr_i32 s19, s18, 31
	s_lshl_b64 s[16:17], s[18:19], 12
	v_lshl_add_u64 v[50:51], v[84:85], 0, s[16:17]
	global_load_dwordx4 v[30:33], v[50:51], off nt
	global_load_dwordx4 v[38:41], v[50:51], off offset:1024 nt
	global_load_dwordx4 v[42:45], v[50:51], off offset:2048 nt
	s_nop 0
	global_load_dwordx4 v[50:53], v[50:51], off offset:3072 nt
.LBB0_134:
	s_add_i32 s14, s2, s37
	s_add_i32 s45, s3, s15
	s_cmpk_lt_i32 s45, 0x4800
	s_cselect_b64 s[16:17], -1, 0
	s_cmpk_gt_i32 s45, 0x47ff
	s_cbranch_scc1 .LBB0_136
	s_ashr_i32 s15, s14, 31
	s_lshl_b64 s[30:31], s[14:15], 12
	v_lshl_add_u64 v[62:63], v[84:85], 0, s[30:31]
	global_load_dwordx4 v[46:49], v[62:63], off nt
	global_load_dwordx4 v[54:57], v[62:63], off offset:1024 nt
	global_load_dwordx4 v[58:61], v[62:63], off offset:2048 nt
	s_nop 0
	global_load_dwordx4 v[62:65], v[62:63], off offset:3072 nt

.LBB0_162:
	v_lshl_add_u64 v[66:67], s[18:19], 0, v[132:133]
	global_load_dwordx4 v[126:129], v[66:67], off nt
	global_load_dwordx4 v[122:125], v[66:67], off offset:1024 nt
	global_load_dwordx4 v[118:121], v[66:67], off offset:2048 nt
	global_load_dwordx4 v[110:113], v[66:67], off offset:3072 nt
	v_lshl_add_u64 v[68:69], s[6:7], 0, v[132:133]
	global_load_dwordx4 v[94:97], v[68:69], off nt
	global_load_dwordx4 v[82:85], v[68:69], off offset:1024 nt
	v_add_co_u32_e32 v66, vcc, 0x1000, v66
	s_movk_i32 s20, 0x1000
	s_nop 0
	v_addc_co_u32_e32 v67, vcc, 0, v67, vcc
	global_load_dwordx4 v[114:117], v[66:67], off nt
	global_load_dwordx4 v[106:109], v[66:67], off offset:1024 nt
	global_load_dwordx4 v[98:101], v[66:67], off offset:3072 nt
	global_load_dwordx4 v[102:105], v[66:67], off offset:2048 nt
	global_load_dwordx4 v[86:89], v[68:69], off offset:2048 nt
	v_add_co_u32_e32 v66, vcc, s20, v68
	s_mov_b32 s20, 0x3a000000
	s_nop 0
	v_addc_co_u32_e32 v67, vcc, 0, v69, vcc
	global_load_dwordx4 v[78:81], v[66:67], off nt
	global_load_dwordx4 v[90:93], v[68:69], off offset:3072 nt
	global_load_dwordx4 v[74:77], v[66:67], off offset:1024 nt
	global_load_dwordx4 v[70:73], v[66:67], off offset:2048 nt
	s_nop 0
	global_load_dwordx4 v[66:69], v[66:67], off offset:3072 nt
	s_waitcnt vmcnt(15)
	v_mov_b32_e32 v152, v127
	s_waitcnt vmcnt(14)
	v_mov_b32_e32 v153, v123
	v_mov_b32_e32 v164, v129
	v_mov_b32_e32 v165, v125
	v_mov_b32_e32 v150, v126
	v_mov_b32_e32 v151, v122
	v_mov_b32_e32 v162, v128
	v_mov_b32_e32 v163, v124
	s_waitcnt vmcnt(13)
	v_pk_mul_f32 v[166:167], v[120:121], v[120:121]
	v_pk_mul_f32 v[168:169], v[118:119], v[118:119]
	v_pk_mul_f32 v[152:153], v[152:153], v[152:153]
	v_pk_mul_f32 v[164:165], v[164:165], v[164:165]
	v_pk_mov_b32 v[178:179], v[168:169], v[166:167] op_sel:[1,0]
	v_mov_b32_e32 v169, v167
	v_pk_fma_f32 v[150:151], v[150:151], v[150:151], v[152:153]
	v_pk_fma_f32 v[152:153], v[162:163], v[162:163], v[164:165]
	s_waitcnt vmcnt(12)
	v_mul_f32_e32 v134, v111, v111
	v_mul_f32_e32 v170, v113, v113
	v_pk_add_f32 v[162:163], v[178:179], v[168:169]
	v_pk_add_f32 v[150:151], v[150:151], v[152:153]
	v_pk_fma_f32 v[166:167], v[110:111], v[110:111], v[134:135] op_sel_hi:[1,1,0]
	v_pk_fma_f32 v[170:171], v[112:113], v[112:113], v[170:171] op_sel_hi:[1,1,0]
	s_waitcnt vmcnt(9)
	v_mul_f32_e32 v161, v114, v114
	v_mul_f32_e32 v178, v115, v115
	v_pk_add_f32 v[162:163], v[162:163], v[162:163] op_sel:[0,1] op_sel_hi:[1,0]
	v_pk_add_f32 v[150:151], v[150:151], v[150:151] op_sel:[0,1] op_sel_hi:[1,0]
	v_mov_b32_e32 v174, v95
	v_mov_b32_e32 v175, v83
	v_mul_f32_e32 v167, v116, v116
	v_mul_f32_e32 v171, v117, v117
	s_waitcnt vmcnt(8)
	v_pk_mul_f32 v[164:165], v[108:109], v[108:109]
	v_pk_mul_f32 v[168:169], v[106:107], v[106:107]
	v_mov_b32_e32 v163, v178
	v_mov_b32_e32 v151, v161
	v_mov_b32_e32 v172, v94
	v_mov_b32_e32 v173, v82
	v_pk_mul_f32 v[174:175], v[174:175], v[174:175]
	v_pk_mov_b32 v[152:153], v[168:169], v[164:165] op_sel:[1,0]
	v_mov_b32_e32 v169, v165
	v_pk_add_f32 v[166:167], v[166:167], v[170:171]
	v_pk_add_f32 v[150:151], v[150:151], v[162:163]
	v_pk_fma_f32 v[172:173], v[172:173], v[172:173], v[174:175]
	s_waitcnt vmcnt(6)
	v_mul_f32_e32 v134, v103, v103
	v_mul_f32_e32 v174, v105, v105
	v_pk_add_f32 v[152:153], v[152:153], v[168:169]
	v_pk_add_f32 v[150:151], v[150:151], v[166:167]
	v_mul_f32_e32 v179, v98, v98
	v_mul_f32_e32 v180, v99, v99
	v_mul_f32_e32 v181, v100, v100
	v_mul_f32_e32 v182, v101, v101
	v_pk_fma_f32 v[164:165], v[102:103], v[102:103], v[134:135] op_sel_hi:[1,1,0]
	v_pk_fma_f32 v[174:175], v[104:105], v[104:105], v[174:175] op_sel_hi:[1,1,0]
	v_pk_add_f32 v[152:153], v[152:153], v[152:153] op_sel:[0,1] op_sel_hi:[1,0]
	v_pk_add_f32 v[150:151], v[150:151], v[150:151] op_sel:[0,1] op_sel_hi:[1,0]
	v_mov_b32_e32 v165, v181
	v_mov_b32_e32 v175, v182
	v_mov_b32_e32 v153, v180
	v_mov_b32_e32 v151, v179
	v_pk_add_f32 v[164:165], v[164:165], v[174:175]
	v_pk_add_f32 v[150:151], v[150:151], v[152:153]
	v_mov_b32_e32 v152, v97
	v_mov_b32_e32 v153, v85
	v_mov_b32_e32 v176, v96
	v_mov_b32_e32 v177, v84
	v_pk_add_f32 v[150:151], v[150:151], v[164:165]
	v_pk_mul_f32 v[152:153], v[152:153], v[152:153]
	s_waitcnt vmcnt(5)
	v_pk_mul_f32 v[162:163], v[88:89], v[88:89]
	v_pk_mul_f32 v[164:165], v[86:87], v[86:87]
	v_pk_fma_f32 v[152:153], v[176:177], v[176:177], v[152:153]
	v_pk_mov_b32 v[166:167], v[164:165], v[162:163] op_sel:[1,0]
	v_mov_b32_e32 v165, v163
	v_pk_add_f32 v[152:153], v[172:173], v[152:153]
	v_pk_add_f32 v[162:163], v[166:167], v[164:165]
	s_waitcnt vmcnt(4)
	v_mul_f32_e32 v134, v78, v78
	v_mul_f32_e32 v161, v79, v79
	v_pk_add_f32 v[152:153], v[152:153], v[152:153] op_sel:[0,1] op_sel_hi:[1,0]
	v_pk_add_f32 v[162:163], v[162:163], v[162:163] op_sel:[0,1] op_sel_hi:[1,0]
	v_mov_b32_e32 v153, v134
	v_mov_b32_e32 v163, v161
	s_waitcnt vmcnt(3)
	v_mul_f32_e32 v134, v91, v91
	v_mul_f32_e32 v164, v80, v80
	v_pk_add_f32 v[152:153], v[152:153], v[162:163]
	v_pk_fma_f32 v[162:163], v[90:91], v[90:91], v[134:135] op_sel_hi:[1,1,0]
	v_mul_f32_e32 v134, v93, v93
	v_mul_f32_e32 v166, v81, v81
	v_mov_b32_e32 v163, v164
	v_pk_fma_f32 v[164:165], v[92:93], v[92:93], v[134:135] op_sel_hi:[1,1,0]
	s_waitcnt vmcnt(0)
	v_mul_f32_e32 v134, v66, v66
	v_mov_b32_e32 v165, v166
	v_pk_add_f32 v[162:163], v[162:163], v[164:165]
	v_pk_mul_f32 v[164:165], v[74:75], v[74:75]
	v_pk_add_f32 v[152:153], v[152:153], v[162:163]
	v_pk_mul_f32 v[162:163], v[76:77], v[76:77]
	v_mul_f32_e32 v161, v67, v67
	v_pk_mov_b32 v[166:167], v[164:165], v[162:163] op_sel:[1,0]
	v_mov_b32_e32 v165, v163
	v_pk_add_f32 v[162:163], v[166:167], v[164:165]
	v_pk_add_f32 v[152:153], v[152:153], v[152:153] op_sel:[0,1] op_sel_hi:[1,0]
	v_pk_add_f32 v[162:163], v[162:163], v[162:163] op_sel:[0,1] op_sel_hi:[1,0]
	v_mov_b32_e32 v153, v134
	v_mov_b32_e32 v163, v161
	v_mul_f32_e32 v134, v71, v71
	v_mul_f32_e32 v164, v68, v68
	v_pk_add_f32 v[152:153], v[152:153], v[162:163]
	v_pk_fma_f32 v[162:163], v[70:71], v[70:71], v[134:135] op_sel_hi:[1,1,0]
	v_mul_f32_e32 v134, v73, v73
	v_mul_f32_e32 v166, v69, v69
	v_mov_b32_e32 v163, v164
	v_pk_fma_f32 v[164:165], v[72:73], v[72:73], v[134:135] op_sel_hi:[1,1,0]
	s_nop 0
	v_mov_b32_e32 v165, v166
	v_pk_add_f32 v[162:163], v[162:163], v[164:165]
	s_nop 0
	v_pk_add_f32 v[152:153], v[152:153], v[162:163]
	v_mov_b32_e32 v163, v150
	v_mov_b32_e32 v162, v152
	v_mov_b32_e32 v150, v153
	v_pk_add_f32 v[150:151], v[162:163], v[150:151]
	ds_bpermute_b32 v153, v131, v151
	ds_bpermute_b32 v152, v131, v150
	s_waitcnt lgkmcnt(0)
	v_pk_add_f32 v[150:151], v[150:151], v[152:153]
	ds_bpermute_b32 v153, v143, v151
	ds_bpermute_b32 v152, v143, v150
	s_waitcnt lgkmcnt(0)
	v_pk_add_f32 v[150:151], v[150:151], v[152:153]
	ds_bpermute_b32 v153, v145, v151
	ds_bpermute_b32 v152, v145, v150
	s_waitcnt lgkmcnt(0)
	v_pk_add_f32 v[150:151], v[150:151], v[152:153]
	ds_bpermute_b32 v153, v154, v151
	ds_bpermute_b32 v152, v154, v150
	s_waitcnt lgkmcnt(0)
	v_pk_add_f32 v[150:151], v[150:151], v[152:153]
	ds_bpermute_b32 v153, v155, v151
	ds_bpermute_b32 v152, v155, v150
	s_waitcnt lgkmcnt(0)
	v_pk_add_f32 v[150:151], v[150:151], v[152:153]
	ds_bpermute_b32 v153, v156, v151
	ds_bpermute_b32 v152, v156, v150
	s_waitcnt lgkmcnt(0)
	v_pk_add_f32 v[150:151], v[150:151], v[152:153]
	s_nop 0
	v_pk_fma_f32 v[162:163], v[150:151], s[20:21], v[144:145] op_sel_hi:[1,0,0]
	s_nop 0
	v_mul_f32_e32 v134, 0x4b800000, v163
	v_cmp_gt_f32_e32 vcc, s3, v163
	s_nop 1
	v_cndmask_b32_e32 v134, v163, v134, vcc
	v_rsq_f32_e32 v134, v134
	s_nop 0
	v_mul_f32_e32 v150, 0x45800000, v134
	v_cndmask_b32_e32 v134, v134, v150, vcc
	v_pk_mul_f32 v[126:127], v[126:127], v[134:135] op_sel_hi:[1,0]
	v_pk_mul_f32 v[128:129], v[128:129], v[134:135] op_sel_hi:[1,0]
	v_pk_fma_f32 v[152:153], v[2:3], v[126:127], v[10:11]
	v_pk_fma_f32 v[150:151], v[4:5], v[128:129], v[12:13]
	v_max_f32_e64 v126, |v152|, |v153|
	v_max_f32_e64 v127, |v150|, |v151|
	v_pk_mul_f32 v[122:123], v[122:123], v[134:135] op_sel_hi:[1,0]
	v_pk_mul_f32 v[124:125], v[124:125], v[134:135] op_sel_hi:[1,0]
	v_max3_f32 v161, v126, 0, v127
	v_pk_fma_f32 v[126:127], v[8:9], v[124:125], v[16:17]
	v_pk_fma_f32 v[128:129], v[6:7], v[122:123], v[14:15]
	v_max_f32_e64 v123, |v126|, |v127|
	v_max_f32_e64 v122, |v128|, |v129|
	v_pk_mul_f32 v[118:119], v[118:119], v[134:135] op_sel_hi:[1,0]
	v_pk_mul_f32 v[120:121], v[120:121], v[134:135] op_sel_hi:[1,0]
	v_max3_f32 v161, v161, v122, v123
	v_pk_fma_f32 v[122:123], v[20:21], v[120:121], v[28:29]
	v_pk_fma_f32 v[124:125], v[18:19], v[118:119], v[26:27]
	v_max_f32_e64 v119, |v122|, |v123|
	v_max_f32_e64 v118, |v124|, |v125|
	v_pk_mul_f32 v[110:111], v[110:111], v[134:135] op_sel_hi:[1,0]
	v_pk_mul_f32 v[112:113], v[112:113], v[134:135] op_sel_hi:[1,0]
	v_max3_f32 v161, v161, v118, v119
	v_pk_fma_f32 v[118:119], v[24:25], v[112:113], v[32:33]
	v_pk_fma_f32 v[120:121], v[22:23], v[110:111], v[30:31]
	v_max_f32_e64 v111, |v118|, |v119|
	v_max_f32_e64 v110, |v120|, |v121|
	v_max3_f32 v161, v161, v110, v111
	v_pk_mul_f32 v[110:111], v[114:115], v[134:135] op_sel_hi:[1,0]
	v_pk_mul_f32 v[112:113], v[116:117], v[134:135] op_sel_hi:[1,0]
	v_pk_fma_f32 v[116:117], v[34:35], v[110:111], v[42:43]
	v_pk_fma_f32 v[114:115], v[36:37], v[112:113], v[44:45]
	v_max_f32_e64 v110, |v116|, |v117|
	v_max_f32_e64 v111, |v114|, |v115|
	v_pk_mul_f32 v[106:107], v[106:107], v[134:135] op_sel_hi:[1,0]
	v_pk_mul_f32 v[108:109], v[108:109], v[134:135] op_sel_hi:[1,0]
	v_max3_f32 v161, v161, v110, v111
	v_pk_fma_f32 v[110:111], v[40:41], v[108:109], v[48:49]
	v_pk_fma_f32 v[112:113], v[38:39], v[106:107], v[46:47]
	v_max_f32_e64 v107, |v110|, |v111|
	v_max_f32_e64 v106, |v112|, |v113|
	v_pk_mul_f32 v[104:105], v[104:105], v[134:135] op_sel_hi:[1,0]
	v_pk_mul_f32 v[98:99], v[98:99], v[134:135] op_sel_hi:[1,0]
	v_max3_f32 v161, v161, v106, v107
	v_pk_fma_f32 v[106:107], v[104:105], v[52:53], v[60:61]
	v_pk_fma_f32 v[104:105], v[98:99], v[54:55], v[62:63]
	v_mul_f32_e32 v98, 0x4b800000, v162
	v_cmp_gt_f32_e32 vcc, s3, v162
	v_pk_mul_f32 v[102:103], v[102:103], v[134:135] op_sel_hi:[1,0]
	v_pk_mul_f32 v[100:101], v[100:101], v[134:135] op_sel_hi:[1,0]
	v_cndmask_b32_e32 v98, v162, v98, vcc
	v_pk_fma_f32 v[108:109], v[102:103], v[50:51], v[58:59]
	v_rsq_f32_e32 v98, v98
	v_max_f32_e64 v102, |v108|, |v109|
	v_max_f32_e64 v103, |v106|, |v107|
	v_max3_f32 v161, v161, v102, v103
	v_pk_fma_f32 v[102:103], v[100:101], v[56:57], v[64:65]
	v_max_f32_e64 v99, |v104|, |v105|
	v_max_f32_e64 v100, |v102|, |v103|
	v_max3_f32 v161, v161, v99, v100
	v_mul_f32_e32 v99, 0x45800000, v98
	v_cndmask_b32_e32 v134, v98, v99, vcc
	v_pk_mul_f32 v[94:95], v[94:95], v[134:135] op_sel_hi:[1,0]
	v_pk_mul_f32 v[96:97], v[96:97], v[134:135] op_sel_hi:[1,0]
	v_pk_fma_f32 v[100:101], v[2:3], v[94:95], v[10:11]
	v_pk_fma_f32 v[98:99], v[4:5], v[96:97], v[12:13]
	v_max_f32_e64 v94, |v100|, |v101|
	v_max_f32_e64 v95, |v98|, |v99|
	v_pk_mul_f32 v[82:83], v[82:83], v[134:135] op_sel_hi:[1,0]
	v_pk_mul_f32 v[84:85], v[84:85], v[134:135] op_sel_hi:[1,0]
	v_max3_f32 v162, v94, 0, v95
	v_pk_fma_f32 v[94:95], v[8:9], v[84:85], v[16:17]
	v_pk_fma_f32 v[96:97], v[6:7], v[82:83], v[14:15]
	v_max_f32_e64 v83, |v94|, |v95|
	v_max_f32_e64 v82, |v96|, |v97|
	v_max3_f32 v162, v162, v82, v83
	v_pk_mul_f32 v[82:83], v[86:87], v[134:135] op_sel_hi:[1,0]
	v_pk_mul_f32 v[84:85], v[88:89], v[134:135] op_sel_hi:[1,0]
	v_pk_fma_f32 v[88:89], v[18:19], v[82:83], v[26:27]
	v_pk_fma_f32 v[86:87], v[20:21], v[84:85], v[28:29]
	v_max_f32_e64 v82, |v88|, |v89|
	v_max_f32_e64 v83, |v86|, |v87|
	v_max3_f32 v162, v162, v82, v83
	v_pk_mul_f32 v[84:85], v[90:91], v[134:135] op_sel_hi:[1,0]
	v_pk_mul_f32 v[82:83], v[92:93], v[134:135] op_sel_hi:[1,0]
	v_pk_fma_f32 v[84:85], v[22:23], v[84:85], v[30:31]
	v_pk_fma_f32 v[82:83], v[24:25], v[82:83], v[32:33]
	v_max_f32_e64 v90, |v84|, |v85|
	v_max_f32_e64 v91, |v82|, |v83|
	v_max3_f32 v92, v162, v90, v91
	v_pk_mul_f32 v[90:91], v[78:79], v[134:135] op_sel_hi:[1,0]
	v_pk_mul_f32 v[78:79], v[80:81], v[134:135] op_sel_hi:[1,0]
	v_pk_fma_f32 v[80:81], v[34:35], v[90:91], v[42:43]
	v_pk_fma_f32 v[78:79], v[36:37], v[78:79], v[44:45]
	v_max_f32_e64 v90, |v80|, |v81|
	v_max_f32_e64 v91, |v78|, |v79|
	v_max3_f32 v92, v92, v90, v91
	v_pk_mul_f32 v[90:91], v[74:75], v[134:135] op_sel_hi:[1,0]
	v_pk_mul_f32 v[74:75], v[76:77], v[134:135] op_sel_hi:[1,0]
	v_pk_fma_f32 v[76:77], v[38:39], v[90:91], v[46:47]
	v_pk_fma_f32 v[74:75], v[40:41], v[74:75], v[48:49]
	v_max_f32_e64 v90, |v76|, |v77|
	v_max_f32_e64 v91, |v74|, |v75|
	v_max3_f32 v92, v92, v90, v91
	v_pk_mul_f32 v[90:91], v[70:71], v[134:135] op_sel_hi:[1,0]
	v_pk_mul_f32 v[70:71], v[72:73], v[134:135] op_sel_hi:[1,0]
	v_pk_fma_f32 v[72:73], v[90:91], v[50:51], v[58:59]
	v_pk_fma_f32 v[70:71], v[70:71], v[52:53], v[60:61]
	v_max_f32_e64 v90, |v72|, |v73|
	v_max_f32_e64 v91, |v70|, |v71|
	v_max3_f32 v92, v92, v90, v91
	v_pk_mul_f32 v[90:91], v[66:67], v[134:135] op_sel_hi:[1,0]
	v_pk_mul_f32 v[66:67], v[68:69], v[134:135] op_sel_hi:[1,0]
	v_pk_fma_f32 v[68:69], v[90:91], v[54:55], v[62:63]
	v_pk_fma_f32 v[66:67], v[66:67], v[56:57], v[64:65]
	v_max_f32_e64 v90, |v68|, |v69|
	v_max_f32_e64 v91, |v66|, |v67|
	ds_bpermute_b32 v93, v131, v161
	v_max3_f32 v90, v92, v90, v91
	ds_bpermute_b32 v91, v131, v90
	s_waitcnt lgkmcnt(1)
	v_max_f32_e32 v92, v93, v93
	v_max_f32_e32 v92, v161, v92
	s_waitcnt lgkmcnt(0)
	v_max_f32_e32 v91, v91, v91
	ds_bpermute_b32 v93, v143, v92
	v_max_f32_e32 v90, v90, v91
	ds_bpermute_b32 v91, v143, v90
	s_waitcnt lgkmcnt(1)
	v_max_f32_e32 v93, v93, v93
	v_max_f32_e32 v92, v92, v93
	s_waitcnt lgkmcnt(0)
	v_max_f32_e32 v91, v91, v91
	ds_bpermute_b32 v93, v145, v92
	v_max_f32_e32 v90, v90, v91
	ds_bpermute_b32 v91, v145, v90
	s_waitcnt lgkmcnt(1)
	v_max_f32_e32 v93, v93, v93
	v_max_f32_e32 v92, v92, v93
	s_waitcnt lgkmcnt(0)
	v_max_f32_e32 v91, v91, v91
	ds_bpermute_b32 v93, v154, v92
	v_max_f32_e32 v90, v90, v91
	ds_bpermute_b32 v91, v154, v90
	s_waitcnt lgkmcnt(1)
	v_max_f32_e32 v93, v93, v93
	v_max_f32_e32 v92, v92, v93
	s_waitcnt lgkmcnt(0)
	v_max_f32_e32 v91, v91, v91
	ds_bpermute_b32 v93, v155, v92
	v_max_f32_e32 v90, v90, v91
	ds_bpermute_b32 v91, v155, v90
	s_waitcnt lgkmcnt(1)
	v_max_f32_e32 v93, v93, v93
	v_max_f32_e32 v93, v92, v93
	s_waitcnt lgkmcnt(0)
	v_max_f32_e32 v91, v91, v91
	ds_bpermute_b32 v134, v156, v93
	v_max_f32_e32 v90, v90, v91
	ds_bpermute_b32 v92, v156, v90
	s_waitcnt lgkmcnt(1)
	v_max_f32_e32 v91, v134, v134
	v_max_f32_e32 v91, v93, v91
	s_and_saveexec_b64 s[20:21], s[0:1]
	s_cbranch_execz .LBB0_164
	s_add_u32 s26, s96, s15
	s_addc_u32 s27, s97, s24
	v_mul_f32_e32 v93, 0x3c010204, v91
	global_store_dword v135, v93, s[26:27]

.LBB0_648:
	s_or_b64 exec, exec, s[26:27]
	v_mov_b32_e32 v2, s3
	s_waitcnt lgkmcnt(0)
	s_barrier
	ds_read_b32 v2, v2
	s_mov_b64 s[26:27], -1
	s_waitcnt lgkmcnt(0)
	v_cmp_gt_i32_e32 vcc, s2, v2
	v_readfirstlane_b32 s40, v2
	s_cbranch_vccz .LBB0_643
	s_ashr_i32 s26, s40, 4
	s_lshl_b32 s27, s40, 7
	s_and_b32 s30, s27, 0x780
	s_ashr_i32 s27, s26, 31
	s_lshl_b64 s[38:39], s[26:27], 11
	s_mul_i32 s50, s26, 0x4800000
	v_readlane_b32 s28, v255, 4
	s_mul_hi_i32 s41, s26, 0x4800000
	v_readlane_b32 s29, v255, 5
	s_add_u32 s28, s28, s50
	v_or_b32_e32 v2, s30, v124
	s_addc_u32 s29, s29, s41
	s_lshl_b32 s49, s30, 1
	v_lshlrev_b32_e32 v2, 2, v2
	s_add_u32 s28, s28, s49
	global_load_dword v169, v2, s[84:85]
	s_addc_u32 s29, s29, 0
	v_mov_b32_e32 v2, v126
	v_mov_b32_e32 v108, v125
	v_mov_b32_e32 v3, v127
	v_mov_b32_e32 v10, v126
	v_lshl_add_u64 v[4:5], s[28:29], 0, v[108:109]
	v_add_co_u32_e32 v4, vcc, s42, v4
	v_mov_b32_e32 v3, v109
	s_nop 0
	v_addc_co_u32_e32 v5, vcc, 0, v5, vcc
	v_lshl_add_u64 v[2:3], s[28:29], 0, v[2:3]
	v_add_co_u32_e32 v6, vcc, s42, v2
	v_mov_b32_e32 v108, v125
	s_nop 0
	v_addc_co_u32_e32 v7, vcc, 0, v3, vcc
	v_mov_b32_e32 v11, v127
	global_load_dwordx4 v[2:5], v[4:5], off nt
	s_nop 0
	global_load_dwordx4 v[6:9], v[6:7], off nt
	v_mov_b32_e32 v18, v126
	v_lshl_add_u64 v[12:13], s[28:29], 0, v[108:109]
	v_add_co_u32_e32 v12, vcc, s43, v12
	v_mov_b32_e32 v11, v109
	s_nop 0
	v_addc_co_u32_e32 v13, vcc, 0, v13, vcc
	v_lshl_add_u64 v[10:11], s[28:29], 0, v[10:11]
	v_add_co_u32_e32 v14, vcc, s43, v10
	v_mov_b32_e32 v108, v125
	s_nop 0
	v_addc_co_u32_e32 v15, vcc, 0, v11, vcc
	v_mov_b32_e32 v19, v127
	global_load_dwordx4 v[10:13], v[12:13], off nt
	s_nop 0
	global_load_dwordx4 v[14:17], v[14:15], off nt
	v_mov_b32_e32 v26, v126
	v_lshl_add_u64 v[20:21], s[28:29], 0, v[108:109]
	v_add_co_u32_e32 v20, vcc, s44, v20
	v_mov_b32_e32 v19, v109
	s_nop 0
	v_addc_co_u32_e32 v21, vcc, 0, v21, vcc
	v_lshl_add_u64 v[18:19], s[28:29], 0, v[18:19]
	v_add_co_u32_e32 v22, vcc, s44, v18
	v_mov_b32_e32 v27, v125
	s_nop 0
	v_addc_co_u32_e32 v23, vcc, 0, v19, vcc
	v_mov_b32_e32 v28, v127
	global_load_dwordx4 v[18:21], v[20:21], off nt
	s_nop 0
	global_load_dwordx4 v[22:25], v[22:23], off nt
	global_load_dwordx4 v[38:41], v28, s[28:29] offset:16 nt
	global_load_dwordx4 v[46:49], v28, s[28:29] nt
	s_and_b32 s28, s40, 15
	s_lshl_b32 s28, s28, 8
	s_or_b32 s28, s50, s28
	s_add_u32 s50, s96, s28
	s_addc_u32 s51, s97, s41
	s_lshl_b64 s[26:27], s[26:27], 22
	s_or_b32 s26, s26, s30
	v_mov_b32_e32 v26, 0
	s_mov_b32 s49, 0
	v_lshl_add_u64 v[116:117], v[112:113], 0, s[30:31]
	v_mov_b32_e32 v119, s39
	v_or_b32_e32 v118, s38, v106
	v_lshl_add_u64 v[120:121], v[114:115], 0, s[26:27]
	v_mov_b64_e32 v[78:79], 0
	s_mov_b64 s[38:39], 0
	v_mov_b32_e32 v74, 0
	v_mov_b32_e32 v75, 0
	v_mov_b32_e32 v76, 0
	v_mov_b32_e32 v77, 0
	v_mov_b32_e32 v27, v26
	v_mov_b32_e32 v28, v26
	v_mov_b32_e32 v29, v26
	v_mov_b32_e32 v30, v26
	v_mov_b32_e32 v31, v26
	v_mov_b32_e32 v32, v26
	s_waitcnt vmcnt(8)
	v_sub_f32_e32 v170, 1.0, v169
	v_mov_b32_e32 v33, v26
	v_mov_b32_e32 v62, v26
	v_mov_b32_e32 v63, v26
	v_mov_b32_e32 v64, v26
	v_mov_b32_e32 v65, v26
	v_mov_b32_e32 v54, v26
	v_mov_b32_e32 v55, v26
	v_mov_b32_e32 v56, v26
	v_mov_b32_e32 v57, v26
	v_mov_b32_e32 v34, v26
	v_mov_b32_e32 v35, v26
	v_mov_b32_e32 v36, v26
	v_mov_b32_e32 v37, v26
	v_mov_b32_e32 v50, v26
	v_mov_b32_e32 v51, v26
	v_mov_b32_e32 v52, v26
	v_mov_b32_e32 v53, v26
	v_mov_b32_e32 v42, v26
	v_mov_b32_e32 v43, v26
	v_mov_b32_e32 v44, v26
	v_mov_b32_e32 v45, v26
	v_mov_b32_e32 v58, v26
	v_mov_b32_e32 v59, v26
	v_mov_b32_e32 v60, v26
	v_mov_b32_e32 v61, v26

.LBB0_652:
	s_waitcnt lgkmcnt(0)
	s_barrier
	s_cmp_lg_u32 s38, 0x45c0000
	s_cselect_b64 s[40:41], -1, 0
	s_cmp_eq_u32 s38, 0x45c0000
	s_cbranch_scc1 .LBB0_654
	s_add_u32 s26, s50, s38
	v_mov_b32_e32 v2, v126
	v_mov_b32_e32 v108, v125
	v_mov_b32_e32 v3, v127
	s_addc_u32 s27, s51, s39
	s_nop 0
	v_lshl_add_u64 v[4:5], s[26:27], 0, v[108:109]
	v_add_co_u32_e32 v4, vcc, 0x26244000, v4
	v_mov_b32_e32 v3, v109
	s_nop 0
	v_addc_co_u32_e32 v5, vcc, 0, v5, vcc
	v_lshl_add_u64 v[2:3], s[26:27], 0, v[2:3]
	v_add_co_u32_e32 v6, vcc, 0x26244000, v2
	s_nop 1
	v_addc_co_u32_e32 v7, vcc, 0, v3, vcc
	global_load_dwordx4 v[2:5], v[4:5], off nt
	s_nop 0
	global_load_dwordx4 v[6:9], v[6:7], off nt
.LBB0_654:
	ds_read_u16 v66, v149
	ds_read_u16 v67, v149 offset:256
	ds_read_u16 v69, v149 offset:512
	ds_read_u16 v71, v149 offset:768
	ds_read_u16 v72, v149 offset:1024
	ds_read_u16 v74, v149 offset:1280
	ds_read_u16 v75, v149 offset:1536
	ds_read_u16 v76, v149 offset:1792
	s_waitcnt lgkmcnt(7)
	v_lshlrev_b32_e32 v66, 16, v66
	v_mul_f32_e32 v66, 0xbfb8aa3b, v66
	v_exp_f32_e32 v66, v66
	s_waitcnt lgkmcnt(6)
	v_lshlrev_b32_e32 v67, 16, v67
	v_mul_f32_e32 v68, 0xbfb8aa3b, v67
	v_exp_f32_e32 v68, v68
	v_add_f32_e32 v66, 1.0, v66
	v_rcp_f32_e32 v66, v66
	s_waitcnt lgkmcnt(5)
	v_lshlrev_b32_e32 v69, 16, v69
	v_add_f32_e32 v68, 1.0, v68
	v_rcp_f32_e32 v68, v68
	v_fma_f32 v67, v170, v66, v169
	v_cmp_gt_f32_e32 vcc, s45, v67
	v_mul_f32_e32 v69, 0xbfb8aa3b, v69
	v_fma_f32 v68, v170, v68, v169
	v_cndmask_b32_e64 v66, 0, 32, vcc
	v_ldexp_f32 v66, v67, v66
	v_log_f32_e32 v66, v66
	v_exp_f32_e32 v69, v69
	s_waitcnt lgkmcnt(4)
	v_lshlrev_b32_e32 v71, 16, v71
	v_mul_f32_e32 v71, 0xbfb8aa3b, v71
	v_mul_f32_e32 v70, 0x3f317217, v66
	v_fma_f32 v70, v66, s46, -v70
	v_fmac_f32_e32 v70, 0x3377d1cf, v66
	v_fmac_f32_e32 v70, 0x3f317217, v66
	v_cmp_lt_f32_e64 s[26:27], |v66|, s47
	v_add_f32_e32 v69, 1.0, v69
	v_rcp_f32_e32 v69, v69
	v_cndmask_b32_e64 v66, v66, v70, s[26:27]
	v_cndmask_b32_e32 v70, 0, v163, vcc
	v_sub_f32_e32 v66, v66, v70
	v_cmp_gt_f32_e32 vcc, s45, v68
	v_add_f32_e32 v104, 0, v66
	v_exp_f32_e32 v71, v71
	v_cndmask_b32_e64 v66, 0, 32, vcc
	v_ldexp_f32 v66, v68, v66
	v_log_f32_e32 v66, v66
	v_cndmask_b32_e32 v73, 0, v163, vcc
	ds_read_u16 v92, v150
	ds_read_u16 v89, v150 offset:256
	ds_read_u16 v88, v150 offset:512
	ds_read_u16 v85, v150 offset:768
	ds_read_u16 v83, v150 offset:1024
	ds_read_u16 v82, v150 offset:1280
	ds_read_u16 v80, v150 offset:1536
	ds_read_u16 v77, v150 offset:1792
	v_mul_f32_e32 v70, 0x3f317217, v66
	v_fma_f32 v70, v66, s46, -v70
	v_fmac_f32_e32 v70, 0x3377d1cf, v66
	v_fmac_f32_e32 v70, 0x3f317217, v66
	v_cmp_lt_f32_e64 s[26:27], |v66|, s47
	s_nop 1
	v_cndmask_b32_e64 v66, v66, v70, s[26:27]
	v_fma_f32 v70, v170, v69, v169
	v_cmp_gt_f32_e64 s[26:27], s45, v70
	v_sub_f32_e32 v66, v66, v73
	v_add_f32_e32 v101, v104, v66
	v_cndmask_b32_e64 v69, 0, 32, s[26:27]
	v_ldexp_f32 v69, v70, v69
	v_log_f32_e32 v69, v69
	s_nop 0
	v_mul_f32_e32 v66, 0x3f317217, v69
	v_fma_f32 v66, v69, s46, -v66
	v_fmac_f32_e32 v66, 0x3377d1cf, v69
	v_fmac_f32_e32 v66, 0x3f317217, v69
	v_cmp_lt_f32_e64 vcc, |v69|, s47
	s_nop 1
	v_cndmask_b32_e32 v66, v69, v66, vcc
	v_add_f32_e32 v69, 1.0, v71
	v_rcp_f32_e32 v69, v69
	v_cndmask_b32_e64 v71, 0, v163, s[26:27]
	v_sub_f32_e32 v66, v66, v71
	v_add_f32_e32 v98, v101, v66
	v_fma_f32 v71, v170, v69, v169
	s_waitcnt lgkmcnt(11)
	v_lshlrev_b32_e32 v69, 16, v72
	v_cmp_gt_f32_e32 vcc, s45, v71
	v_mul_f32_e32 v69, 0xbfb8aa3b, v69
	v_exp_f32_e32 v69, v69
	v_cndmask_b32_e64 v66, 0, 32, vcc
	v_ldexp_f32 v66, v71, v66
	v_log_f32_e32 v66, v66
	v_add_f32_e32 v69, 1.0, v69
	v_rcp_f32_e32 v69, v69
	v_mul_f32_e32 v72, 0x3f317217, v66
	v_fma_f32 v72, v66, s46, -v72
	v_fmac_f32_e32 v72, 0x3377d1cf, v66
	v_fmac_f32_e32 v72, 0x3f317217, v66
	v_cmp_lt_f32_e64 s[26:27], |v66|, s47
	v_fma_f32 v73, v170, v69, v169
	s_nop 0
	v_cndmask_b32_e64 v66, v66, v72, s[26:27]
	v_cmp_gt_f32_e64 s[26:27], s45, v73
	v_cndmask_b32_e32 v72, 0, v163, vcc
	v_sub_f32_e32 v66, v66, v72
	v_cndmask_b32_e64 v69, 0, 32, s[26:27]
	v_ldexp_f32 v69, v73, v69
	v_log_f32_e32 v69, v69
	s_waitcnt lgkmcnt(10)
	v_lshlrev_b32_e32 v72, 16, v74
	v_mul_f32_e32 v72, 0xbfb8aa3b, v72
	v_add_f32_e32 v95, v98, v66
	v_mul_f32_e32 v66, 0x3f317217, v69
	v_exp_f32_e32 v72, v72
	v_fma_f32 v66, v69, s46, -v66
	v_fmac_f32_e32 v66, 0x3377d1cf, v69
	v_fmac_f32_e32 v66, 0x3f317217, v69
	v_cmp_lt_f32_e64 vcc, |v69|, s47
	s_nop 1
	v_cndmask_b32_e32 v66, v69, v66, vcc
	v_add_f32_e32 v69, 1.0, v72
	v_rcp_f32_e32 v69, v69
	v_cndmask_b32_e64 v72, 0, v163, s[26:27]
	v_sub_f32_e32 v66, v66, v72
	v_add_f32_e32 v93, v95, v66
	v_fma_f32 v74, v170, v69, v169
	s_waitcnt lgkmcnt(9)
	v_lshlrev_b32_e32 v69, 16, v75
	v_cmp_gt_f32_e32 vcc, s45, v74
	v_mul_f32_e32 v69, 0xbfb8aa3b, v69
	v_exp_f32_e32 v69, v69
	v_cndmask_b32_e64 v66, 0, 32, vcc
	v_ldexp_f32 v66, v74, v66
	v_log_f32_e32 v66, v66
	v_add_f32_e32 v69, 1.0, v69
	v_rcp_f32_e32 v69, v69
	v_mul_f32_e32 v72, 0x3f317217, v66
	v_fma_f32 v72, v66, s46, -v72
	v_fmac_f32_e32 v72, 0x3377d1cf, v66
	v_fmac_f32_e32 v72, 0x3f317217, v66
	v_cmp_lt_f32_e64 s[26:27], |v66|, s47
	v_fma_f32 v75, v170, v69, v169
	s_nop 0
	v_cndmask_b32_e64 v66, v66, v72, s[26:27]
	v_cmp_gt_f32_e64 s[26:27], s45, v75
	v_cndmask_b32_e32 v72, 0, v163, vcc
	v_sub_f32_e32 v66, v66, v72
	v_cndmask_b32_e64 v69, 0, 32, s[26:27]
	v_ldexp_f32 v69, v75, v69
	v_log_f32_e32 v69, v69
	v_add_f32_e32 v90, v93, v66
	v_cndmask_b32_e64 v72, 0, v163, s[26:27]
	v_mul_f32_e32 v66, 0x3f317217, v69
	v_fma_f32 v66, v69, s46, -v66
	v_fmac_f32_e32 v66, 0x3377d1cf, v69
	v_fmac_f32_e32 v66, 0x3f317217, v69
	v_cmp_lt_f32_e64 vcc, |v69|, s47
	s_nop 1
	v_cndmask_b32_e32 v66, v69, v66, vcc
	s_waitcnt lgkmcnt(8)
	v_lshlrev_b32_e32 v69, 16, v76
	v_mul_f32_e32 v69, 0xbfb8aa3b, v69
	v_exp_f32_e32 v69, v69
	v_sub_f32_e32 v66, v66, v72
	v_add_f32_e32 v86, v90, v66
	v_add_f32_e32 v66, 1.0, v69
	v_rcp_f32_e32 v66, v66
	ds_read_u16 v69, v149 offset:2048
	ds_read_u16 v72, v149 offset:2304
	ds_read_u16 v76, v149 offset:2560
	ds_read_u16 v79, v149 offset:2816
	ds_read_u16 v96, v149 offset:3072
	ds_read_u16 v97, v149 offset:3328
	ds_read_u16 v99, v149 offset:3584
	ds_read_u16 v100, v149 offset:3840
	s_waitcnt lgkmcnt(7)
	v_lshlrev_b32_e32 v69, 16, v69
	v_mul_f32_e32 v69, 0xbfb8aa3b, v69
	v_fma_f32 v78, v170, v66, v169
	v_cmp_gt_f32_e32 vcc, s45, v78
	v_exp_f32_e32 v69, v69
	s_waitcnt lgkmcnt(6)
	v_lshlrev_b32_e32 v72, 16, v72
	v_cndmask_b32_e64 v66, 0, 32, vcc
	v_ldexp_f32 v66, v78, v66
	v_log_f32_e32 v66, v66
	v_add_f32_e32 v69, 1.0, v69
	v_rcp_f32_e32 v69, v69
	v_mul_f32_e32 v72, 0xbfb8aa3b, v72
	v_mul_f32_e32 v81, 0x3f317217, v66
	v_fma_f32 v81, v66, s46, -v81
	v_fmac_f32_e32 v81, 0x3377d1cf, v66
	v_fmac_f32_e32 v81, 0x3f317217, v66
	v_cmp_lt_f32_e64 s[26:27], |v66|, s47
	v_fma_f32 v94, v170, v69, v169
	v_exp_f32_e32 v72, v72
	v_cndmask_b32_e64 v66, v66, v81, s[26:27]
	v_cmp_gt_f32_e64 s[26:27], s45, v94
	v_cndmask_b32_e32 v81, 0, v163, vcc
	v_sub_f32_e32 v66, v66, v81
	v_cndmask_b32_e64 v69, 0, 32, s[26:27]
	v_ldexp_f32 v69, v94, v69
	v_log_f32_e32 v69, v69
	v_add_f32_e32 v91, v86, v66
	v_mul_f32_e32 v66, 0x3f317217, v69
	v_fma_f32 v66, v69, s46, -v66
	v_fmac_f32_e32 v66, 0x3377d1cf, v69
	v_fmac_f32_e32 v66, 0x3f317217, v69
	v_cmp_lt_f32_e64 vcc, |v69|, s47
	s_nop 1
	v_cndmask_b32_e32 v66, v69, v66, vcc
	v_add_f32_e32 v69, 1.0, v72
	v_rcp_f32_e32 v69, v69
	v_cndmask_b32_e64 v72, 0, v163, s[26:27]
	v_sub_f32_e32 v66, v66, v72
	v_add_f32_e32 v87, v91, v66
	v_fma_f32 v122, v170, v69, v169
	s_waitcnt lgkmcnt(5)
	v_lshlrev_b32_e32 v69, 16, v76
	v_cmp_gt_f32_e32 vcc, s45, v122
	v_mul_f32_e32 v69, 0xbfb8aa3b, v69
	v_exp_f32_e32 v69, v69
	v_cndmask_b32_e64 v66, 0, 32, vcc
	v_ldexp_f32 v66, v122, v66
	v_log_f32_e32 v66, v66
	v_add_f32_e32 v69, 1.0, v69
	v_rcp_f32_e32 v69, v69
	v_mul_f32_e32 v72, 0x3f317217, v66
	v_fma_f32 v72, v66, s46, -v72
	v_fmac_f32_e32 v72, 0x3377d1cf, v66
	v_fmac_f32_e32 v72, 0x3f317217, v66
	v_cmp_lt_f32_e64 s[26:27], |v66|, s47
	v_fma_f32 v123, v170, v69, v169
	s_nop 0
	v_cndmask_b32_e64 v66, v66, v72, s[26:27]
	v_cmp_gt_f32_e64 s[26:27], s45, v123
	v_cndmask_b32_e32 v72, 0, v163, vcc
	v_sub_f32_e32 v66, v66, v72
	v_cndmask_b32_e64 v69, 0, 32, s[26:27]
	v_ldexp_f32 v69, v123, v69
	v_log_f32_e32 v69, v69
	s_waitcnt lgkmcnt(4)
	v_lshlrev_b32_e32 v72, 16, v79
	v_mul_f32_e32 v72, 0xbfb8aa3b, v72
	v_add_f32_e32 v84, v87, v66
	v_mul_f32_e32 v66, 0x3f317217, v69
	v_exp_f32_e32 v72, v72
	v_fma_f32 v66, v69, s46, -v66
	v_fmac_f32_e32 v66, 0x3377d1cf, v69
	v_fmac_f32_e32 v66, 0x3f317217, v69
	v_cmp_lt_f32_e64 vcc, |v69|, s47
	s_nop 1
	v_cndmask_b32_e32 v66, v69, v66, vcc
	v_add_f32_e32 v69, 1.0, v72
	v_rcp_f32_e32 v69, v69
	v_cndmask_b32_e64 v72, 0, v163, s[26:27]
	v_sub_f32_e32 v66, v66, v72
	v_add_f32_e32 v81, v84, v66
	v_fma_f32 v171, v170, v69, v169
	s_waitcnt lgkmcnt(3)
	v_lshlrev_b32_e32 v69, 16, v96
	v_cmp_gt_f32_e32 vcc, s45, v171
	v_mul_f32_e32 v69, 0xbfb8aa3b, v69
	v_exp_f32_e32 v69, v69
	v_cndmask_b32_e64 v66, 0, 32, vcc
	v_ldexp_f32 v66, v171, v66
	v_log_f32_e32 v66, v66
	v_add_f32_e32 v69, 1.0, v69
	v_rcp_f32_e32 v69, v69
	s_waitcnt lgkmcnt(0)
	v_lshlrev_b32_e32 v96, 16, v100
	v_mul_f32_e32 v72, 0x3f317217, v66
	v_fma_f32 v72, v66, s46, -v72
	v_fmac_f32_e32 v72, 0x3377d1cf, v66
	v_fmac_f32_e32 v72, 0x3f317217, v66
	v_cmp_lt_f32_e64 s[26:27], |v66|, s47
	v_fma_f32 v172, v170, v69, v169
	v_mul_f32_e32 v96, 0xbfb8aa3b, v96
	v_cndmask_b32_e64 v66, v66, v72, s[26:27]
	v_cmp_gt_f32_e64 s[26:27], s45, v172
	v_cndmask_b32_e32 v72, 0, v163, vcc
	v_sub_f32_e32 v66, v66, v72
	v_cndmask_b32_e64 v69, 0, 32, s[26:27]
	v_ldexp_f32 v69, v172, v69
	v_log_f32_e32 v69, v69
	v_lshlrev_b32_e32 v72, 16, v97
	v_mul_f32_e32 v72, 0xbfb8aa3b, v72
	v_add_f32_e32 v79, v81, v66
	v_mul_f32_e32 v66, 0x3f317217, v69
	v_exp_f32_e32 v72, v72
	v_fma_f32 v66, v69, s46, -v66
	v_fmac_f32_e32 v66, 0x3377d1cf, v69
	v_fmac_f32_e32 v66, 0x3f317217, v69
	v_cmp_lt_f32_e64 vcc, |v69|, s47
	v_exp_f32_e32 v96, v96
	s_nop 0
	v_cndmask_b32_e32 v66, v69, v66, vcc
	v_add_f32_e32 v69, 1.0, v72
	v_rcp_f32_e32 v69, v69
	v_cndmask_b32_e64 v72, 0, v163, s[26:27]
	v_sub_f32_e32 v66, v66, v72
	v_add_f32_e32 v76, v79, v66
	v_fma_f32 v173, v170, v69, v169
	v_lshlrev_b32_e32 v69, 16, v99
	v_cmp_gt_f32_e32 vcc, s45, v173
	v_mul_f32_e32 v69, 0xbfb8aa3b, v69
	v_exp_f32_e32 v69, v69
	v_cndmask_b32_e64 v66, 0, 32, vcc
	v_ldexp_f32 v66, v173, v66
	v_log_f32_e32 v66, v66
	v_add_f32_e32 v69, 1.0, v69
	v_rcp_f32_e32 v69, v69
	v_mul_f32_e32 v72, 0x3f317217, v66
	v_fma_f32 v72, v66, s46, -v72
	v_fmac_f32_e32 v72, 0x3377d1cf, v66
	v_fmac_f32_e32 v72, 0x3f317217, v66
	v_cmp_lt_f32_e64 s[26:27], |v66|, s47
	v_fma_f32 v174, v170, v69, v169
	s_nop 0
	v_cndmask_b32_e64 v66, v66, v72, s[26:27]
	v_cmp_gt_f32_e64 s[26:27], s45, v174
	v_cndmask_b32_e32 v72, 0, v163, vcc
	v_sub_f32_e32 v66, v66, v72
	v_cndmask_b32_e64 v69, 0, 32, s[26:27]
	v_ldexp_f32 v69, v174, v69
	v_log_f32_e32 v69, v69
	v_add_f32_e32 v72, v76, v66
	v_mul_f32_e32 v66, 0x3f317217, v69
	v_fma_f32 v66, v69, s46, -v66
	v_fmac_f32_e32 v66, 0x3377d1cf, v69
	v_fmac_f32_e32 v66, 0x3f317217, v69
	v_cmp_lt_f32_e64 vcc, |v69|, s47
	s_nop 1
	v_cndmask_b32_e32 v66, v69, v66, vcc
	v_add_f32_e32 v69, 1.0, v96
	v_rcp_f32_e32 v96, v69
	v_cndmask_b32_e64 v69, 0, v163, s[26:27]
	v_sub_f32_e32 v66, v66, v69
	v_add_f32_e32 v69, v72, v66
	v_fma_f32 v175, v170, v96, v169
	v_cmp_gt_f32_e32 vcc, s45, v175
	ds_read_u16 v96, v150 offset:2048
	ds_read_u16 v183, v150 offset:2304
	ds_read_u16 v182, v150 offset:2560
	ds_read_u16 v181, v150 offset:2816
	ds_read_u16 v180, v150 offset:3072
	ds_read_u16 v178, v150 offset:3328
	ds_read_u16 v177, v150 offset:3584
	ds_read_u16 v176, v150 offset:3840
	v_cndmask_b32_e64 v66, 0, 32, vcc
	v_ldexp_f32 v66, v175, v66
	v_log_f32_e32 v66, v66
	s_nop 0
	v_mul_f32_e32 v97, 0x3f317217, v66
	v_fma_f32 v97, v66, s46, -v97
	v_fmac_f32_e32 v97, 0x3377d1cf, v66
	v_fmac_f32_e32 v97, 0x3f317217, v66
	v_cmp_lt_f32_e64 s[26:27], |v66|, s47
	s_nop 1
	v_cndmask_b32_e64 v66, v66, v97, s[26:27]
	v_cndmask_b32_e32 v97, 0, v163, vcc
	v_sub_f32_e32 v66, v66, v97
	v_add_f32_e32 v66, v69, v66
	ds_write_b32 v131, v66
	s_waitcnt lgkmcnt(0)
	s_barrier
	v_cndmask_b32_e64 v97, 0, 1, s[40:41]
	v_cmp_ne_u32_e64 s[26:27], 1, v97
	s_andn2_b64 vcc, exec, s[40:41]
	s_cbranch_vccnz .LBB0_656
	s_add_u32 s28, s50, s38
	v_mov_b32_e32 v10, v126
	v_mov_b32_e32 v108, v125
	v_mov_b32_e32 v11, v127
	s_addc_u32 s29, s51, s39
	s_nop 0
	v_lshl_add_u64 v[12:13], s[28:29], 0, v[108:109]
	v_add_co_u32_e32 v12, vcc, 0x26243000, v12
	v_mov_b32_e32 v11, v109
	s_nop 0
	v_addc_co_u32_e32 v13, vcc, 0, v13, vcc
	v_lshl_add_u64 v[10:11], s[28:29], 0, v[10:11]
	v_add_co_u32_e32 v14, vcc, 0x26243000, v10
	s_nop 1
	v_addc_co_u32_e32 v15, vcc, 0, v11, vcc
	global_load_dwordx4 v[10:13], v[12:13], off nt
	s_nop 0
	global_load_dwordx4 v[14:17], v[14:15], off nt

.LBB0_658:
	s_or_b64 exec, exec, s[40:41]
	s_waitcnt lgkmcnt(0)
	s_barrier
	s_and_b64 vcc, exec, s[26:27]
	s_cbranch_vccnz .LBB0_660
	s_add_u32 s28, s50, s38
	v_mov_b32_e32 v18, v126
	v_mov_b32_e32 v108, v125
	v_mov_b32_e32 v19, v127
	s_addc_u32 s29, s51, s39
	s_nop 0
	v_lshl_add_u64 v[20:21], s[28:29], 0, v[108:109]
	v_add_co_u32_e32 v20, vcc, 0x26245000, v20
	v_mov_b32_e32 v19, v109
	s_nop 0
	v_addc_co_u32_e32 v21, vcc, 0, v21, vcc
	v_lshl_add_u64 v[18:19], s[28:29], 0, v[18:19]
	v_add_co_u32_e32 v22, vcc, 0x26245000, v18
	s_nop 1
	v_addc_co_u32_e32 v23, vcc, 0, v19, vcc
	global_load_dwordx4 v[18:21], v[20:21], off nt
	s_nop 0
	global_load_dwordx4 v[22:25], v[22:23], off nt

.LBB0_664:
	s_nop 7
	v_cndmask_b32_e64 v66, v66, 0, s[18:19]
	v_bfe_u32 v70, v66, 16, 1
	v_add3_u32 v66, v66, v70, s48
	ds_write_b16_d16_hi v156, v66
	v_cndmask_b32_e64 v66, v67, 0, s[20:21]
	v_bfe_u32 v67, v66, 16, 1
	v_add3_u32 v66, v66, v67, s48
	ds_write_b16_d16_hi v156, v66 offset:144
	v_cndmask_b32_e64 v66, v68, 0, s[22:23]
	v_bfe_u32 v67, v66, 16, 1
	v_add3_u32 v66, v66, v67, s48
	ds_write_b16_d16_hi v156, v66 offset:288
	v_cndmask_b32_e64 v66, v69, 0, s[24:25]
	v_bfe_u32 v67, v66, 16, 1
	v_add3_u32 v66, v66, v67, s48
	ds_write_b16_d16_hi v156, v66 offset:432
	s_waitcnt lgkmcnt(0)
	s_barrier
	s_waitcnt vmcnt(0)
	v_mov_b64_e32 v[68:69], v[48:49]
	v_mov_b64_e32 v[72:73], v[40:41]
	s_and_b64 vcc, exec, s[26:27]
	v_mov_b64_e32 v[66:67], v[46:47]
	v_mov_b64_e32 v[70:71], v[38:39]
	s_cbranch_vccnz .LBB0_666
	v_mov_b32_e32 v66, v126
	v_mov_b32_e32 v67, v125
	v_mov_b32_e32 v108, v127
	s_add_u32 s26, s50, s38
	s_addc_u32 s27, s51, s39
	v_lshl_add_u64 v[66:67], s[26:27], 0, v[108:109]
	s_mov_b64 s[26:27], 0x26240000
	v_lshl_add_u64 v[70:71], v[66:67], 0, s[26:27]
	v_add_co_u32_e32 v66, vcc, 0x26240000, v66
	s_nop 1
	v_addc_co_u32_e32 v67, vcc, 0, v67, vcc
	global_load_dwordx4 v[66:69], v[66:67], off nt
	s_nop 0
	global_load_dwordx4 v[70:73], v[70:71], off offset:16 nt
.LBB0_666:
	ds_read_b64_tr_b16 v[78:79], v157 offset:53248
	ds_read_b64_tr_b16 v[80:81], v157 offset:54400
	ds_read_b64_tr_b16 v[74:75], v157 offset:62464
	ds_read_b64_tr_b16 v[76:77], v157 offset:63616
	ds_read_b128 v[82:85], v158
	ds_read_b128 v[86:89], v158 offset:2304
	ds_read_b128 v[90:93], v158 offset:4608
	ds_read_b128 v[94:97], v158 offset:4672
	ds_read_b128 v[98:101], v158 offset:6976
	v_add_u32_e32 v108, v137, v135
	v_add_u32_e32 v104, v137, v141
	s_waitcnt lgkmcnt(4)
	v_mfma_f32_16x16x32_bf16 v[82:85], v[82:85], v[78:81], 0
	v_add_u32_e32 v122, v142, v135
	v_add_u32_e32 v123, v143, v135
	v_add_u32_e32 v171, v144, v135
	s_waitcnt lgkmcnt(2)
	v_mfma_f32_16x16x32_bf16 v[90:93], v[90:93], v[78:81], 0
	s_lshl_b32 s30, s49, 6
	s_add_i32 s49, s49, 1
	s_add_u32 s38, s38, 0x240000
	s_waitcnt lgkmcnt(1)
	v_mfma_f32_16x16x32_bf16 v[90:93], v[94:97], v[74:77], v[90:93]
	ds_read_b128 v[94:97], v158 offset:6912
	s_addc_u32 s39, s39, 0
	s_mov_b64 s[26:27], 0x20000
	v_mfma_f32_16x16x32_bf16 v[86:89], v[86:89], v[78:81], 0
	v_lshl_add_u64 v[120:121], v[120:121], 0, s[26:27]
	s_cmp_lg_u32 s38, 0x4800000
	s_waitcnt lgkmcnt(0)
	v_mfma_f32_16x16x32_bf16 v[94:97], v[94:97], v[78:81], 0
	v_mfma_f32_16x16x32_bf16 v[94:97], v[98:101], v[74:77], v[94:97]
	v_cvt_pk_bf16_f32 v98, v26, v27
	v_cvt_pk_bf16_f32 v99, v28, v29
	v_cvt_pk_bf16_f32 v100, v30, v31
	v_cvt_pk_bf16_f32 v101, v32, v33
	ds_read_b64 v[102:103], v108
	ds_read_b64 v[104:105], v104
	s_waitcnt lgkmcnt(0)
	v_mfma_f32_16x16x32_bf16 v[82:85], v[102:105], v[98:101], v[82:85]
	v_add_u32_e32 v104, v142, v141
	ds_read_b64 v[102:103], v122
	ds_read_b64 v[104:105], v104
	s_waitcnt lgkmcnt(0)
	v_mfma_f32_16x16x32_bf16 v[86:89], v[102:105], v[98:101], v[86:89]
	v_add_u32_e32 v104, v143, v141
	ds_read_b64 v[102:103], v123
	ds_read_b64 v[104:105], v104
	s_waitcnt lgkmcnt(0)
	v_mfma_f32_16x16x32_bf16 v[90:93], v[102:105], v[98:101], v[90:93]
	v_add_u32_e32 v104, v144, v141
	ds_read_b64 v[102:103], v171
	ds_read_b64 v[104:105], v104
	s_waitcnt lgkmcnt(0)
	v_mfma_f32_16x16x32_bf16 v[94:97], v[102:105], v[98:101], v[94:97]
	v_add_u32_e32 v102, v137, v145
	v_add_u32_e32 v104, v137, v146
	v_cvt_pk_bf16_f32 v98, v62, v63
	v_cvt_pk_bf16_f32 v99, v64, v65
	v_cvt_pk_bf16_f32 v100, v54, v55
	v_cvt_pk_bf16_f32 v101, v56, v57
	ds_read_b64 v[102:103], v102
	ds_read_b64 v[104:105], v104
	s_waitcnt lgkmcnt(0)
	v_mfma_f32_16x16x32_bf16 v[82:85], v[102:105], v[98:101], v[82:85]
	v_add_u32_e32 v102, v142, v145
	v_add_u32_e32 v104, v142, v146
	ds_read_b64 v[102:103], v102
	ds_read_b64 v[104:105], v104
	s_waitcnt lgkmcnt(0)
	v_mfma_f32_16x16x32_bf16 v[86:89], v[102:105], v[98:101], v[86:89]
	v_add_u32_e32 v102, v143, v145
	v_add_u32_e32 v104, v143, v146
	ds_read_b64 v[102:103], v102
	ds_read_b64 v[104:105], v104
	s_waitcnt lgkmcnt(0)
	v_mfma_f32_16x16x32_bf16 v[90:93], v[102:105], v[98:101], v[90:93]
	v_add_u32_e32 v102, v144, v145
	v_add_u32_e32 v104, v144, v146
	ds_read_b64 v[102:103], v102
	ds_read_b64 v[104:105], v104
	s_waitcnt lgkmcnt(0)
	v_mfma_f32_16x16x32_bf16 v[94:97], v[102:105], v[98:101], v[94:97]
	v_cvt_pk_bf16_f32 v98, v34, v35
	v_cvt_pk_bf16_f32 v99, v36, v37
	v_cvt_pk_bf16_f32 v100, v50, v51
	v_cvt_pk_bf16_f32 v101, v52, v53
	ds_read2_b64 v[102:105], v108 offset0:16 offset1:20
	s_waitcnt lgkmcnt(0)
	v_mfma_f32_16x16x32_bf16 v[82:85], v[102:105], v[98:101], v[82:85]
	ds_read2_b64 v[102:105], v122 offset0:16 offset1:20
	s_waitcnt lgkmcnt(0)
	v_mfma_f32_16x16x32_bf16 v[86:89], v[102:105], v[98:101], v[86:89]
	ds_read2_b64 v[102:105], v123 offset0:16 offset1:20
	s_waitcnt lgkmcnt(0)
	v_mfma_f32_16x16x32_bf16 v[90:93], v[102:105], v[98:101], v[90:93]
	ds_read2_b64 v[102:105], v171 offset0:16 offset1:20
	s_waitcnt lgkmcnt(0)
	v_mfma_f32_16x16x32_bf16 v[94:97], v[102:105], v[98:101], v[94:97]
	v_cvt_pk_bf16_f32 v98, v42, v43
	v_cvt_pk_bf16_f32 v99, v44, v45
	v_cvt_pk_bf16_f32 v100, v58, v59
	v_cvt_pk_bf16_f32 v101, v60, v61
	ds_read2_b64 v[102:105], v108 offset0:24 offset1:28
	s_waitcnt lgkmcnt(0)
	v_mfma_f32_16x16x32_bf16 v[82:85], v[102:105], v[98:101], v[82:85]
	ds_read2_b64 v[102:105], v122 offset0:24 offset1:28
	s_waitcnt lgkmcnt(0)
	v_mfma_f32_16x16x32_bf16 v[86:89], v[102:105], v[98:101], v[86:89]
	ds_read2_b64 v[102:105], v123 offset0:24 offset1:28
	v_lshl_add_u64 v[122:123], v[118:119], 0, s[30:31]
	s_waitcnt lgkmcnt(0)
	v_mfma_f32_16x16x32_bf16 v[90:93], v[102:105], v[98:101], v[90:93]
	ds_read2_b64 v[102:105], v171 offset0:24 offset1:28
	ds_write2_b32 v159, v82, v83 offset1:132
	v_add_u32_e32 v82, 0x400, v159
	s_waitcnt lgkmcnt(1)
	v_mfma_f32_16x16x32_bf16 v[94:97], v[102:105], v[98:101], v[94:97]
	ds_write2_b32 v82, v84, v85 offset0:8 offset1:140
	ds_write_b32 v160, v86
	v_add_u32_e32 v82, 0x2200, v159
	ds_write2_b32 v82, v87, v88 offset0:68 offset1:200
	ds_write_b32 v159, v89 offset:10032
	ds_write_b32 v160, v90 offset:8448
	v_add_u32_e32 v82, 0x4400, v159
	ds_write2_b32 v82, v91, v92 offset0:4 offset1:136
	ds_write_b32 v159, v93 offset:18480
	ds_write_b32 v160, v94 offset:16896
	v_add_u32_e32 v82, 0x6400, v159
	ds_write2_b32 v82, v95, v96 offset0:68 offset1:200
	ds_write_b32 v159, v97 offset:26928
	v_add_u32_e32 v92, 0x1c000, v134
	ds_read_b128 v[82:85], v92
	s_waitcnt lgkmcnt(0)
	v_pk_mul_f32 v[26:27], v[26:27], v[82:83]
	v_add_u32_e32 v82, v140, v136
	v_pk_mul_f32 v[28:29], v[28:29], v[84:85]
	ds_read_b64_tr_b16 v[86:87], v82 offset:35968
	ds_read_b64_tr_b16 v[84:85], v82 offset:34816
	ds_read_b64_tr_b16 v[88:89], v82 offset:34848
	s_waitcnt lgkmcnt(1)
	v_mfma_f32_16x16x32_bf16 v[26:29], v[84:87], v[78:81], v[26:29]
	ds_read_b64_tr_b16 v[84:85], v82 offset:44032
	ds_read_b64_tr_b16 v[86:87], v82 offset:45184
	ds_read_b64_tr_b16 v[90:91], v82 offset:36000
	s_waitcnt lgkmcnt(1)
	v_mfma_f32_16x16x32_bf16 v[26:29], v[84:87], v[74:77], v[26:29]
	ds_read_b128 v[84:87], v92 offset:64
	s_waitcnt lgkmcnt(0)
	v_pk_mul_f32 v[30:31], v[30:31], v[84:85]
	v_pk_mul_f32 v[32:33], v[32:33], v[86:87]
	ds_read_b64_tr_b16 v[84:85], v82 offset:44064
	ds_read_b64_tr_b16 v[86:87], v82 offset:45216
	v_mfma_f32_16x16x32_bf16 v[30:33], v[88:91], v[78:81], v[30:33]
	s_waitcnt lgkmcnt(0)
	v_mfma_f32_16x16x32_bf16 v[30:33], v[84:87], v[74:77], v[30:33]
	ds_read_b128 v[84:87], v92 offset:128
	s_waitcnt lgkmcnt(0)
	v_pk_mul_f32 v[62:63], v[62:63], v[84:85]
	v_pk_mul_f32 v[64:65], v[64:65], v[86:87]
	ds_read_b64_tr_b16 v[84:85], v82 offset:34880
	ds_read_b64_tr_b16 v[86:87], v82 offset:36032
	s_waitcnt lgkmcnt(0)
	v_mfma_f32_16x16x32_bf16 v[62:65], v[84:87], v[78:81], v[62:65]
	ds_read_b64_tr_b16 v[84:85], v82 offset:44096
	ds_read_b64_tr_b16 v[86:87], v82 offset:45248
	s_waitcnt lgkmcnt(0)
	v_mfma_f32_16x16x32_bf16 v[62:65], v[84:87], v[74:77], v[62:65]
	ds_read_b128 v[84:87], v92 offset:192
	s_waitcnt lgkmcnt(0)
	v_pk_mul_f32 v[54:55], v[54:55], v[84:85]
	v_pk_mul_f32 v[56:57], v[56:57], v[86:87]
	ds_read_b64_tr_b16 v[84:85], v82 offset:34912
	ds_read_b64_tr_b16 v[86:87], v82 offset:36064
	s_waitcnt lgkmcnt(0)
	v_mfma_f32_16x16x32_bf16 v[54:57], v[84:87], v[78:81], v[54:57]
	ds_read_b64_tr_b16 v[84:85], v82 offset:44128
	ds_read_b64_tr_b16 v[86:87], v82 offset:45280
	s_waitcnt lgkmcnt(0)
	v_mfma_f32_16x16x32_bf16 v[54:57], v[84:87], v[74:77], v[54:57]
	ds_read_b128 v[84:87], v92 offset:256
	s_waitcnt lgkmcnt(0)
	v_pk_mul_f32 v[34:35], v[34:35], v[84:85]
	v_pk_mul_f32 v[36:37], v[36:37], v[86:87]
	ds_read_b64_tr_b16 v[84:85], v82 offset:34944
	ds_read_b64_tr_b16 v[86:87], v82 offset:36096
	s_waitcnt lgkmcnt(0)
	v_mfma_f32_16x16x32_bf16 v[34:37], v[84:87], v[78:81], v[34:37]
	ds_read_b64_tr_b16 v[84:85], v82 offset:44160
	ds_read_b64_tr_b16 v[86:87], v82 offset:45312
	s_waitcnt lgkmcnt(0)
	v_mfma_f32_16x16x32_bf16 v[34:37], v[84:87], v[74:77], v[34:37]
	ds_read_b128 v[84:87], v92 offset:320
	s_waitcnt lgkmcnt(0)
	v_pk_mul_f32 v[50:51], v[50:51], v[84:85]
	v_pk_mul_f32 v[52:53], v[52:53], v[86:87]
	ds_read_b64_tr_b16 v[84:85], v82 offset:34976
	ds_read_b64_tr_b16 v[86:87], v82 offset:36128
	s_waitcnt lgkmcnt(0)
	v_mfma_f32_16x16x32_bf16 v[50:53], v[84:87], v[78:81], v[50:53]
	ds_read_b64_tr_b16 v[84:85], v82 offset:44192
	ds_read_b64_tr_b16 v[86:87], v82 offset:45344
	s_waitcnt lgkmcnt(0)
	v_mfma_f32_16x16x32_bf16 v[50:53], v[84:87], v[74:77], v[50:53]
	ds_read_b128 v[84:87], v92 offset:384
	s_waitcnt lgkmcnt(0)
	v_pk_mul_f32 v[42:43], v[42:43], v[84:85]
	v_pk_mul_f32 v[44:45], v[44:45], v[86:87]
	ds_read_b64_tr_b16 v[84:85], v82 offset:35008
	ds_read_b64_tr_b16 v[86:87], v82 offset:36160
	s_waitcnt lgkmcnt(0)
	v_mfma_f32_16x16x32_bf16 v[42:45], v[84:87], v[78:81], v[42:45]
	ds_read_b64_tr_b16 v[84:85], v82 offset:44224
	ds_read_b64_tr_b16 v[86:87], v82 offset:45376
	s_waitcnt lgkmcnt(0)
	v_mfma_f32_16x16x32_bf16 v[42:45], v[84:87], v[74:77], v[42:45]
	ds_read_b128 v[84:87], v92 offset:448
	s_waitcnt lgkmcnt(0)
	v_pk_mul_f32 v[58:59], v[58:59], v[84:85]
	v_pk_mul_f32 v[60:61], v[60:61], v[86:87]
	ds_read_b64_tr_b16 v[84:85], v82 offset:35040
	ds_read_b64_tr_b16 v[86:87], v82 offset:36192
	s_waitcnt lgkmcnt(0)
	v_mfma_f32_16x16x32_bf16 v[58:61], v[84:87], v[78:81], v[58:61]
	ds_read_b64_tr_b16 v[78:79], v82 offset:44256
	ds_read_b64_tr_b16 v[80:81], v82 offset:45408
	s_waitcnt lgkmcnt(0)
	s_barrier
	s_waitcnt lgkmcnt(0)
	v_mfma_f32_16x16x32_bf16 v[58:61], v[78:81], v[74:77], v[58:61]
	ds_read_b128 v[86:89], v161
	ds_read_b128 v[82:85], v161 offset:16
	ds_read_b128 v[78:81], v161 offset:32
	ds_read_b128 v[74:77], v161 offset:48
	s_waitcnt lgkmcnt(3)
	v_pk_mul_f32 v[90:91], v[88:89], v[88:89]
	v_pk_mul_f32 v[92:93], v[86:87], v[86:87]
	s_nop 0
	v_pk_mov_b32 v[94:95], v[92:93], v[90:91] op_sel:[1,0]
	v_mov_b32_e32 v93, v91
	v_pk_add_f32 v[90:91], v[94:95], v[92:93]
	s_waitcnt lgkmcnt(2)
	v_pk_mul_f32 v[92:93], v[84:85], v[84:85]
	v_pk_mul_f32 v[94:95], v[82:83], v[82:83]
	v_pk_add_f32 v[90:91], v[90:91], v[90:91] op_sel:[0,1] op_sel_hi:[1,0]
	v_pk_mov_b32 v[96:97], v[94:95], v[92:93] op_sel:[1,0]
	v_mov_b32_e32 v95, v93
	v_pk_add_f32 v[92:93], v[96:97], v[94:95]
	s_waitcnt lgkmcnt(0)
	v_mul_f32_e32 v94, v74, v74
	v_mul_f32_e32 v95, v75, v75
	v_pk_add_f32 v[92:93], v[92:93], v[92:93] op_sel:[0,1] op_sel_hi:[1,0]
	v_mov_b32_e32 v91, v94
	v_mov_b32_e32 v93, v95
	v_pk_add_f32 v[90:91], v[90:91], v[92:93]
	v_mul_f32_e32 v92, v79, v79
	v_mul_f32_e32 v94, v81, v81
	v_mul_f32_e32 v96, v76, v76
	v_mul_f32_e32 v97, v77, v77
	v_pk_fma_f32 v[92:93], v[78:79], v[78:79], v[92:93] op_sel_hi:[1,1,0]
	v_pk_fma_f32 v[94:95], v[80:81], v[80:81], v[94:95] op_sel_hi:[1,1,0]
	v_mov_b32_e32 v93, v96
	v_mov_b32_e32 v95, v97
	v_pk_add_f32 v[92:93], v[92:93], v[94:95]
	s_nop 0
	v_pk_add_f32 v[90:91], v[90:91], v[92:93]
	v_and_b32_e32 v92, 64, v166
	v_add_f32_e32 v90, v90, v91
	v_xor_b32_e32 v91, 1, v166
	v_add_u32_e32 v92, 64, v92
	v_cmp_lt_i32_e32 vcc, v91, v92
	s_nop 1
	v_cndmask_b32_e32 v91, v166, v91, vcc
	v_lshlrev_b32_e32 v91, 2, v91
	ds_bpermute_b32 v91, v91, v90
	s_waitcnt lgkmcnt(0)
	v_add_f32_e32 v90, v90, v91
	v_xor_b32_e32 v91, 2, v166
	v_cmp_lt_i32_e32 vcc, v91, v92
	s_nop 1
	v_cndmask_b32_e32 v91, v166, v91, vcc
	v_lshlrev_b32_e32 v91, 2, v91
	ds_bpermute_b32 v91, v91, v90
	s_waitcnt lgkmcnt(0)
	v_add_f32_e32 v90, v90, v91
	v_xor_b32_e32 v91, 4, v166
	v_cmp_lt_i32_e32 vcc, v91, v92
	s_nop 1
	v_cndmask_b32_e32 v91, v166, v91, vcc
	v_lshlrev_b32_e32 v91, 2, v91
	ds_bpermute_b32 v91, v91, v90
	s_waitcnt lgkmcnt(0)
	v_add_f32_e32 v90, v90, v91
	v_fmamk_f32 v90, v90, 0x3c000000, v162
	v_cmp_gt_f32_e32 vcc, s45, v90
	v_mul_f32_e32 v91, 0x4b800000, v90
	s_nop 0
	v_cndmask_b32_e32 v90, v90, v91, vcc
	v_rsq_f32_e32 v90, v90
	s_nop 0
	v_mul_f32_e32 v91, 0x45800000, v90
	v_cndmask_b32_e32 v108, v90, v91, vcc
	global_load_dwordx4 v[90:93], v[110:111], off offset:48 nt
	global_load_dwordx4 v[94:97], v[110:111], off offset:32 nt
	global_load_dwordx4 v[98:101], v[110:111], off offset:16 nt
	global_load_dwordx4 v[102:105], v[110:111], off nt
	v_mul_f32_e32 v86, v86, v108
	v_mul_f32_e32 v87, v87, v108
	v_mul_f32_e32 v83, v83, v108
	v_mul_f32_e32 v79, v79, v108
	v_mul_f32_e32 v74, v74, v108
	v_mul_f32_e32 v82, v82, v108
	v_mul_f32_e32 v78, v78, v108
	s_waitcnt vmcnt(3)
	v_mul_f32_e32 v74, v90, v74
	s_waitcnt vmcnt(2)
	v_mul_f32_e32 v79, v95, v79
	s_waitcnt vmcnt(1)
	v_mul_f32_e32 v83, v99, v83
	s_waitcnt vmcnt(0)
	v_mul_f32_e32 v86, v102, v86
	v_lshlrev_b32_e32 v102, 16, v46
	v_mul_f32_e32 v87, v103, v87
	v_and_b32_e32 v46, 0xffff0000, v46
	v_mul_f32_e32 v46, v87, v46
	v_mul_f32_e32 v87, v88, v108
	v_mul_f32_e32 v87, v104, v87
	v_lshlrev_b32_e32 v88, 16, v47
	v_mul_f32_e32 v87, v87, v88
	v_mul_f32_e32 v88, v89, v108
	v_mul_f32_e32 v88, v105, v88
	v_and_b32_e32 v47, 0xffff0000, v47
	v_mul_f32_e32 v47, v88, v47
	v_lshlrev_b32_e32 v88, 16, v48
	v_and_b32_e32 v48, 0xffff0000, v48
	v_mul_f32_e32 v48, v83, v48
	v_mul_f32_e32 v83, v84, v108
	v_mul_f32_e32 v83, v100, v83
	v_lshlrev_b32_e32 v84, 16, v49
	v_mul_f32_e32 v83, v83, v84
	v_mul_f32_e32 v84, v85, v108
	v_mul_f32_e32 v84, v101, v84
	v_and_b32_e32 v49, 0xffff0000, v49
	v_mul_f32_e32 v49, v84, v49
	v_lshlrev_b32_e32 v84, 16, v38
	v_and_b32_e32 v38, 0xffff0000, v38
	v_mul_f32_e32 v38, v79, v38
	v_mul_f32_e32 v79, v80, v108
	v_mul_f32_e32 v79, v96, v79
	v_lshlrev_b32_e32 v80, 16, v39
	v_mul_f32_e32 v79, v79, v80
	v_mul_f32_e32 v80, v81, v108
	v_mul_f32_e32 v80, v97, v80
	v_and_b32_e32 v39, 0xffff0000, v39
	v_mul_f32_e32 v39, v80, v39
	v_lshlrev_b32_e32 v80, 16, v40
	v_mul_f32_e32 v80, v74, v80
	v_mul_f32_e32 v74, v75, v108
	v_mul_f32_e32 v74, v91, v74
	v_and_b32_e32 v40, 0xffff0000, v40
	v_mul_f32_e32 v40, v74, v40
	v_mul_f32_e32 v74, v76, v108
	v_mul_f32_e32 v74, v92, v74
	v_lshlrev_b32_e32 v75, 16, v41
	v_mul_f32_e32 v81, v74, v75
	v_mul_f32_e32 v74, v77, v108
	v_mul_f32_e32 v82, v98, v82
	v_mul_f32_e32 v78, v94, v78
	v_mul_f32_e32 v74, v93, v74
	v_and_b32_e32 v41, 0xffff0000, v41
	v_mul_f32_e32 v86, v86, v102
	v_mul_f32_e32 v82, v82, v88
	v_mul_f32_e32 v78, v78, v84
	v_mul_f32_e32 v41, v74, v41
	v_mov_b32_e32 v74, 0
	v_mov_b32_e32 v75, 0
	v_mov_b32_e32 v76, 0
	v_mov_b32_e32 v77, 0
	v_cvt_pk_fp8_f32 v74, v86, v46
	v_cvt_pk_fp8_f32 v75, v82, v48
	v_cvt_pk_fp8_f32 v76, v78, v38
	v_cvt_pk_fp8_f32 v77, v80, v40
	v_cvt_pk_fp8_f32 v74, v87, v47 op_sel:[0,0,1]
	v_cvt_pk_fp8_f32 v75, v83, v49 op_sel:[0,0,1]
	v_cvt_pk_fp8_f32 v76, v79, v39 op_sel:[0,0,1]
	v_cvt_pk_fp8_f32 v77, v81, v41 op_sel:[0,0,1]
	v_lshlrev_b64 v[38:39], 11, v[122:123]
	v_lshl_add_u64 v[78:79], v[116:117], 0, v[38:39]
	s_cbranch_scc0 .LBB0_642
	v_mov_b64_e32 v[38:39], v[70:71]
	v_mov_b64_e32 v[46:47], v[66:67]
	v_mov_b64_e32 v[40:41], v[72:73]
	v_mov_b64_e32 v[48:49], v[68:69]
	s_branch .LBB0_650

.LBB0_995:
	v_lshl_or_b32 v2, s41, 8, v198
	v_ashrrev_i32_e32 v3, 31, v2
	v_readlane_b32 s24, v255, 4
	v_lshlrev_b64 v[10:11], 1, v[2:3]
	v_readlane_b32 s25, v255, 5
	v_lshl_add_u32 v180, s20, 8, v196
	s_nop 15
	s_nop 15
	v_or_b32_e32 v203, 16, v180
	v_lshl_add_u64 v[14:15], s[24:25], 0, v[10:11]
	v_mad_i64_i32 v[2:3], s[22:23], v180, s38, v[14:15]
	v_add_co_u32_e32 v2, vcc, 0x7000, v2
	v_mov_b64_e32 v[12:13], s[24:25]
	s_nop 0
	v_addc_co_u32_e32 v3, vcc, 0, v3, vcc
	global_load_dwordx4 v[16:19], v[2:3], off nt
	global_load_dwordx4 v[20:23], v[2:3], off offset:256 nt
	v_mad_i64_i32 v[2:3], s[22:23], v203, s38, v[14:15]
	v_add_co_u32_e32 v2, vcc, 0x7000, v2
	v_mad_i64_i32 v[4:5], s[22:23], v180, s38, v[12:13]
	s_nop 0
	v_addc_co_u32_e32 v3, vcc, 0, v3, vcc
	global_load_dwordx4 v[24:27], v[2:3], off nt
	global_load_dwordx4 v[28:31], v[2:3], off offset:256 nt
	v_lshl_add_u64 v[4:5], v[4:5], 0, v[10:11]
	v_or_b32_e32 v204, 32, v180
	v_add_co_u32_e32 v32, vcc, s40, v4
	v_mad_i64_i32 v[6:7], s[22:23], v204, s38, v[14:15]
	s_nop 0
	v_addc_co_u32_e32 v33, vcc, 0, v5, vcc
	v_add_co_u32_e32 v4, vcc, 0x7000, v6
	v_mul_f32_e32 v181, 0x3d000000, v150
	s_nop 0
	v_addc_co_u32_e32 v5, vcc, 0, v7, vcc
	v_mul_f32_e32 v182, 0x3d000000, v146
	v_mul_f32_e32 v183, 0x3d000000, v151
	v_mul_f32_e32 v184, 0x3d000000, v147
	v_mul_f32_e32 v185, 0x3d000000, v152
	v_mul_f32_e32 v186, 0x3d000000, v148
	v_mul_f32_e32 v187, 0x3d000000, v153
	v_mul_f32_e32 v202, 0x3d000000, v149
	global_load_dwordx4 v[146:149], v[4:5], off nt
	global_load_dwordx4 v[150:153], v[4:5], off offset:256 nt
	v_or_b32_e32 v205, 48, v180
	v_mad_i64_i32 v[8:9], s[22:23], v205, s38, v[14:15]
	v_add_co_u32_e32 v2, vcc, 0x7000, v8
	v_mul_f32_e32 v161, 0x3d000000, v161
	s_nop 0
	v_addc_co_u32_e32 v3, vcc, 0, v9, vcc
	global_load_dwordx4 v[6:9], v[2:3], off nt
	s_nop 0
	global_load_dwordx4 v[2:5], v[2:3], off offset:256 nt
	v_mul_f32_e32 v159, 0x3d000000, v159
	v_mul_f32_e32 v155, 0x3d000000, v155
	v_mul_f32_e32 v160, 0x3d000000, v160
	v_mul_f32_e32 v157, 0x3d000000, v157
	v_mul_f32_e32 v158, 0x3d000000, v158
	v_mul_f32_e32 v154, 0x3d000000, v154
	v_mul_f32_e32 v156, 0x3d000000, v156
	v_mul_f32_e32 v94, 0x3d000000, v94
	v_mul_f32_e32 v95, 0x3d000000, v95
	v_mul_f32_e32 v91, 0x3d000000, v91
	v_mul_f32_e32 v96, 0x3d000000, v96
	v_mul_f32_e32 v90, 0x3d000000, v90
	v_mul_f32_e32 v97, 0x3d000000, v97
	v_mul_f32_e32 v93, 0x3d000000, v93
	v_mul_f32_e32 v92, 0x3d000000, v92
	s_waitcnt vmcnt(0)
	v_lshlrev_b32_e32 v207, 16, v17
	v_and_b32_e32 v17, 0xffff0000, v17
	v_lshlrev_b32_e32 v206, 16, v16
	v_and_b32_e32 v16, 0xffff0000, v16
	v_lshlrev_b32_e32 v208, 16, v18
	v_and_b32_e32 v18, 0xffff0000, v18
	v_lshlrev_b32_e32 v209, 16, v19
	v_and_b32_e32 v19, 0xffff0000, v19
	v_mul_f32_e32 v17, v161, v17
	v_mul_f32_e32 v16, v159, v16
	v_mul_f32_e32 v159, v160, v207
	v_mul_f32_e32 v18, v155, v18
	v_mul_f32_e32 v19, v157, v19
	v_cvt_pk_bf16_f32 v17, v159, v17
	v_lshlrev_b32_e32 v210, 16, v20
	v_mul_f32_e32 v158, v158, v206
	v_mul_f32_e32 v154, v154, v208
	v_mul_f32_e32 v155, v156, v209
	v_cvt_pk_bf16_f32 v16, v158, v16
	v_cvt_pk_bf16_f32 v18, v154, v18
	v_cvt_pk_bf16_f32 v19, v155, v19
	global_store_dwordx4 v[32:33], v[16:19], off
	s_nop 1
	v_and_b32_e32 v17, 0xffff0000, v20
	v_mul_f32_e32 v16, v181, v210
	v_mul_f32_e32 v17, v183, v17
	v_lshlrev_b32_e32 v18, 16, v21
	v_and_b32_e32 v19, 0xffff0000, v21
	v_mul_f32_e32 v18, v185, v18
	v_mul_f32_e32 v19, v187, v19
	v_lshlrev_b32_e32 v20, 16, v22
	v_and_b32_e32 v21, 0xffff0000, v22
	v_lshlrev_b32_e32 v22, 16, v23
	v_and_b32_e32 v23, 0xffff0000, v23
	v_cvt_pk_bf16_f32 v16, v16, v17
	v_cvt_pk_bf16_f32 v17, v18, v19
	v_mul_f32_e32 v20, v182, v20
	v_mul_f32_e32 v21, v184, v21
	v_mul_f32_e32 v22, v186, v22
	v_mul_f32_e32 v23, v202, v23
	v_cvt_pk_bf16_f32 v18, v20, v21
	v_cvt_pk_bf16_f32 v19, v22, v23
	global_store_dwordx4 v[32:33], v[16:19], off offset:256
	v_mul_f32_e32 v22, 0x3d000000, v143
	v_mul_f32_e32 v23, 0x3d000000, v139
	v_mad_i64_i32 v[16:17], s[22:23], v203, s38, v[12:13]
	v_mul_f32_e32 v18, 0x3d000000, v142
	v_mul_f32_e32 v19, 0x3d000000, v138
	v_lshl_add_u64 v[20:21], v[16:17], 0, v[10:11]
	v_lshlrev_b32_e32 v16, 16, v24
	v_and_b32_e32 v17, 0xffff0000, v24
	v_lshlrev_b32_e32 v24, 16, v26
	v_mul_f32_e32 v32, 0x3d000000, v144
	v_mul_f32_e32 v16, v18, v16
	v_lshlrev_b32_e32 v18, 16, v25
	v_mul_f32_e32 v19, v19, v24
	v_and_b32_e32 v24, 0xffff0000, v26
	v_add_co_u32_e32 v20, vcc, s40, v20
	v_mul_f32_e32 v33, 0x3d000000, v140
	v_mul_f32_e32 v138, 0x3d000000, v145
	v_mul_f32_e32 v139, 0x3d000000, v141
	v_mul_f32_e32 v17, v22, v17
	v_mul_f32_e32 v18, v32, v18
	v_and_b32_e32 v22, 0xffff0000, v25
	v_mul_f32_e32 v23, v23, v24
	v_lshlrev_b32_e32 v24, 16, v27
	v_and_b32_e32 v25, 0xffff0000, v27
	v_cvt_pk_bf16_f32 v16, v16, v17
	v_addc_co_u32_e32 v21, vcc, 0, v21, vcc
	v_mul_f32_e32 v22, v138, v22
	v_mul_f32_e32 v24, v33, v24
	v_mul_f32_e32 v25, v139, v25
	v_cvt_pk_bf16_f32 v17, v18, v22
	v_cvt_pk_bf16_f32 v18, v19, v23
	v_cvt_pk_bf16_f32 v19, v24, v25
	global_store_dwordx4 v[20:21], v[16:19], off
	v_lshlrev_b32_e32 v26, 16, v28
	v_mul_f32_e32 v22, 0x3d000000, v136
	v_mul_f32_e32 v16, 0x3d000000, v134
	v_mul_f32_e32 v18, 0x3d000000, v135
	v_mul_f32_e32 v16, v16, v26
	v_and_b32_e32 v26, 0xffff0000, v28
	v_mul_f32_e32 v18, v18, v26
	v_lshlrev_b32_e32 v26, 16, v29
	v_mul_f32_e32 v24, 0x3d000000, v137
	v_mul_f32_e32 v22, v22, v26
	v_and_b32_e32 v26, 0xffff0000, v29
	v_mul_f32_e32 v17, 0x3d000000, v130
	v_mul_f32_e32 v24, v24, v26
	v_lshlrev_b32_e32 v26, 16, v30
	v_mul_f32_e32 v19, 0x3d000000, v131
	v_mul_f32_e32 v26, v17, v26
	v_and_b32_e32 v17, 0xffff0000, v30
	v_mul_f32_e32 v23, 0x3d000000, v132
	v_mul_f32_e32 v19, v19, v17
	v_lshlrev_b32_e32 v17, 16, v31
	v_mul_f32_e32 v25, 0x3d000000, v133
	v_mul_f32_e32 v23, v23, v17
	v_and_b32_e32 v17, 0xffff0000, v31
	v_mul_f32_e32 v25, v25, v17
	v_cvt_pk_bf16_f32 v16, v16, v18
	v_cvt_pk_bf16_f32 v17, v22, v24
	v_cvt_pk_bf16_f32 v18, v26, v19
	v_cvt_pk_bf16_f32 v19, v23, v25
	global_store_dwordx4 v[20:21], v[16:19], off offset:256
	v_mul_f32_e32 v24, 0x3d000000, v128
	v_mul_f32_e32 v23, 0x3d000000, v123
	v_mad_i64_i32 v[16:17], s[22:23], v204, s38, v[12:13]
	v_mul_f32_e32 v18, 0x3d000000, v126
	v_lshl_add_u64 v[20:21], v[16:17], 0, v[10:11]
	v_lshlrev_b32_e32 v16, 16, v146
	v_mul_f32_e32 v16, v18, v16
	v_lshlrev_b32_e32 v18, 16, v147
	v_mul_f32_e32 v19, 0x3d000000, v122
	v_mul_f32_e32 v18, v24, v18
	v_lshlrev_b32_e32 v24, 16, v148
	v_mul_f32_e32 v19, v19, v24
	v_and_b32_e32 v24, 0xffff0000, v148
	v_mul_f32_e32 v22, 0x3d000000, v127
	v_mul_f32_e32 v25, 0x3d000000, v124
	v_and_b32_e32 v17, 0xffff0000, v146
	v_mul_f32_e32 v23, v23, v24
	v_lshlrev_b32_e32 v24, 16, v149
	v_add_co_u32_e32 v20, vcc, s40, v20
	v_mul_f32_e32 v26, 0x3d000000, v129
	v_mul_f32_e32 v27, 0x3d000000, v125
	v_mul_f32_e32 v17, v22, v17
	v_and_b32_e32 v22, 0xffff0000, v147
	v_mul_f32_e32 v24, v25, v24
	v_and_b32_e32 v25, 0xffff0000, v149
	v_cvt_pk_bf16_f32 v16, v16, v17
	v_addc_co_u32_e32 v21, vcc, 0, v21, vcc
	v_mul_f32_e32 v22, v26, v22
	v_mul_f32_e32 v25, v27, v25
	v_cvt_pk_bf16_f32 v17, v18, v22
	v_cvt_pk_bf16_f32 v18, v19, v23
	v_cvt_pk_bf16_f32 v19, v24, v25
	global_store_dwordx4 v[20:21], v[16:19], off
	v_lshlrev_b32_e32 v26, 16, v150
	v_mul_f32_e32 v22, 0x3d000000, v120
	v_mul_f32_e32 v16, 0x3d000000, v118
	v_mul_f32_e32 v18, 0x3d000000, v119
	v_mul_f32_e32 v16, v16, v26
	v_and_b32_e32 v26, 0xffff0000, v150
	v_mul_f32_e32 v18, v18, v26
	v_lshlrev_b32_e32 v26, 16, v151
	v_mul_f32_e32 v24, 0x3d000000, v121
	v_mul_f32_e32 v22, v22, v26
	v_and_b32_e32 v26, 0xffff0000, v151
	v_mul_f32_e32 v17, 0x3d000000, v114
	v_mul_f32_e32 v24, v24, v26
	v_lshlrev_b32_e32 v26, 16, v152
	v_mul_f32_e32 v19, 0x3d000000, v115
	v_mul_f32_e32 v26, v17, v26
	v_and_b32_e32 v17, 0xffff0000, v152
	v_mul_f32_e32 v23, 0x3d000000, v116
	v_mul_f32_e32 v19, v19, v17
	v_lshlrev_b32_e32 v17, 16, v153
	v_mul_f32_e32 v25, 0x3d000000, v117
	v_mul_f32_e32 v23, v23, v17
	v_and_b32_e32 v17, 0xffff0000, v153
	v_mul_f32_e32 v25, v25, v17
	v_cvt_pk_bf16_f32 v16, v16, v18
	v_cvt_pk_bf16_f32 v17, v22, v24
	v_cvt_pk_bf16_f32 v18, v26, v19
	v_cvt_pk_bf16_f32 v19, v23, v25
	global_store_dwordx4 v[20:21], v[16:19], off offset:256
	v_mul_f32_e32 v22, 0x3d000000, v111
	v_mul_f32_e32 v24, 0x3d000000, v112
	v_mad_i64_i32 v[16:17], s[22:23], v205, s38, v[12:13]
	v_lshl_add_u64 v[20:21], v[16:17], 0, v[10:11]
	v_lshlrev_b32_e32 v16, 16, v6
	v_and_b32_e32 v6, 0xffff0000, v6
	v_mul_f32_e32 v29, v22, v6
	v_lshlrev_b32_e32 v6, 16, v7
	v_mul_f32_e32 v26, 0x3d000000, v113
	v_mul_f32_e32 v24, v24, v6
	v_and_b32_e32 v6, 0xffff0000, v7
	v_mul_f32_e32 v19, 0x3d000000, v106
	v_mul_f32_e32 v26, v26, v6
	v_lshlrev_b32_e32 v6, 16, v8
	v_mul_f32_e32 v23, 0x3d000000, v107
	v_mul_f32_e32 v30, v19, v6
	v_and_b32_e32 v6, 0xffff0000, v8
	v_mul_f32_e32 v25, 0x3d000000, v108
	v_mul_f32_e32 v8, v23, v6
	v_lshlrev_b32_e32 v6, 16, v9
	v_add_u32_e32 v32, 0x80, v180
	v_mul_f32_e32 v25, v25, v6
	v_mad_i64_i32 v[6:7], s[22:23], v32, s38, v[14:15]
	v_add_co_u32_e32 v22, vcc, s39, v6
	v_mul_f32_e32 v18, 0x3d000000, v110
	s_nop 0
	v_addc_co_u32_e32 v23, vcc, 0, v7, vcc
	v_mul_f32_e32 v27, 0x3d000000, v109
	v_mul_f32_e32 v28, v18, v16
	global_load_dwordx4 v[16:19], v[22:23], off nt
	v_and_b32_e32 v6, 0xffff0000, v9
	v_add_co_u32_e32 v20, vcc, s40, v20
	v_mul_f32_e32 v9, v27, v6
	v_cvt_pk_bf16_f32 v6, v28, v29
	s_nop 0
	v_addc_co_u32_e32 v21, vcc, 0, v21, vcc
	v_cvt_pk_bf16_f32 v7, v24, v26
	v_cvt_pk_bf16_f32 v8, v30, v8
	v_cvt_pk_bf16_f32 v9, v25, v9
	global_store_dwordx4 v[20:21], v[6:9], off
	v_lshlrev_b32_e32 v28, 16, v2
	v_mul_f32_e32 v24, 0x3d000000, v104
	v_mul_f32_e32 v6, 0x3d000000, v102
	v_mul_f32_e32 v28, v6, v28
	v_lshlrev_b32_e32 v6, 16, v3
	v_mul_f32_e32 v7, 0x3d000000, v98
	v_mul_f32_e32 v8, 0x3d000000, v103
	v_mul_f32_e32 v9, 0x3d000000, v99
	v_mul_f32_e32 v26, 0x3d000000, v105
	v_and_b32_e32 v2, 0xffff0000, v2
	v_mul_f32_e32 v24, v24, v6
	v_and_b32_e32 v3, 0xffff0000, v3
	v_lshlrev_b32_e32 v6, 16, v4
	v_and_b32_e32 v4, 0xffff0000, v4
	v_mul_f32_e32 v2, v8, v2
	v_mul_f32_e32 v3, v26, v3
	v_mul_f32_e32 v26, v7, v6
	v_mul_f32_e32 v4, v9, v4
	global_load_dwordx4 v[6:9], v[22:23], off offset:256 nt
	v_mul_f32_e32 v27, 0x3d000000, v101
	v_lshlrev_b32_e32 v29, 16, v5
	v_and_b32_e32 v5, 0xffff0000, v5
	v_mul_f32_e32 v25, 0x3d000000, v100
	v_mul_f32_e32 v5, v27, v5
	v_cvt_pk_bf16_f32 v2, v28, v2
	v_cvt_pk_bf16_f32 v3, v24, v3
	v_add_u32_e32 v106, 0x90, v180
	v_mul_f32_e32 v22, v25, v29
	v_cvt_pk_bf16_f32 v4, v26, v4
	v_cvt_pk_bf16_f32 v5, v22, v5
	global_store_dwordx4 v[20:21], v[2:5], off offset:256
	v_add_u32_e32 v107, 0xa0, v180
	v_add_u32_e32 v108, 0xb0, v180
	v_mad_i64_i32 v[2:3], s[22:23], v106, s38, v[14:15]
	v_add_co_u32_e32 v2, vcc, s39, v2
	s_nop 1
	v_addc_co_u32_e32 v3, vcc, 0, v3, vcc
	global_load_dwordx4 v[20:23], v[2:3], off nt
	global_load_dwordx4 v[24:27], v[2:3], off offset:256 nt
	v_mad_i64_i32 v[2:3], s[22:23], v107, s38, v[14:15]
	v_add_co_u32_e32 v2, vcc, s39, v2
	s_nop 1
	v_addc_co_u32_e32 v3, vcc, 0, v3, vcc
	global_load_dwordx4 v[28:31], v[2:3], off nt
	global_load_dwordx4 v[98:101], v[2:3], off offset:256 nt
	v_mad_i64_i32 v[2:3], s[22:23], v108, s38, v[14:15]
	v_add_co_u32_e32 v2, vcc, s39, v2
	v_mad_i64_i32 v[14:15], s[22:23], v32, s38, v[12:13]
	s_nop 0
	v_addc_co_u32_e32 v3, vcc, 0, v3, vcc
	global_load_dwordx4 v[102:105], v[2:3], off nt
	s_nop 0
	global_load_dwordx4 v[2:5], v[2:3], off offset:256 nt
	v_lshl_add_u64 v[32:33], v[14:15], 0, v[10:11]
	s_waitcnt vmcnt(9)
	v_lshlrev_b32_e32 v14, 16, v16
	v_mul_f32_e32 v14, v94, v14
	v_and_b32_e32 v15, 0xffff0000, v16
	v_lshlrev_b32_e32 v16, 16, v17
	v_lshlrev_b32_e32 v94, 16, v18
	v_and_b32_e32 v18, 0xffff0000, v18
	v_mul_f32_e32 v15, v95, v15
	v_mul_f32_e32 v16, v96, v16
	v_and_b32_e32 v17, 0xffff0000, v17
	v_mul_f32_e32 v18, v91, v18
	v_lshlrev_b32_e32 v91, 16, v19
	v_and_b32_e32 v19, 0xffff0000, v19
	v_mul_f32_e32 v17, v97, v17
	v_mul_f32_e32 v90, v90, v94
	v_mul_f32_e32 v19, v93, v19
	v_cvt_pk_bf16_f32 v14, v14, v15
	v_cvt_pk_bf16_f32 v15, v16, v17
	v_cvt_pk_bf16_f32 v16, v90, v18
	v_add_co_u32_e32 v18, vcc, s40, v32
	v_mul_f32_e32 v91, v92, v91
	v_cvt_pk_bf16_f32 v17, v91, v19
	s_nop 0
	v_addc_co_u32_e32 v19, vcc, 0, v33, vcc
	global_store_dwordx4 v[18:19], v[14:17], off
	v_mul_f32_e32 v33, 0x3d000000, v84
	v_mul_f32_e32 v32, 0x3d000000, v88
	v_mul_f32_e32 v16, 0x3d000000, v87
	v_mul_f32_e32 v15, 0x3d000000, v82
	v_mul_f32_e32 v17, 0x3d000000, v83
	s_waitcnt vmcnt(8)
	v_lshlrev_b32_e32 v84, 16, v6
	v_and_b32_e32 v6, 0xffff0000, v6
	v_mul_f32_e32 v6, v16, v6
	v_lshlrev_b32_e32 v16, 16, v7
	v_mul_f32_e32 v82, 0x3d000000, v89
	v_mul_f32_e32 v16, v32, v16
	v_and_b32_e32 v7, 0xffff0000, v7
	v_lshlrev_b32_e32 v32, 16, v8
	v_and_b32_e32 v8, 0xffff0000, v8
	v_mul_f32_e32 v14, 0x3d000000, v86
	v_mul_f32_e32 v83, 0x3d000000, v85
	v_mul_f32_e32 v7, v82, v7
	v_mul_f32_e32 v8, v17, v8
	v_lshlrev_b32_e32 v17, 16, v9
	v_and_b32_e32 v9, 0xffff0000, v9
	v_mul_f32_e32 v14, v14, v84
	v_mul_f32_e32 v9, v83, v9
	v_cvt_pk_bf16_f32 v6, v14, v6
	v_cvt_pk_bf16_f32 v7, v16, v7
	v_mul_f32_e32 v15, v15, v32
	v_mul_f32_e32 v17, v33, v17
	v_cvt_pk_bf16_f32 v8, v15, v8
	v_cvt_pk_bf16_f32 v9, v17, v9
	global_store_dwordx4 v[18:19], v[6:9], off offset:256
	v_mul_f32_e32 v18, 0x3d000000, v80
	v_mul_f32_e32 v17, 0x3d000000, v75
	v_mad_i64_i32 v[6:7], s[22:23], v106, s38, v[12:13]
	v_mul_f32_e32 v8, 0x3d000000, v78
	v_lshl_add_u64 v[14:15], v[6:7], 0, v[10:11]
	s_waitcnt vmcnt(7)
	v_lshlrev_b32_e32 v6, 16, v20
	v_mul_f32_e32 v6, v8, v6
	v_lshlrev_b32_e32 v8, 16, v21
	v_mul_f32_e32 v9, 0x3d000000, v74
	v_mul_f32_e32 v8, v18, v8
	v_lshlrev_b32_e32 v18, 16, v22
	v_mul_f32_e32 v9, v9, v18
	v_and_b32_e32 v18, 0xffff0000, v22
	v_mul_f32_e32 v16, 0x3d000000, v79
	v_mul_f32_e32 v19, 0x3d000000, v76
	v_and_b32_e32 v7, 0xffff0000, v20
	v_mul_f32_e32 v17, v17, v18
	v_lshlrev_b32_e32 v18, 16, v23
	v_add_co_u32_e32 v14, vcc, s40, v14
	v_mul_f32_e32 v32, 0x3d000000, v81
	v_mul_f32_e32 v33, 0x3d000000, v77
	v_mul_f32_e32 v7, v16, v7
	v_and_b32_e32 v16, 0xffff0000, v21
	v_mul_f32_e32 v18, v19, v18
	v_and_b32_e32 v19, 0xffff0000, v23
	v_cvt_pk_bf16_f32 v6, v6, v7
	v_addc_co_u32_e32 v15, vcc, 0, v15, vcc
	v_mul_f32_e32 v16, v32, v16
	v_mul_f32_e32 v19, v33, v19
	v_cvt_pk_bf16_f32 v7, v8, v16
	v_cvt_pk_bf16_f32 v8, v9, v17
	v_cvt_pk_bf16_f32 v9, v18, v19
	global_store_dwordx4 v[14:15], v[6:9], off
	s_waitcnt vmcnt(7)
	v_lshlrev_b32_e32 v20, 16, v24
	v_mul_f32_e32 v16, 0x3d000000, v72
	v_mul_f32_e32 v6, 0x3d000000, v70
	v_mul_f32_e32 v8, 0x3d000000, v71
	v_mul_f32_e32 v6, v6, v20
	v_and_b32_e32 v20, 0xffff0000, v24
	v_mul_f32_e32 v8, v8, v20
	v_lshlrev_b32_e32 v20, 16, v25
	v_mul_f32_e32 v18, 0x3d000000, v73
	v_mul_f32_e32 v16, v16, v20
	v_and_b32_e32 v20, 0xffff0000, v25
	v_mul_f32_e32 v7, 0x3d000000, v66
	v_mul_f32_e32 v18, v18, v20
	v_lshlrev_b32_e32 v20, 16, v26
	v_mul_f32_e32 v9, 0x3d000000, v67
	v_mul_f32_e32 v20, v7, v20
	v_and_b32_e32 v7, 0xffff0000, v26
	v_mul_f32_e32 v17, 0x3d000000, v68
	v_mul_f32_e32 v9, v9, v7
	v_lshlrev_b32_e32 v7, 16, v27
	v_mul_f32_e32 v19, 0x3d000000, v69
	v_mul_f32_e32 v17, v17, v7
	v_and_b32_e32 v7, 0xffff0000, v27
	v_mul_f32_e32 v19, v19, v7
	v_cvt_pk_bf16_f32 v6, v6, v8
	v_cvt_pk_bf16_f32 v7, v16, v18
	v_cvt_pk_bf16_f32 v8, v20, v9
	v_cvt_pk_bf16_f32 v9, v17, v19
	global_store_dwordx4 v[14:15], v[6:9], off offset:256
	v_mul_f32_e32 v18, 0x3d000000, v64
	v_mul_f32_e32 v17, 0x3d000000, v59
	v_mad_i64_i32 v[6:7], s[22:23], v107, s38, v[12:13]
	v_mul_f32_e32 v8, 0x3d000000, v62
	v_lshl_add_u64 v[14:15], v[6:7], 0, v[10:11]
	s_waitcnt vmcnt(7)
	v_lshlrev_b32_e32 v6, 16, v28
	v_mul_f32_e32 v6, v8, v6
	v_lshlrev_b32_e32 v8, 16, v29
	v_mul_f32_e32 v9, 0x3d000000, v58
	v_mul_f32_e32 v8, v18, v8
	v_lshlrev_b32_e32 v18, 16, v30
	v_mul_f32_e32 v9, v9, v18
	v_and_b32_e32 v18, 0xffff0000, v30
	v_mul_f32_e32 v16, 0x3d000000, v63
	v_mul_f32_e32 v19, 0x3d000000, v60
	v_and_b32_e32 v7, 0xffff0000, v28
	v_mul_f32_e32 v17, v17, v18
	v_lshlrev_b32_e32 v18, 16, v31
	v_add_co_u32_e32 v14, vcc, s40, v14
	v_mul_f32_e32 v20, 0x3d000000, v65
	v_mul_f32_e32 v21, 0x3d000000, v61
	v_mul_f32_e32 v7, v16, v7
	v_and_b32_e32 v16, 0xffff0000, v29
	v_mul_f32_e32 v18, v19, v18
	v_and_b32_e32 v19, 0xffff0000, v31
	v_cvt_pk_bf16_f32 v6, v6, v7
	v_addc_co_u32_e32 v15, vcc, 0, v15, vcc
	v_mul_f32_e32 v16, v20, v16
	v_mul_f32_e32 v19, v21, v19
	v_cvt_pk_bf16_f32 v7, v8, v16
	v_cvt_pk_bf16_f32 v8, v9, v17
	v_cvt_pk_bf16_f32 v9, v18, v19
	global_store_dwordx4 v[14:15], v[6:9], off
	s_waitcnt vmcnt(7)
	v_lshlrev_b32_e32 v20, 16, v98
	v_mul_f32_e32 v16, 0x3d000000, v56
	v_mul_f32_e32 v6, 0x3d000000, v54
	v_mul_f32_e32 v8, 0x3d000000, v55
	v_mul_f32_e32 v6, v6, v20
	v_and_b32_e32 v20, 0xffff0000, v98
	v_mul_f32_e32 v8, v8, v20
	v_lshlrev_b32_e32 v20, 16, v99
	v_mul_f32_e32 v18, 0x3d000000, v57
	v_mul_f32_e32 v16, v16, v20
	v_and_b32_e32 v20, 0xffff0000, v99
	v_mul_f32_e32 v7, 0x3d000000, v50
	v_mul_f32_e32 v18, v18, v20
	v_lshlrev_b32_e32 v20, 16, v100
	v_mul_f32_e32 v9, 0x3d000000, v51
	v_mul_f32_e32 v20, v7, v20
	v_and_b32_e32 v7, 0xffff0000, v100
	v_mul_f32_e32 v17, 0x3d000000, v52
	v_mul_f32_e32 v9, v9, v7
	v_lshlrev_b32_e32 v7, 16, v101
	v_mul_f32_e32 v19, 0x3d000000, v53
	v_mul_f32_e32 v17, v17, v7
	v_and_b32_e32 v7, 0xffff0000, v101
	v_mul_f32_e32 v19, v19, v7
	v_cvt_pk_bf16_f32 v6, v6, v8
	v_cvt_pk_bf16_f32 v7, v16, v18
	v_cvt_pk_bf16_f32 v8, v20, v9
	v_cvt_pk_bf16_f32 v9, v17, v19
	global_store_dwordx4 v[14:15], v[6:9], off offset:256
	v_mul_f32_e32 v14, 0x3d000000, v48
	v_mul_f32_e32 v15, 0x3d000000, v44
	v_mad_i64_i32 v[6:7], s[22:23], v108, s38, v[12:13]
	v_mul_f32_e32 v8, 0x3d000000, v46
	v_lshl_add_u64 v[10:11], v[6:7], 0, v[10:11]
	s_waitcnt vmcnt(7)
	v_lshlrev_b32_e32 v6, 16, v102
	v_mul_f32_e32 v6, v8, v6
	v_lshlrev_b32_e32 v8, 16, v103
	v_mul_f32_e32 v9, 0x3d000000, v42
	v_mul_f32_e32 v8, v14, v8
	v_lshlrev_b32_e32 v14, 16, v104
	v_mul_f32_e32 v12, 0x3d000000, v47
	v_mul_f32_e32 v13, 0x3d000000, v43
	v_and_b32_e32 v7, 0xffff0000, v102
	v_mul_f32_e32 v9, v9, v14
	v_and_b32_e32 v14, 0xffff0000, v104
	v_mul_f32_e32 v16, 0x3d000000, v49
	v_mul_f32_e32 v7, v12, v7
	v_and_b32_e32 v12, 0xffff0000, v103
	v_mul_f32_e32 v13, v13, v14
	v_lshlrev_b32_e32 v14, 16, v105
	v_add_co_u32_e32 v10, vcc, s40, v10
	v_mul_f32_e32 v17, 0x3d000000, v45
	v_mul_f32_e32 v12, v16, v12
	v_mul_f32_e32 v14, v15, v14
	v_and_b32_e32 v15, 0xffff0000, v105
	v_cvt_pk_bf16_f32 v6, v6, v7
	v_cvt_pk_bf16_f32 v7, v8, v12
	v_cvt_pk_bf16_f32 v8, v9, v13
	v_addc_co_u32_e32 v11, vcc, 0, v11, vcc
	v_mul_f32_e32 v15, v17, v15
	v_cvt_pk_bf16_f32 v9, v14, v15
	global_store_dwordx4 v[10:11], v[6:9], off
	s_waitcnt vmcnt(7)
	v_lshlrev_b32_e32 v16, 16, v2
	v_and_b32_e32 v2, 0xffff0000, v2
	v_mul_f32_e32 v8, 0x3d000000, v39
	v_mul_f32_e32 v12, 0x3d000000, v40
	v_mul_f32_e32 v2, v8, v2
	v_lshlrev_b32_e32 v8, 16, v3
	v_mul_f32_e32 v9, 0x3d000000, v35
	v_mul_f32_e32 v8, v12, v8
	v_lshlrev_b32_e32 v12, 16, v4
	v_and_b32_e32 v4, 0xffff0000, v4
	v_mul_f32_e32 v14, 0x3d000000, v41
	v_mul_f32_e32 v15, 0x3d000000, v37
	v_and_b32_e32 v3, 0xffff0000, v3
	v_mul_f32_e32 v4, v9, v4
	v_lshlrev_b32_e32 v9, 16, v5
	v_and_b32_e32 v5, 0xffff0000, v5
	v_mul_f32_e32 v6, 0x3d000000, v38
	v_mul_f32_e32 v7, 0x3d000000, v34
	v_mul_f32_e32 v13, 0x3d000000, v36
	v_mul_f32_e32 v3, v14, v3
	v_mul_f32_e32 v5, v15, v5
	s_andn2_b64 vcc, exec, s[0:1]
	s_mov_b64 s[0:1], -1
	v_mul_f32_e32 v6, v6, v16
	v_mul_f32_e32 v7, v7, v12
	v_mul_f32_e32 v9, v13, v9
	v_cvt_pk_bf16_f32 v2, v6, v2
	v_cvt_pk_bf16_f32 v3, v8, v3
	v_cvt_pk_bf16_f32 v4, v7, v4
	v_cvt_pk_bf16_f32 v5, v9, v5
	global_store_dwordx4 v[10:11], v[2:5], off offset:256
	s_cbranch_vccnz .LBB0_984
	s_andn2_b64 vcc, exec, s[6:7]
	s_cbranch_vccnz .LBB0_983
	s_barrier
	s_branch .LBB0_983

.LBB0_1019:
	v_lshl_or_b32 v180, s42, 8, v192
	v_readlane_b32 s20, v255, 4
	v_ashrrev_i32_e32 v181, 31, v180
	v_readlane_b32 s21, v255, 5
	v_lshl_add_u32 v186, s16, 8, v196
	s_nop 15
	s_nop 15
	v_mul_f32_e32 v187, 0x3d000000, v158
	v_lshl_add_u64 v[184:185], v[180:181], 1, s[20:21]
	v_mad_i64_i32 v[2:3], s[18:19], v186, s40, v[184:185]
	v_add_co_u32_e32 v4, vcc, 0x8000, v2
	v_mul_f32_e32 v191, 0x3d000000, v154
	s_nop 0
	v_addc_co_u32_e32 v5, vcc, 0, v3, vcc
	v_add_co_u32_e32 v2, vcc, 0x1000, v2
	global_load_dwordx4 v[198:201], v[4:5], off nt
	s_nop 0
	v_addc_co_u32_e32 v3, vcc, 0, v3, vcc
	global_load_dwordx4 v[202:205], v[2:3], off nt
	v_mul_f32_e32 v194, 0x3d000000, v159
	v_mul_f32_e32 v195, 0x3d000000, v155
	v_mul_f32_e32 v197, 0x3d000000, v160
	v_mul_f32_e32 v218, 0x3d000000, v156
	v_mul_f32_e32 v219, 0x3d000000, v161
	v_mul_f32_e32 v220, 0x3d000000, v157
	global_load_dwordx4 v[154:157], v[4:5], off offset:256 nt
	global_load_dwordx4 v[158:161], v[2:3], off offset:256 nt
	v_or_b32_e32 v221, 16, v186
	v_mad_i64_i32 v[6:7], s[18:19], v221, s40, v[184:185]
	v_add_co_u32_e32 v4, vcc, 0x8000, v6
	v_or_b32_e32 v226, 32, v186
	s_nop 0
	v_addc_co_u32_e32 v5, vcc, 0, v7, vcc
	v_add_co_u32_e32 v2, vcc, 0x1000, v6
	global_load_dwordx4 v[206:209], v[4:5], off nt
	global_load_dwordx4 v[210:213], v[4:5], off offset:256 nt
	v_addc_co_u32_e32 v3, vcc, 0, v7, vcc
	global_load_dwordx4 v[214:217], v[2:3], off nt
	global_load_dwordx4 v[222:225], v[2:3], off offset:256 nt
	v_mad_i64_i32 v[8:9], s[18:19], v226, s40, v[184:185]
	v_add_co_u32_e32 v4, vcc, 0x8000, v8
	v_or_b32_e32 v227, 48, v186
	s_nop 0
	v_addc_co_u32_e32 v5, vcc, 0, v9, vcc
	v_add_co_u32_e32 v2, vcc, 0x1000, v8
	global_load_dwordx4 v[30:33], v[4:5], off nt
	global_load_dwordx4 v[22:25], v[4:5], off offset:256 nt
	v_addc_co_u32_e32 v3, vcc, 0, v9, vcc
	global_load_dwordx4 v[26:29], v[2:3], off nt
	global_load_dwordx4 v[18:21], v[2:3], off offset:256 nt
	v_mad_i64_i32 v[10:11], s[18:19], v227, s40, v[184:185]
	v_add_co_u32_e32 v4, vcc, 0x8000, v10
	v_mul_f32_e32 v150, 0x3d000000, v150
	s_nop 0
	v_addc_co_u32_e32 v5, vcc, 0, v11, vcc
	v_add_co_u32_e32 v2, vcc, 0x1000, v10
	v_mul_f32_e32 v151, 0x3d000000, v151
	s_nop 0
	v_addc_co_u32_e32 v3, vcc, 0, v11, vcc
	global_load_dwordx4 v[14:17], v[4:5], off nt
	global_load_dwordx4 v[6:9], v[4:5], off offset:256 nt
	global_load_dwordx4 v[10:13], v[2:3], off nt
	s_nop 0
	global_load_dwordx4 v[2:5], v[2:3], off offset:256 nt
	v_mul_f32_e32 v152, 0x3d000000, v152
	v_mul_f32_e32 v153, 0x3d000000, v153
	v_mul_f32_e32 v146, 0x3d000000, v146
	v_mul_f32_e32 v147, 0x3d000000, v147
	v_mul_f32_e32 v148, 0x3d000000, v148
	v_mov_b64_e32 v[182:183], s[20:21]
	v_mul_f32_e32 v149, 0x3d000000, v149
	v_mul_f32_e32 v142, 0x3d000000, v142
	v_mul_f32_e32 v143, 0x3d000000, v143
	v_mul_f32_e32 v144, 0x3d000000, v144
	v_mul_f32_e32 v145, 0x3d000000, v145
	v_mul_f32_e32 v138, 0x3d000000, v138
	v_mul_f32_e32 v139, 0x3d000000, v139
	v_mul_f32_e32 v134, 0x3d000000, v134
	v_mul_f32_e32 v140, 0x3d000000, v140
	v_mul_f32_e32 v135, 0x3d000000, v135
	v_mul_f32_e32 v141, 0x3d000000, v141
	v_mul_f32_e32 v136, 0x3d000000, v136
	v_mul_f32_e32 v137, 0x3d000000, v137
	v_mul_f32_e32 v130, 0x3d000000, v130
	v_mul_f32_e32 v131, 0x3d000000, v131
	v_mul_f32_e32 v132, 0x3d000000, v132
	v_mul_f32_e32 v133, 0x3d000000, v133
	v_mul_f32_e32 v126, 0x3d000000, v126
	v_mul_f32_e32 v127, 0x3d000000, v127
	v_mul_f32_e32 v129, 0x3d000000, v129
	v_mul_f32_e32 v122, 0x3d000000, v122
	v_mul_f32_e32 v123, 0x3d000000, v123
	s_waitcnt vmcnt(0)
	v_lshlrev_b32_e32 v228, 16, v198
	v_and_b32_e32 v198, 0xffff0000, v198
	v_lshlrev_b32_e32 v229, 16, v199
	v_lshlrev_b32_e32 v232, 16, v202
	v_fmac_f32_e32 v232, v187, v228
	v_and_b32_e32 v187, 0xffff0000, v202
	v_fmac_f32_e32 v187, v194, v198
	v_lshlrev_b32_e32 v198, 16, v203
	v_and_b32_e32 v199, 0xffff0000, v199
	v_fmac_f32_e32 v198, v197, v229
	v_and_b32_e32 v197, 0xffff0000, v203
	v_lshlrev_b32_e32 v230, 16, v200
	v_fmac_f32_e32 v197, v219, v199
	v_lshlrev_b32_e32 v199, 16, v204
	v_and_b32_e32 v200, 0xffff0000, v200
	v_fmac_f32_e32 v199, v191, v230
	v_and_b32_e32 v191, 0xffff0000, v204
	v_fmac_f32_e32 v191, v195, v200
	v_mov_b32_e32 v195, 0
	v_cvt_pk_fp8_f32 v195, v199, v191
	v_mov_b32_e32 v194, 0
	v_lshlrev_b32_e32 v231, 16, v201
	v_and_b32_e32 v201, 0xffff0000, v201
	v_lshlrev_b32_e32 v200, 16, v205
	v_cvt_pk_fp8_f32 v194, v232, v187
	v_and_b32_e32 v187, 0xffff0000, v205
	v_fmac_f32_e32 v200, v218, v231
	v_fmac_f32_e32 v187, v220, v201
	v_cvt_pk_fp8_f32 v195, v200, v187 op_sel:[0,0,1]
	v_lshlrev_b32_e32 v187, 16, v154
	v_lshlrev_b32_e32 v201, 16, v158
	v_and_b32_e32 v154, 0xffff0000, v154
	v_fmac_f32_e32 v201, v150, v187
	v_and_b32_e32 v150, 0xffff0000, v158
	v_lshlrev_b32_e32 v191, 16, v155
	v_fmac_f32_e32 v150, v151, v154
	v_lshlrev_b32_e32 v151, 16, v159
	v_and_b32_e32 v155, 0xffff0000, v155
	v_fmac_f32_e32 v151, v152, v191
	v_and_b32_e32 v152, 0xffff0000, v159
	v_cvt_pk_fp8_f32 v194, v198, v197 op_sel:[0,0,1]
	v_lshlrev_b32_e32 v197, 16, v156
	v_and_b32_e32 v156, 0xffff0000, v156
	v_fmac_f32_e32 v152, v153, v155
	v_lshlrev_b32_e32 v153, 16, v160
	v_and_b32_e32 v154, 0xffff0000, v160
	v_fmac_f32_e32 v153, v146, v197
	v_fmac_f32_e32 v154, v147, v156
	v_mov_b32_e32 v146, 0
	v_mov_b32_e32 v147, 0
	v_cvt_pk_fp8_f32 v146, v201, v150
	v_cvt_pk_fp8_f32 v147, v153, v154
	v_lshlrev_b32_e32 v200, 16, v157
	v_lshlrev_b32_e32 v155, 16, v161
	v_and_b32_e32 v157, 0xffff0000, v157
	v_fmac_f32_e32 v155, v148, v200
	v_and_b32_e32 v148, 0xffff0000, v161
	v_mad_i64_i32 v[198:199], s[18:19], v186, s40, v[182:183]
	v_fmac_f32_e32 v148, v149, v157
	v_lshl_add_u64 v[198:199], v[198:199], 0, v[180:181]
	v_cvt_pk_fp8_f32 v146, v151, v152 op_sel:[0,0,1]
	v_cvt_pk_fp8_f32 v147, v155, v148 op_sel:[0,0,1]
	v_add_co_u32_e32 v148, vcc, s33, v198
	v_lshlrev_b32_e32 v154, 16, v214
	s_nop 0
	v_addc_co_u32_e32 v149, vcc, 0, v199, vcc
	global_store_dwordx2 v[148:149], v[194:195], off
	global_store_dwordx2 v[148:149], v[146:147], off offset:128
	v_lshlrev_b32_e32 v146, 16, v206
	v_and_b32_e32 v147, 0xffff0000, v206
	v_fmac_f32_e32 v154, v142, v146
	v_and_b32_e32 v142, 0xffff0000, v214
	v_lshlrev_b32_e32 v148, 16, v207
	v_fmac_f32_e32 v142, v143, v147
	v_lshlrev_b32_e32 v143, 16, v215
	v_and_b32_e32 v149, 0xffff0000, v207
	v_fmac_f32_e32 v143, v144, v148
	v_and_b32_e32 v144, 0xffff0000, v215
	v_lshlrev_b32_e32 v150, 16, v208
	v_fmac_f32_e32 v144, v145, v149
	v_lshlrev_b32_e32 v145, 16, v216
	v_fmac_f32_e32 v145, v138, v150
	v_mov_b32_e32 v138, 0
	v_cvt_pk_fp8_f32 v138, v154, v142
	v_and_b32_e32 v151, 0xffff0000, v208
	v_and_b32_e32 v146, 0xffff0000, v216
	v_fmac_f32_e32 v146, v139, v151
	v_mov_b32_e32 v139, 0
	v_cvt_pk_fp8_f32 v139, v145, v146
	v_lshlrev_b32_e32 v142, 16, v210
	v_lshlrev_b32_e32 v150, 16, v222
	v_lshlrev_b32_e32 v152, 16, v209
	v_lshlrev_b32_e32 v147, 16, v217
	v_cvt_pk_fp8_f32 v138, v143, v144 op_sel:[0,0,1]
	v_and_b32_e32 v143, 0xffff0000, v210
	v_fmac_f32_e32 v150, v134, v142
	v_and_b32_e32 v134, 0xffff0000, v222
	v_and_b32_e32 v153, 0xffff0000, v209
	v_fmac_f32_e32 v147, v140, v152
	v_and_b32_e32 v140, 0xffff0000, v217
	v_lshlrev_b32_e32 v144, 16, v211
	v_fmac_f32_e32 v134, v135, v143
	v_lshlrev_b32_e32 v135, 16, v223
	v_fmac_f32_e32 v140, v141, v153
	v_and_b32_e32 v145, 0xffff0000, v211
	v_fmac_f32_e32 v135, v136, v144
	v_and_b32_e32 v136, 0xffff0000, v223
	v_cvt_pk_fp8_f32 v139, v147, v140 op_sel:[0,0,1]
	v_lshlrev_b32_e32 v146, 16, v212
	v_and_b32_e32 v147, 0xffff0000, v212
	v_fmac_f32_e32 v136, v137, v145
	v_lshlrev_b32_e32 v137, 16, v224
	v_and_b32_e32 v142, 0xffff0000, v224
	v_fmac_f32_e32 v137, v130, v146
	v_fmac_f32_e32 v142, v131, v147
	v_mov_b32_e32 v130, 0
	v_mov_b32_e32 v131, 0
	v_cvt_pk_fp8_f32 v130, v150, v134
	v_cvt_pk_fp8_f32 v131, v137, v142
	v_lshlrev_b32_e32 v148, 16, v213
	v_lshlrev_b32_e32 v143, 16, v225
	v_and_b32_e32 v149, 0xffff0000, v213
	v_fmac_f32_e32 v143, v132, v148
	v_and_b32_e32 v132, 0xffff0000, v225
	v_mad_i64_i32 v[140:141], s[18:19], v221, s40, v[182:183]
	v_fmac_f32_e32 v132, v133, v149
	v_lshl_add_u64 v[140:141], v[140:141], 0, v[180:181]
	v_cvt_pk_fp8_f32 v130, v135, v136 op_sel:[0,0,1]
	v_cvt_pk_fp8_f32 v131, v143, v132 op_sel:[0,0,1]
	v_add_co_u32_e32 v132, vcc, s33, v140
	v_lshlrev_b32_e32 v134, 16, v26
	s_nop 0
	v_addc_co_u32_e32 v133, vcc, 0, v141, vcc
	global_store_dwordx2 v[132:133], v[138:139], off
	global_store_dwordx2 v[132:133], v[130:131], off offset:128
	v_lshlrev_b32_e32 v130, 16, v30
	v_and_b32_e32 v30, 0xffff0000, v30
	v_fmac_f32_e32 v134, v126, v130
	v_and_b32_e32 v126, 0xffff0000, v26
	v_lshlrev_b32_e32 v131, 16, v31
	v_and_b32_e32 v31, 0xffff0000, v31
	v_fmac_f32_e32 v126, v127, v30
	v_and_b32_e32 v127, 0xffff0000, v27
	v_lshlrev_b32_e32 v132, 16, v32
	v_and_b32_e32 v32, 0xffff0000, v32
	v_fmac_f32_e32 v127, v129, v31
	v_lshlrev_b32_e32 v31, 16, v28
	v_and_b32_e32 v28, 0xffff0000, v28
	v_mov_b32_e32 v26, 0
	v_lshlrev_b32_e32 v30, 16, v27
	v_fmac_f32_e32 v31, v122, v132
	v_fmac_f32_e32 v28, v123, v32
	v_cvt_pk_fp8_f32 v26, v134, v126
	v_mov_b32_e32 v27, 0
	v_cvt_pk_fp8_f32 v27, v31, v28
	v_mul_f32_e32 v128, 0x3d000000, v128
	v_mul_f32_e32 v124, 0x3d000000, v124
	v_mul_f32_e32 v125, 0x3d000000, v125
	v_lshlrev_b32_e32 v133, 16, v33
	v_and_b32_e32 v33, 0xffff0000, v33
	v_fmac_f32_e32 v30, v128, v131
	v_lshlrev_b32_e32 v32, 16, v29
	v_and_b32_e32 v28, 0xffff0000, v29
	v_fmac_f32_e32 v32, v124, v133
	v_fmac_f32_e32 v28, v125, v33
	v_cvt_pk_fp8_f32 v26, v30, v127 op_sel:[0,0,1]
	v_mul_f32_e32 v30, 0x3d000000, v118
	v_lshlrev_b32_e32 v118, 16, v22
	v_lshlrev_b32_e32 v122, 16, v18
	v_cvt_pk_fp8_f32 v27, v32, v28 op_sel:[0,0,1]
	v_mul_f32_e32 v32, 0x3d000000, v119
	v_and_b32_e32 v22, 0xffff0000, v22
	v_fmac_f32_e32 v122, v30, v118
	v_and_b32_e32 v30, 0xffff0000, v18
	v_mul_f32_e32 v33, 0x3d000000, v115
	v_mul_f32_e32 v115, 0x3d000000, v116
	v_mul_f32_e32 v116, 0x3d000000, v121
	v_lshlrev_b32_e32 v119, 16, v23
	v_and_b32_e32 v23, 0xffff0000, v23
	v_fmac_f32_e32 v30, v32, v22
	v_and_b32_e32 v32, 0xffff0000, v19
	v_mul_f32_e32 v31, 0x3d000000, v114
	v_mul_f32_e32 v114, 0x3d000000, v120
	v_lshlrev_b32_e32 v120, 16, v24
	v_and_b32_e32 v24, 0xffff0000, v24
	v_fmac_f32_e32 v32, v116, v23
	v_lshlrev_b32_e32 v23, 16, v20
	v_and_b32_e32 v20, 0xffff0000, v20
	v_lshlrev_b32_e32 v22, 16, v19
	v_fmac_f32_e32 v23, v31, v120
	v_fmac_f32_e32 v20, v33, v24
	v_mov_b32_e32 v18, 0
	v_mov_b32_e32 v19, 0
	v_cvt_pk_fp8_f32 v18, v122, v30
	v_cvt_pk_fp8_f32 v19, v23, v20
	v_mul_f32_e32 v117, 0x3d000000, v117
	v_lshlrev_b32_e32 v121, 16, v25
	v_and_b32_e32 v25, 0xffff0000, v25
	v_lshlrev_b32_e32 v24, 16, v21
	v_and_b32_e32 v20, 0xffff0000, v21
	v_mad_i64_i32 v[28:29], s[18:19], v226, s40, v[182:183]
	v_fmac_f32_e32 v22, v114, v119
	v_fmac_f32_e32 v24, v115, v121
	v_fmac_f32_e32 v20, v117, v25
	v_lshl_add_u64 v[28:29], v[28:29], 0, v[180:181]
	v_cvt_pk_fp8_f32 v18, v22, v32 op_sel:[0,0,1]
	v_cvt_pk_fp8_f32 v19, v24, v20 op_sel:[0,0,1]
	v_add_co_u32_e32 v20, vcc, s33, v28
	v_lshlrev_b32_e32 v30, 16, v10
	s_nop 0
	v_addc_co_u32_e32 v21, vcc, 0, v29, vcc
	global_store_dwordx2 v[20:21], v[26:27], off
	global_store_dwordx2 v[20:21], v[18:19], off offset:128
	v_mul_f32_e32 v18, 0x3d000000, v110
	v_lshlrev_b32_e32 v26, 16, v14
	v_mul_f32_e32 v20, 0x3d000000, v111
	v_and_b32_e32 v14, 0xffff0000, v14
	v_fmac_f32_e32 v30, v18, v26
	v_and_b32_e32 v18, 0xffff0000, v10
	v_mul_f32_e32 v24, 0x3d000000, v113
	v_lshlrev_b32_e32 v27, 16, v15
	v_and_b32_e32 v15, 0xffff0000, v15
	v_fmac_f32_e32 v18, v20, v14
	v_and_b32_e32 v20, 0xffff0000, v11
	v_mul_f32_e32 v19, 0x3d000000, v106
	v_mul_f32_e32 v21, 0x3d000000, v107
	v_lshlrev_b32_e32 v28, 16, v16
	v_and_b32_e32 v16, 0xffff0000, v16
	v_fmac_f32_e32 v20, v24, v15
	v_lshlrev_b32_e32 v15, 16, v12
	v_and_b32_e32 v12, 0xffff0000, v12
	v_mov_b32_e32 v10, 0
	v_lshlrev_b32_e32 v14, 16, v11
	v_fmac_f32_e32 v15, v19, v28
	v_fmac_f32_e32 v12, v21, v16
	v_cvt_pk_fp8_f32 v10, v30, v18
	v_mov_b32_e32 v11, 0
	v_cvt_pk_fp8_f32 v11, v15, v12
	v_mul_f32_e32 v22, 0x3d000000, v112
	v_mul_f32_e32 v23, 0x3d000000, v108
	v_mul_f32_e32 v25, 0x3d000000, v109
	v_lshlrev_b32_e32 v29, 16, v17
	v_and_b32_e32 v17, 0xffff0000, v17
	v_fmac_f32_e32 v14, v22, v27
	v_lshlrev_b32_e32 v16, 16, v13
	v_and_b32_e32 v12, 0xffff0000, v13
	v_fmac_f32_e32 v16, v23, v29
	v_fmac_f32_e32 v12, v25, v17
	v_cvt_pk_fp8_f32 v10, v14, v20 op_sel:[0,0,1]
	v_mul_f32_e32 v14, 0x3d000000, v102
	v_lshlrev_b32_e32 v22, 16, v6
	v_lshlrev_b32_e32 v26, 16, v2
	v_cvt_pk_fp8_f32 v11, v16, v12 op_sel:[0,0,1]
	v_mul_f32_e32 v16, 0x3d000000, v103
	v_and_b32_e32 v6, 0xffff0000, v6
	v_fmac_f32_e32 v26, v14, v22
	v_and_b32_e32 v14, 0xffff0000, v2
	v_mul_f32_e32 v20, 0x3d000000, v105
	v_lshlrev_b32_e32 v23, 16, v7
	v_and_b32_e32 v7, 0xffff0000, v7
	v_fmac_f32_e32 v14, v16, v6
	v_and_b32_e32 v16, 0xffff0000, v3
	v_mul_f32_e32 v15, 0x3d000000, v98
	v_mul_f32_e32 v17, 0x3d000000, v99
	v_lshlrev_b32_e32 v24, 16, v8
	v_and_b32_e32 v8, 0xffff0000, v8
	v_fmac_f32_e32 v16, v20, v7
	v_lshlrev_b32_e32 v7, 16, v4
	v_and_b32_e32 v4, 0xffff0000, v4
	v_lshlrev_b32_e32 v6, 16, v3
	v_fmac_f32_e32 v7, v15, v24
	v_fmac_f32_e32 v4, v17, v8
	v_mov_b32_e32 v2, 0
	v_mov_b32_e32 v3, 0
	v_cvt_pk_fp8_f32 v2, v26, v14
	v_cvt_pk_fp8_f32 v3, v7, v4
	v_mul_f32_e32 v18, 0x3d000000, v104
	v_mul_f32_e32 v19, 0x3d000000, v100
	v_mul_f32_e32 v21, 0x3d000000, v101
	v_lshlrev_b32_e32 v25, 16, v9
	v_and_b32_e32 v9, 0xffff0000, v9
	v_lshlrev_b32_e32 v8, 16, v5
	v_and_b32_e32 v4, 0xffff0000, v5
	v_mad_i64_i32 v[12:13], s[18:19], v227, s40, v[182:183]
	v_fmac_f32_e32 v6, v18, v23
	v_fmac_f32_e32 v8, v19, v25
	v_fmac_f32_e32 v4, v21, v9
	v_lshl_add_u64 v[12:13], v[12:13], 0, v[180:181]
	v_cvt_pk_fp8_f32 v2, v6, v16 op_sel:[0,0,1]
	v_cvt_pk_fp8_f32 v3, v8, v4 op_sel:[0,0,1]
	v_add_co_u32_e32 v4, vcc, s33, v12
	v_add_u32_e32 v130, 0x80, v186
	s_nop 0
	v_addc_co_u32_e32 v5, vcc, 0, v13, vcc
	global_store_dwordx2 v[4:5], v[10:11], off
	global_store_dwordx2 v[4:5], v[2:3], off offset:128
	v_mad_i64_i32 v[2:3], s[18:19], v130, s40, v[184:185]
	v_add_co_u32_e32 v4, vcc, s36, v2
	v_add_u32_e32 v131, 0x90, v186
	s_nop 0
	v_addc_co_u32_e32 v5, vcc, 0, v3, vcc
	global_load_dwordx4 v[102:105], v[4:5], off nt
	v_add_co_u32_e32 v2, vcc, s41, v2
	v_add_u32_e32 v132, 0xa0, v186
	s_nop 0
	v_addc_co_u32_e32 v3, vcc, 0, v3, vcc
	global_load_dwordx4 v[106:109], v[2:3], off nt
	global_load_dwordx4 v[110:113], v[4:5], off offset:256 nt
	global_load_dwordx4 v[114:117], v[2:3], off offset:256 nt
	v_mad_i64_i32 v[2:3], s[18:19], v131, s40, v[184:185]
	v_add_co_u32_e32 v4, vcc, s36, v2
	v_add_u32_e32 v133, 0xb0, v186
	s_nop 0
	v_addc_co_u32_e32 v5, vcc, 0, v3, vcc
	v_add_co_u32_e32 v2, vcc, s41, v2
	v_mul_f32_e32 v94, 0x3d000000, v94
	s_nop 0
	v_addc_co_u32_e32 v3, vcc, 0, v3, vcc
	global_load_dwordx4 v[118:121], v[4:5], off nt
	global_load_dwordx4 v[122:125], v[4:5], off offset:256 nt
	global_load_dwordx4 v[126:129], v[2:3], off nt
	global_load_dwordx4 v[98:101], v[2:3], off offset:256 nt
	v_mad_i64_i32 v[2:3], s[18:19], v132, s40, v[184:185]
	v_add_co_u32_e32 v4, vcc, s36, v2
	v_mul_f32_e32 v95, 0x3d000000, v95
	s_nop 0
	v_addc_co_u32_e32 v5, vcc, 0, v3, vcc
	v_add_co_u32_e32 v2, vcc, s41, v2
	v_mul_f32_e32 v96, 0x3d000000, v96
	s_nop 0
	v_addc_co_u32_e32 v3, vcc, 0, v3, vcc
	global_load_dwordx4 v[30:33], v[4:5], off nt
	global_load_dwordx4 v[22:25], v[4:5], off offset:256 nt
	global_load_dwordx4 v[26:29], v[2:3], off nt
	global_load_dwordx4 v[18:21], v[2:3], off offset:256 nt
	v_mad_i64_i32 v[2:3], s[18:19], v133, s40, v[184:185]
	v_add_co_u32_e32 v4, vcc, s36, v2
	v_mul_f32_e32 v97, 0x3d000000, v97
	s_nop 0
	v_addc_co_u32_e32 v5, vcc, 0, v3, vcc
	v_add_co_u32_e32 v2, vcc, s41, v2
	v_mul_f32_e32 v90, 0x3d000000, v90
	s_nop 0
	v_addc_co_u32_e32 v3, vcc, 0, v3, vcc
	global_load_dwordx4 v[14:17], v[4:5], off nt
	global_load_dwordx4 v[6:9], v[4:5], off offset:256 nt
	global_load_dwordx4 v[10:13], v[2:3], off nt
	s_nop 0
	global_load_dwordx4 v[2:5], v[2:3], off offset:256 nt
	v_mul_f32_e32 v91, 0x3d000000, v91
	v_mul_f32_e32 v86, 0x3d000000, v86
	v_mul_f32_e32 v92, 0x3d000000, v92
	v_mul_f32_e32 v87, 0x3d000000, v87
	v_mul_f32_e32 v93, 0x3d000000, v93
	v_mul_f32_e32 v88, 0x3d000000, v88
	v_mul_f32_e32 v89, 0x3d000000, v89
	v_mul_f32_e32 v82, 0x3d000000, v82
	v_mul_f32_e32 v83, 0x3d000000, v83
	v_mul_f32_e32 v84, 0x3d000000, v84
	v_mul_f32_e32 v85, 0x3d000000, v85
	v_mul_f32_e32 v78, 0x3d000000, v78
	v_mul_f32_e32 v79, 0x3d000000, v79
	v_mul_f32_e32 v80, 0x3d000000, v80
	v_mul_f32_e32 v81, 0x3d000000, v81
	v_mul_f32_e32 v74, 0x3d000000, v74
	v_mul_f32_e32 v75, 0x3d000000, v75
	v_mul_f32_e32 v70, 0x3d000000, v70
	v_mul_f32_e32 v76, 0x3d000000, v76
	v_mul_f32_e32 v71, 0x3d000000, v71
	v_mul_f32_e32 v77, 0x3d000000, v77
	v_mul_f32_e32 v72, 0x3d000000, v72
	v_mul_f32_e32 v73, 0x3d000000, v73
	v_mul_f32_e32 v66, 0x3d000000, v66
	v_mul_f32_e32 v67, 0x3d000000, v67
	v_mul_f32_e32 v68, 0x3d000000, v68
	v_mul_f32_e32 v69, 0x3d000000, v69
	v_mul_f32_e32 v62, 0x3d000000, v62
	v_mul_f32_e32 v63, 0x3d000000, v63
	v_mul_f32_e32 v65, 0x3d000000, v65
	v_mul_f32_e32 v58, 0x3d000000, v58
	v_mul_f32_e32 v59, 0x3d000000, v59
	v_mul_f32_e32 v64, 0x3d000000, v64
	v_mul_f32_e32 v60, 0x3d000000, v60
	s_waitcnt vmcnt(15)
	v_lshlrev_b32_e32 v134, 16, v102
	v_and_b32_e32 v102, 0xffff0000, v102
	v_lshlrev_b32_e32 v135, 16, v103
	v_and_b32_e32 v103, 0xffff0000, v103
	s_waitcnt vmcnt(14)
	v_lshlrev_b32_e32 v138, 16, v106
	v_fmac_f32_e32 v138, v94, v134
	v_and_b32_e32 v94, 0xffff0000, v106
	v_fmac_f32_e32 v94, v95, v102
	v_lshlrev_b32_e32 v95, 16, v107
	v_fmac_f32_e32 v95, v96, v135
	v_and_b32_e32 v96, 0xffff0000, v107
	v_lshlrev_b32_e32 v136, 16, v104
	v_fmac_f32_e32 v96, v97, v103
	v_lshlrev_b32_e32 v97, 16, v108
	v_fmac_f32_e32 v97, v90, v136
	v_mov_b32_e32 v90, 0
	v_cvt_pk_fp8_f32 v90, v138, v94
	v_and_b32_e32 v104, 0xffff0000, v104
	v_and_b32_e32 v102, 0xffff0000, v108
	v_fmac_f32_e32 v102, v91, v104
	v_mov_b32_e32 v91, 0
	v_cvt_pk_fp8_f32 v91, v97, v102
	s_waitcnt vmcnt(13)
	v_lshlrev_b32_e32 v94, 16, v110
	s_waitcnt vmcnt(12)
	v_lshlrev_b32_e32 v106, 16, v114
	v_lshlrev_b32_e32 v137, 16, v105
	v_lshlrev_b32_e32 v103, 16, v109
	v_cvt_pk_fp8_f32 v90, v95, v96 op_sel:[0,0,1]
	v_and_b32_e32 v95, 0xffff0000, v110
	v_fmac_f32_e32 v106, v86, v94
	v_and_b32_e32 v86, 0xffff0000, v114
	v_and_b32_e32 v105, 0xffff0000, v105
	v_fmac_f32_e32 v103, v92, v137
	v_and_b32_e32 v92, 0xffff0000, v109
	v_lshlrev_b32_e32 v96, 16, v111
	v_fmac_f32_e32 v86, v87, v95
	v_lshlrev_b32_e32 v87, 16, v115
	v_fmac_f32_e32 v92, v93, v105
	v_and_b32_e32 v97, 0xffff0000, v111
	v_fmac_f32_e32 v87, v88, v96
	v_and_b32_e32 v88, 0xffff0000, v115
	v_cvt_pk_fp8_f32 v91, v103, v92 op_sel:[0,0,1]
	v_lshlrev_b32_e32 v102, 16, v112
	v_and_b32_e32 v103, 0xffff0000, v112
	v_fmac_f32_e32 v88, v89, v97
	v_lshlrev_b32_e32 v89, 16, v116
	v_and_b32_e32 v94, 0xffff0000, v116
	v_fmac_f32_e32 v89, v82, v102
	v_fmac_f32_e32 v94, v83, v103
	v_mov_b32_e32 v82, 0
	v_mov_b32_e32 v83, 0
	v_cvt_pk_fp8_f32 v82, v106, v86
	v_cvt_pk_fp8_f32 v83, v89, v94
	v_lshlrev_b32_e32 v104, 16, v113
	v_lshlrev_b32_e32 v95, 16, v117
	v_and_b32_e32 v105, 0xffff0000, v113
	v_fmac_f32_e32 v95, v84, v104
	v_and_b32_e32 v84, 0xffff0000, v117
	v_mad_i64_i32 v[92:93], s[18:19], v130, s40, v[182:183]
	v_fmac_f32_e32 v84, v85, v105
	v_lshl_add_u64 v[92:93], v[92:93], 0, v[180:181]
	v_cvt_pk_fp8_f32 v82, v87, v88 op_sel:[0,0,1]
	v_cvt_pk_fp8_f32 v83, v95, v84 op_sel:[0,0,1]
	v_add_co_u32_e32 v84, vcc, s33, v92
	s_waitcnt vmcnt(11)
	v_lshlrev_b32_e32 v86, 16, v120
	v_addc_co_u32_e32 v85, vcc, 0, v93, vcc
	global_store_dwordx2 v[84:85], v[90:91], off
	global_store_dwordx2 v[84:85], v[82:83], off offset:128
	v_lshlrev_b32_e32 v82, 16, v118
	s_waitcnt vmcnt(11)
	v_lshlrev_b32_e32 v90, 16, v126
	v_and_b32_e32 v83, 0xffff0000, v118
	v_fmac_f32_e32 v90, v78, v82
	v_and_b32_e32 v78, 0xffff0000, v126
	v_lshlrev_b32_e32 v84, 16, v119
	v_fmac_f32_e32 v78, v79, v83
	v_lshlrev_b32_e32 v79, 16, v127
	v_and_b32_e32 v85, 0xffff0000, v119
	v_fmac_f32_e32 v79, v80, v84
	v_and_b32_e32 v80, 0xffff0000, v127
	v_fmac_f32_e32 v80, v81, v85
	v_lshlrev_b32_e32 v81, 16, v128
	v_fmac_f32_e32 v81, v74, v86
	v_mov_b32_e32 v74, 0
	v_cvt_pk_fp8_f32 v74, v90, v78
	v_and_b32_e32 v87, 0xffff0000, v120
	v_and_b32_e32 v82, 0xffff0000, v128
	v_fmac_f32_e32 v82, v75, v87
	v_mov_b32_e32 v75, 0
	v_cvt_pk_fp8_f32 v75, v81, v82
	v_lshlrev_b32_e32 v78, 16, v122
	s_waitcnt vmcnt(10)
	v_lshlrev_b32_e32 v86, 16, v98
	v_lshlrev_b32_e32 v88, 16, v121
	v_lshlrev_b32_e32 v83, 16, v129
	v_cvt_pk_fp8_f32 v74, v79, v80 op_sel:[0,0,1]
	v_and_b32_e32 v79, 0xffff0000, v122
	v_fmac_f32_e32 v86, v70, v78
	v_and_b32_e32 v70, 0xffff0000, v98
	v_and_b32_e32 v89, 0xffff0000, v121
	v_fmac_f32_e32 v83, v76, v88
	v_and_b32_e32 v76, 0xffff0000, v129
	v_lshlrev_b32_e32 v80, 16, v123
	v_fmac_f32_e32 v70, v71, v79
	v_lshlrev_b32_e32 v71, 16, v99
	v_fmac_f32_e32 v76, v77, v89
	v_and_b32_e32 v81, 0xffff0000, v123
	v_fmac_f32_e32 v71, v72, v80
	v_and_b32_e32 v72, 0xffff0000, v99
	v_cvt_pk_fp8_f32 v75, v83, v76 op_sel:[0,0,1]
	v_lshlrev_b32_e32 v82, 16, v124
	v_and_b32_e32 v83, 0xffff0000, v124
	v_fmac_f32_e32 v72, v73, v81
	v_lshlrev_b32_e32 v73, 16, v100
	v_and_b32_e32 v78, 0xffff0000, v100
	v_fmac_f32_e32 v73, v66, v82
	v_fmac_f32_e32 v78, v67, v83
	v_mov_b32_e32 v66, 0
	v_mov_b32_e32 v67, 0
	v_cvt_pk_fp8_f32 v66, v86, v70
	v_cvt_pk_fp8_f32 v67, v73, v78
	v_lshlrev_b32_e32 v84, 16, v125
	v_lshlrev_b32_e32 v79, 16, v101
	v_and_b32_e32 v85, 0xffff0000, v125
	v_fmac_f32_e32 v79, v68, v84
	v_and_b32_e32 v68, 0xffff0000, v101
	v_mad_i64_i32 v[76:77], s[18:19], v131, s40, v[182:183]
	v_fmac_f32_e32 v68, v69, v85
	v_lshl_add_u64 v[76:77], v[76:77], 0, v[180:181]
	v_cvt_pk_fp8_f32 v66, v71, v72 op_sel:[0,0,1]
	v_cvt_pk_fp8_f32 v67, v79, v68 op_sel:[0,0,1]
	v_add_co_u32_e32 v68, vcc, s33, v76
	s_waitcnt vmcnt(7)
	v_lshlrev_b32_e32 v70, 16, v26
	v_addc_co_u32_e32 v69, vcc, 0, v77, vcc
	global_store_dwordx2 v[68:69], v[74:75], off
	global_store_dwordx2 v[68:69], v[66:67], off offset:128
	v_lshlrev_b32_e32 v66, 16, v30
	v_and_b32_e32 v30, 0xffff0000, v30
	v_fmac_f32_e32 v70, v62, v66
	v_and_b32_e32 v62, 0xffff0000, v26
	v_lshlrev_b32_e32 v67, 16, v31
	v_and_b32_e32 v31, 0xffff0000, v31
	v_fmac_f32_e32 v62, v63, v30
	v_and_b32_e32 v63, 0xffff0000, v27
	v_lshlrev_b32_e32 v68, 16, v32
	v_and_b32_e32 v32, 0xffff0000, v32
	v_fmac_f32_e32 v63, v65, v31
	v_lshlrev_b32_e32 v31, 16, v28
	v_and_b32_e32 v28, 0xffff0000, v28
	v_mov_b32_e32 v26, 0
	v_lshlrev_b32_e32 v30, 16, v27
	v_fmac_f32_e32 v31, v58, v68
	v_fmac_f32_e32 v28, v59, v32
	v_cvt_pk_fp8_f32 v26, v70, v62
	v_mov_b32_e32 v27, 0
	v_cvt_pk_fp8_f32 v27, v31, v28
	v_mul_f32_e32 v61, 0x3d000000, v61
	v_lshlrev_b32_e32 v69, 16, v33
	v_and_b32_e32 v33, 0xffff0000, v33
	v_fmac_f32_e32 v30, v64, v67
	v_lshlrev_b32_e32 v32, 16, v29
	v_and_b32_e32 v28, 0xffff0000, v29
	v_fmac_f32_e32 v32, v60, v69
	v_fmac_f32_e32 v28, v61, v33
	v_cvt_pk_fp8_f32 v26, v30, v63 op_sel:[0,0,1]
	v_mul_f32_e32 v30, 0x3d000000, v54
	v_lshlrev_b32_e32 v54, 16, v22
	s_waitcnt vmcnt(8)
	v_lshlrev_b32_e32 v58, 16, v18
	v_cvt_pk_fp8_f32 v27, v32, v28 op_sel:[0,0,1]
	v_mul_f32_e32 v32, 0x3d000000, v55
	v_and_b32_e32 v22, 0xffff0000, v22
	v_fmac_f32_e32 v58, v30, v54
	v_and_b32_e32 v30, 0xffff0000, v18
	v_mul_f32_e32 v33, 0x3d000000, v51
	v_mul_f32_e32 v51, 0x3d000000, v52
	v_mul_f32_e32 v52, 0x3d000000, v57
	v_lshlrev_b32_e32 v55, 16, v23
	v_and_b32_e32 v23, 0xffff0000, v23
	v_fmac_f32_e32 v30, v32, v22
	v_and_b32_e32 v32, 0xffff0000, v19
	v_mul_f32_e32 v31, 0x3d000000, v50
	v_mul_f32_e32 v50, 0x3d000000, v56
	v_lshlrev_b32_e32 v56, 16, v24
	v_and_b32_e32 v24, 0xffff0000, v24
	v_fmac_f32_e32 v32, v52, v23
	v_lshlrev_b32_e32 v23, 16, v20
	v_and_b32_e32 v20, 0xffff0000, v20
	v_lshlrev_b32_e32 v22, 16, v19
	v_fmac_f32_e32 v23, v31, v56
	v_fmac_f32_e32 v20, v33, v24
	v_mov_b32_e32 v18, 0
	v_mov_b32_e32 v19, 0
	v_cvt_pk_fp8_f32 v18, v58, v30
	v_cvt_pk_fp8_f32 v19, v23, v20
	v_mul_f32_e32 v53, 0x3d000000, v53
	v_lshlrev_b32_e32 v57, 16, v25
	v_and_b32_e32 v25, 0xffff0000, v25
	v_lshlrev_b32_e32 v24, 16, v21
	v_and_b32_e32 v20, 0xffff0000, v21
	v_mad_i64_i32 v[28:29], s[18:19], v132, s40, v[182:183]
	v_fmac_f32_e32 v22, v50, v55
	v_fmac_f32_e32 v24, v51, v57
	v_fmac_f32_e32 v20, v53, v25
	v_lshl_add_u64 v[28:29], v[28:29], 0, v[180:181]
	v_cvt_pk_fp8_f32 v18, v22, v32 op_sel:[0,0,1]
	v_cvt_pk_fp8_f32 v19, v24, v20 op_sel:[0,0,1]
	v_add_co_u32_e32 v20, vcc, s33, v28
	s_waitcnt vmcnt(5)
	v_lshlrev_b32_e32 v30, 16, v10
	v_addc_co_u32_e32 v21, vcc, 0, v29, vcc
	global_store_dwordx2 v[20:21], v[26:27], off
	global_store_dwordx2 v[20:21], v[18:19], off offset:128
	v_mul_f32_e32 v18, 0x3d000000, v46
	v_lshlrev_b32_e32 v26, 16, v14
	v_mul_f32_e32 v20, 0x3d000000, v47
	v_and_b32_e32 v14, 0xffff0000, v14
	v_fmac_f32_e32 v30, v18, v26
	v_and_b32_e32 v18, 0xffff0000, v10
	v_mul_f32_e32 v24, 0x3d000000, v49
	v_lshlrev_b32_e32 v27, 16, v15
	v_and_b32_e32 v15, 0xffff0000, v15
	v_fmac_f32_e32 v18, v20, v14
	v_and_b32_e32 v20, 0xffff0000, v11
	v_mul_f32_e32 v19, 0x3d000000, v42
	v_mul_f32_e32 v21, 0x3d000000, v43
	v_lshlrev_b32_e32 v28, 16, v16
	v_and_b32_e32 v16, 0xffff0000, v16
	v_fmac_f32_e32 v20, v24, v15
	v_lshlrev_b32_e32 v15, 16, v12
	v_and_b32_e32 v12, 0xffff0000, v12
	v_mov_b32_e32 v10, 0
	v_lshlrev_b32_e32 v14, 16, v11
	v_fmac_f32_e32 v15, v19, v28
	v_fmac_f32_e32 v12, v21, v16
	v_cvt_pk_fp8_f32 v10, v30, v18
	v_mov_b32_e32 v11, 0
	v_cvt_pk_fp8_f32 v11, v15, v12
	v_mul_f32_e32 v22, 0x3d000000, v48
	v_mul_f32_e32 v23, 0x3d000000, v44
	v_mul_f32_e32 v25, 0x3d000000, v45
	v_lshlrev_b32_e32 v29, 16, v17
	v_and_b32_e32 v17, 0xffff0000, v17
	v_fmac_f32_e32 v14, v22, v27
	v_lshlrev_b32_e32 v16, 16, v13
	v_and_b32_e32 v12, 0xffff0000, v13
	v_fmac_f32_e32 v16, v23, v29
	v_fmac_f32_e32 v12, v25, v17
	v_cvt_pk_fp8_f32 v10, v14, v20 op_sel:[0,0,1]
	v_mul_f32_e32 v14, 0x3d000000, v38
	v_lshlrev_b32_e32 v22, 16, v6
	s_waitcnt vmcnt(6)
	v_lshlrev_b32_e32 v26, 16, v2
	v_cvt_pk_fp8_f32 v11, v16, v12 op_sel:[0,0,1]
	v_mul_f32_e32 v16, 0x3d000000, v39
	v_and_b32_e32 v6, 0xffff0000, v6
	v_fmac_f32_e32 v26, v14, v22
	v_and_b32_e32 v14, 0xffff0000, v2
	v_mul_f32_e32 v20, 0x3d000000, v41
	v_lshlrev_b32_e32 v23, 16, v7
	v_and_b32_e32 v7, 0xffff0000, v7
	v_fmac_f32_e32 v14, v16, v6
	v_and_b32_e32 v16, 0xffff0000, v3
	v_mul_f32_e32 v15, 0x3d000000, v34
	v_mul_f32_e32 v17, 0x3d000000, v35
	v_lshlrev_b32_e32 v24, 16, v8
	v_and_b32_e32 v8, 0xffff0000, v8
	v_fmac_f32_e32 v16, v20, v7
	v_lshlrev_b32_e32 v7, 16, v4
	v_and_b32_e32 v4, 0xffff0000, v4
	v_lshlrev_b32_e32 v6, 16, v3
	v_fmac_f32_e32 v7, v15, v24
	v_fmac_f32_e32 v4, v17, v8
	v_mov_b32_e32 v2, 0
	v_mov_b32_e32 v3, 0
	v_cvt_pk_fp8_f32 v2, v26, v14
	v_cvt_pk_fp8_f32 v3, v7, v4
	v_mad_i64_i32 v[12:13], s[18:19], v133, s40, v[182:183]
	v_mul_f32_e32 v18, 0x3d000000, v40
	v_mul_f32_e32 v19, 0x3d000000, v36
	v_mul_f32_e32 v21, 0x3d000000, v37
	v_lshlrev_b32_e32 v25, 16, v9
	v_and_b32_e32 v9, 0xffff0000, v9
	v_lshlrev_b32_e32 v8, 16, v5
	v_and_b32_e32 v4, 0xffff0000, v5
	v_lshl_add_u64 v[12:13], v[12:13], 0, v[180:181]
	v_fmac_f32_e32 v6, v18, v23
	v_fmac_f32_e32 v8, v19, v25
	v_fmac_f32_e32 v4, v21, v9
	v_cvt_pk_fp8_f32 v2, v6, v16 op_sel:[0,0,1]
	v_cvt_pk_fp8_f32 v3, v8, v4 op_sel:[0,0,1]
	v_add_co_u32_e32 v4, vcc, s33, v12
	s_nop 1
	v_addc_co_u32_e32 v5, vcc, 0, v13, vcc
	s_andn2_b64 vcc, exec, s[0:1]
	s_mov_b64 s[0:1], -1
	global_store_dwordx2 v[4:5], v[10:11], off
	global_store_dwordx2 v[4:5], v[2:3], off offset:128
	s_cbranch_vccnz .LBB0_1008
	s_andn2_b64 vcc, exec, s[2:3]
	s_cbranch_vccnz .LBB0_1007
	s_barrier
	s_branch .LBB0_1007

.LBB0_1102:
	s_ashr_i32 s3, s47, 3
	s_lshl_b32 s8, s47, 8
	v_lshl_or_b32 v192, s2, 8, v226
	s_mul_hi_i32 s9, s3, 0xc000
	s_mul_i32 s3, s3, 0xc000
	s_add_u32 s26, s74, s3
	v_ashrrev_i32_e32 v193, 31, v192
	s_addc_u32 s27, s75, s9
	v_lshlrev_b64 v[222:223], 2, v[192:193]
	v_lshl_add_u64 v[2:3], s[26:27], 0, v[222:223]
	s_mov_b64 s[26:27], 0x4000
	s_movk_i32 s3, 0x4000
	v_lshl_add_u64 v[10:11], v[2:3], 0, s[26:27]
	v_add_co_u32_e32 v2, vcc, s3, v2
	s_nop 15
	s_nop 15
	v_add_u32_e32 v210, s8, v224
	s_nop 0
	v_addc_co_u32_e32 v3, vcc, 0, v3, vcc
	global_load_dwordx4 v[2:5], v[2:3], off nt
	s_nop 0
	global_load_dwordx4 v[6:9], v[10:11], off offset:16 nt
	v_readlane_b32 s48, v254, 7
	v_readlane_b32 s49, v254, 8
	v_ashrrev_i32_e32 v211, 31, v210
	v_lshlrev_b64 v[250:251], 13, v[210:211]
	v_lshl_add_u64 v[212:213], s[48:49], 0, v[222:223]
	v_readlane_b32 s50, v254, 9
	v_readlane_b32 s51, v254, 10
	v_readlane_b32 s52, v254, 11
	v_readlane_b32 s53, v254, 12
	v_readlane_b32 s54, v254, 13
	v_readlane_b32 s55, v254, 14
	v_readlane_b32 s56, v254, 15
	v_readlane_b32 s57, v254, 16
	v_readlane_b32 s58, v254, 17
	v_readlane_b32 s59, v254, 18
	v_readlane_b32 s60, v254, 19
	v_readlane_b32 s61, v254, 20
	v_readlane_b32 s62, v254, 21
	v_readlane_b32 s63, v254, 22
	s_waitcnt vmcnt(0)
	v_pk_mul_f32 v[206:207], v[4:5], s[16:17] op_sel_hi:[1,0]
	v_pk_mul_f32 v[208:209], v[2:3], s[16:17] op_sel_hi:[1,0]
	v_pk_mul_f32 v[204:205], v[8:9], s[16:17] op_sel_hi:[1,0]
	v_pk_mul_f32 v[202:203], v[6:7], s[16:17] op_sel_hi:[1,0]
	global_load_dwordx4 v[2:5], v[10:11], off offset:528 nt
	global_load_dwordx4 v[6:9], v[10:11], off offset:512 nt
	s_waitcnt vmcnt(1)
	v_pk_mul_f32 v[194:195], v[2:3], s[16:17] op_sel_hi:[1,0]
	v_and_b32_e32 v3, 64, v231
	v_xor_b32_e32 v2, 16, v231
	v_add_u32_e32 v3, 64, v3
	v_cmp_lt_i32_e32 vcc, v2, v3
	s_waitcnt vmcnt(0)
	v_pk_mul_f32 v[200:201], v[6:7], s[16:17] op_sel_hi:[1,0]
	v_pk_mul_f32 v[198:199], v[8:9], s[16:17] op_sel_hi:[1,0]
	v_cndmask_b32_e32 v2, v231, v2, vcc
	v_lshlrev_b32_e32 v232, 2, v2
	v_xor_b32_e32 v2, 32, v231
	v_cmp_lt_i32_e32 vcc, v2, v3
	v_pk_mul_f32 v[196:197], v[4:5], s[16:17] op_sel_hi:[1,0]
	s_nop 0
	v_cndmask_b32_e32 v2, v231, v2, vcc
	v_lshlrev_b32_e32 v233, 2, v2
	v_lshl_add_u64 v[2:3], v[212:213], 0, v[250:251]
	global_load_dwordx4 v[234:237], v[2:3], off offset:16 nt
	global_load_dwordx4 v[238:241], v[2:3], off nt
	global_load_dwordx4 v[242:245], v[2:3], off offset:528 nt
	global_load_dwordx4 v[246:249], v[2:3], off offset:512 nt
	v_or_b32_e32 v2, 16, v210
	v_ashrrev_i32_e32 v3, 31, v2
	v_lshlrev_b64 v[218:219], 13, v[2:3]
	v_lshl_add_u64 v[2:3], v[212:213], 0, v[218:219]
	global_load_dwordx4 v[170:173], v[2:3], off offset:16 nt
	global_load_dwordx4 v[174:177], v[2:3], off nt
	global_load_dwordx4 v[162:165], v[2:3], off offset:528 nt
	global_load_dwordx4 v[166:169], v[2:3], off offset:512 nt
	v_or_b32_e32 v2, 32, v210
	v_ashrrev_i32_e32 v3, 31, v2
	v_lshlrev_b64 v[216:217], 13, v[2:3]
	v_lshl_add_u64 v[2:3], v[212:213], 0, v[216:217]
	global_load_dwordx4 v[26:29], v[2:3], off offset:16 nt
	global_load_dwordx4 v[30:33], v[2:3], off nt
	global_load_dwordx4 v[18:21], v[2:3], off offset:528 nt
	global_load_dwordx4 v[22:25], v[2:3], off offset:512 nt
	v_or_b32_e32 v2, 48, v210
	v_ashrrev_i32_e32 v3, 31, v2
	v_lshlrev_b64 v[214:215], 13, v[2:3]
	v_lshl_add_u64 v[6:7], v[212:213], 0, v[214:215]
	global_load_dwordx4 v[10:13], v[6:7], off offset:16 nt
	global_load_dwordx4 v[14:17], v[6:7], off nt
	global_load_dwordx4 v[2:5], v[6:7], off offset:528 nt
	s_nop 0
	global_load_dwordx4 v[6:9], v[6:7], off offset:512 nt
	v_lshl_add_u64 v[250:251], s[78:79], 0, v[250:251]
	v_lshl_add_u64 v[222:223], v[250:251], 0, v[222:223]
	s_waitcnt vmcnt(14)
	v_pk_fma_f32 v[160:161], v[160:161], v[206:207], v[240:241]
	v_pk_fma_f32 v[158:159], v[158:159], v[208:209], v[238:239]
	v_pk_fma_f32 v[154:155], v[154:155], v[202:203], v[234:235]
	s_waitcnt vmcnt(12)
	v_pk_fma_f32 v[152:153], v[152:153], v[198:199], v[248:249]
	v_pk_fma_f32 v[150:151], v[150:151], v[200:201], v[246:247]
	v_pk_fma_f32 v[146:147], v[146:147], v[194:195], v[242:243]
	v_pk_fma_f32 v[156:157], v[156:157], v[204:205], v[236:237]
	global_store_dwordx4 v[222:223], v[158:161], off
	global_store_dwordx4 v[222:223], v[154:157], off offset:16
	v_pk_fma_f32 v[148:149], v[148:149], v[196:197], v[244:245]
	v_mul_f32_e32 v159, v159, v159
	v_mul_f32_e32 v155, v155, v155
	global_store_dwordx4 v[222:223], v[150:153], off offset:512
	global_store_dwordx4 v[222:223], v[146:149], off offset:528
	v_fmac_f32_e32 v159, v158, v158
	v_mul_f32_e32 v151, v151, v151
	v_mul_f32_e32 v147, v147, v147
	v_mul_f32_e32 v158, v161, v161
	v_fmac_f32_e32 v155, v154, v154
	v_mul_f32_e32 v154, v157, v157
	v_fmac_f32_e32 v151, v150, v150
	v_mul_f32_e32 v150, v153, v153
	v_fmac_f32_e32 v147, v146, v146
	v_mul_f32_e32 v146, v149, v149
	v_fmac_f32_e32 v158, v160, v160
	v_fmac_f32_e32 v154, v156, v156
	v_fmac_f32_e32 v150, v152, v152
	v_fmac_f32_e32 v146, v148, v148
	v_add_f32_e32 v158, v159, v158
	v_add_f32_e32 v154, v155, v154
	v_add_f32_e32 v150, v151, v150
	v_add_f32_e32 v146, v147, v146
	v_add_f32_e32 v154, v158, v154
	v_add_f32_e32 v146, v150, v146
	v_add_f32_e32 v146, v154, v146
	ds_bpermute_b32 v147, v232, v146
	s_waitcnt lgkmcnt(0)
	v_add_f32_e32 v146, v146, v147
	ds_bpermute_b32 v147, v233, v146
	s_and_saveexec_b64 s[26:27], s[0:1]
	s_cbranch_execz .LBB0_1104
	s_waitcnt lgkmcnt(0)
	v_add_f32_e32 v146, v146, v147
	ds_write_b32 v227, v146

.LBB0_1110:
	s_or_b64 exec, exec, s[26:27]
	s_waitcnt lgkmcnt(0)
	v_lshlrev_b64 v[2:3], 13, v[210:211]
	s_mov_b64 s[26:27], 0x100000
	v_lshl_add_u64 v[136:137], v[2:3], 0, s[26:27]
	s_mov_b64 s[26:27], 0x120000
	v_lshl_add_u64 v[4:5], v[212:213], 0, v[136:137]
	v_lshl_add_u64 v[118:119], v[2:3], 0, s[26:27]
	s_mov_b64 s[26:27], 0x140000
	global_load_dwordx4 v[120:123], v[4:5], off offset:16 nt
	global_load_dwordx4 v[124:127], v[4:5], off nt
	global_load_dwordx4 v[128:131], v[4:5], off offset:528 nt
	global_load_dwordx4 v[132:135], v[4:5], off offset:512 nt
	v_lshl_add_u64 v[4:5], v[212:213], 0, v[118:119]
	v_lshl_add_u64 v[116:117], v[2:3], 0, s[26:27]
	v_lshl_add_u64 v[114:115], v[2:3], 0, s[18:19]
	global_load_dwordx4 v[106:109], v[4:5], off offset:16 nt
	global_load_dwordx4 v[110:113], v[4:5], off nt
	global_load_dwordx4 v[98:101], v[4:5], off offset:528 nt
	global_load_dwordx4 v[102:105], v[4:5], off offset:512 nt
	v_lshl_add_u64 v[4:5], v[212:213], 0, v[116:117]
	v_lshl_add_u64 v[6:7], v[212:213], 0, v[114:115]
	global_load_dwordx4 v[26:29], v[4:5], off offset:16 nt
	global_load_dwordx4 v[30:33], v[4:5], off nt
	global_load_dwordx4 v[18:21], v[4:5], off offset:528 nt
	global_load_dwordx4 v[22:25], v[4:5], off offset:512 nt
	global_load_dwordx4 v[10:13], v[6:7], off offset:16 nt
	global_load_dwordx4 v[14:17], v[6:7], off nt
	s_nop 0
	global_load_dwordx4 v[2:5], v[6:7], off offset:528 nt
	s_nop 0
	global_load_dwordx4 v[6:9], v[6:7], off offset:512 nt
	s_waitcnt vmcnt(14)
	v_pk_fma_f32 v[96:97], v[96:97], v[206:207], v[126:127]
	v_pk_fma_f32 v[94:95], v[94:95], v[208:209], v[124:125]
	v_pk_fma_f32 v[90:91], v[90:91], v[202:203], v[120:121]
	v_mul_f32_e32 v120, v95, v95
	v_mul_f32_e32 v121, v97, v97
	v_pk_fma_f32 v[92:93], v[92:93], v[204:205], v[122:123]
	v_fmac_f32_e32 v120, v94, v94
	v_fmac_f32_e32 v121, v96, v96
	v_add_f32_e32 v120, v120, v121
	v_mul_f32_e32 v121, v91, v91
	v_mul_f32_e32 v122, v93, v93
	v_fmac_f32_e32 v121, v90, v90
	v_fmac_f32_e32 v122, v92, v92
	v_add_f32_e32 v121, v121, v122
	s_waitcnt vmcnt(12)
	v_pk_fma_f32 v[88:89], v[88:89], v[198:199], v[134:135]
	v_pk_fma_f32 v[86:87], v[86:87], v[200:201], v[132:133]
	v_add_f32_e32 v124, v120, v121
	v_pk_fma_f32 v[120:121], v[82:83], v[194:195], v[128:129]
	v_mul_f32_e32 v82, v87, v87
	v_mul_f32_e32 v83, v89, v89
	v_pk_fma_f32 v[122:123], v[84:85], v[196:197], v[130:131]
	v_fmac_f32_e32 v82, v86, v86
	v_fmac_f32_e32 v83, v88, v88
	v_add_f32_e32 v82, v82, v83
	v_mul_f32_e32 v83, v121, v121
	v_mul_f32_e32 v84, v123, v123
	v_fmac_f32_e32 v83, v120, v120
	v_fmac_f32_e32 v84, v122, v122
	v_add_f32_e32 v83, v83, v84
	v_add_f32_e32 v82, v82, v83
	v_add_f32_e32 v124, v124, v82
	ds_bpermute_b32 v125, v232, v124
	v_lshl_add_u64 v[82:83], s[78:79], 0, v[136:137]
	v_lshl_add_u64 v[84:85], v[192:193], 2, v[82:83]
	global_store_dwordx4 v[84:85], v[94:97], off
	global_store_dwordx4 v[84:85], v[90:93], off offset:16
	global_store_dwordx4 v[84:85], v[86:89], off offset:512
	global_store_dwordx4 v[84:85], v[120:123], off offset:528
	s_waitcnt lgkmcnt(0)
	v_add_f32_e32 v82, v124, v125
	ds_bpermute_b32 v83, v233, v82
	s_and_saveexec_b64 s[26:27], s[0:1]
	s_cbranch_execz .LBB0_1112
	s_waitcnt lgkmcnt(0)
	v_add_f32_e32 v82, v82, v83
	ds_write_b32 v227, v82 offset:2048

.LBB0_1492:
	v_lshl_add_u64 v[4:5], s[18:19], 0, v[178:179]
	s_add_i32 s28, s9, s5
	s_ashr_i32 s29, s28, 31
	v_add_co_u32_e32 v6, vcc, s23, v4
	s_mov_b64 s[0:1], vcc
	v_add_co_u32_e32 v8, vcc, s24, v4
	s_lshl_b64 s[28:29], s[28:29], 2
	s_nop 0
	v_addc_co_u32_e32 v9, vcc, 0, v5, vcc
	s_add_u32 s28, s12, s28
	global_load_dwordx2 v[90:91], v[8:9], off offset:-4096 nt
	global_load_dwordx2 v[100:101], v[8:9], off nt
	s_addc_u32 s29, s13, s29
	global_load_dwordx4 v[0:3], v179, s[28:29] nt
	v_addc_co_u32_e64 v7, vcc, 0, v5, s[0:1]
	global_load_dwordx2 v[102:103], v[8:9], off offset:512 nt
	global_load_dwordx2 v[108:109], v[6:7], off offset:512 nt
	v_lshl_add_u64 v[72:73], s[16:17], 0, v[60:61]
	global_load_dwordx4 v[86:89], v[72:73], off nt
	global_load_dwordx4 v[96:99], v[72:73], off offset:1024 nt
	global_load_dwordx2 v[110:111], v[6:7], off offset:1024 nt
	global_load_dwordx2 v[114:115], v[8:9], off offset:1024 nt
	global_load_dwordx4 v[56:59], v[72:73], off offset:2048 nt
	global_load_dwordx4 v[52:55], v[72:73], off offset:3072 nt
	v_add_co_u32_e32 v70, vcc, s25, v72
	v_lshl_add_u64 v[4:5], s[10:11], 0, v[178:179]
	s_nop 0
	v_addc_co_u32_e32 v71, vcc, 0, v73, vcc
	v_add_co_u32_e32 v74, vcc, s23, v4
	v_lshl_add_u64 v[68:69], s[14:15], 0, v[60:61]
	s_nop 0
	v_addc_co_u32_e32 v75, vcc, 0, v5, vcc
	v_add_co_u32_e32 v76, vcc, s24, v4
	global_load_dwordx2 v[118:119], v[6:7], off offset:1536 nt
	global_load_dwordx2 v[128:129], v[6:7], off offset:2048 nt
	global_load_dwordx4 v[48:51], v[70:71], off nt
	global_load_dwordx4 v[44:47], v[70:71], off offset:1024 nt
	global_load_dwordx2 v[138:139], v[8:9], off offset:1536 nt
	global_load_dwordx2 v[140:141], v[8:9], off offset:2048 nt
	global_load_dwordx2 v[142:143], v[8:9], off offset:2560 nt
	global_load_dwordx2 v[144:145], v[8:9], off offset:3072 nt
	global_load_dwordx4 v[40:43], v[70:71], off offset:2048 nt
	global_load_dwordx4 v[36:39], v[70:71], off offset:3072 nt
	global_load_dwordx2 v[146:147], v[6:7], off offset:2560 nt
	global_load_dwordx2 v[148:149], v[6:7], off offset:3072 nt
	global_load_dwordx2 v[150:151], v[6:7], off offset:3584 nt
	global_load_dwordx2 v[152:153], v[8:9], off offset:3584 nt
	v_addc_co_u32_e32 v77, vcc, 0, v5, vcc
	v_add_co_u32_e32 v66, vcc, s25, v68
	global_load_dwordx4 v[32:35], v[68:69], off nt
	global_load_dwordx4 v[28:31], v[68:69], off offset:1024 nt
	global_load_dwordx2 v[124:125], v[76:77], off offset:-4096 nt
	global_load_dwordx2 v[126:127], v[76:77], off nt
	global_load_dwordx2 v[120:121], v[76:77], off offset:512 nt
	global_load_dwordx2 v[112:113], v[76:77], off offset:1024 nt
	global_load_dwordx4 v[24:27], v[68:69], off offset:2048 nt
	global_load_dwordx4 v[20:23], v[68:69], off offset:3072 nt
	v_addc_co_u32_e32 v67, vcc, 0, v69, vcc
	global_load_dwordx2 v[122:123], v[74:75], off offset:512 nt
	global_load_dwordx2 v[116:117], v[74:75], off offset:1024 nt
	global_load_dwordx2 v[104:105], v[74:75], off offset:1536 nt
	global_load_dwordx2 v[92:93], v[74:75], off offset:2048 nt
	global_load_dwordx4 v[16:19], v[66:67], off nt
	global_load_dwordx4 v[12:15], v[66:67], off offset:1024 nt
	global_load_dwordx2 v[106:107], v[76:77], off offset:1536 nt
	global_load_dwordx2 v[94:95], v[76:77], off offset:2048 nt
	global_load_dwordx2 v[82:83], v[76:77], off offset:2560 nt
	global_load_dwordx2 v[78:79], v[76:77], off offset:3072 nt
	global_load_dwordx4 v[8:11], v[66:67], off offset:2048 nt
	global_load_dwordx4 v[4:7], v[66:67], off offset:3072 nt
	global_load_dwordx2 v[84:85], v[74:75], off offset:2560 nt
	global_load_dwordx2 v[80:81], v[74:75], off offset:3072 nt
	s_nop 0
	global_load_dwordx2 v[74:75], v[74:75], off offset:3584 nt
	s_nop 0
	global_load_dwordx2 v[76:77], v[76:77], off offset:3584 nt
	s_waitcnt vmcnt(48)
	v_lshlrev_b32_e32 v156, 16, v90
	s_waitcnt vmcnt(47)
	v_and_b32_e32 v157, 0xffff0000, v100
	v_lshlrev_b32_e32 v154, 16, v100
	v_and_b32_e32 v155, 0xffff0000, v90
	s_waitcnt vmcnt(46)
	v_pk_mul_f32 v[156:157], v[0:1], v[156:157]
	v_lshlrev_b32_e32 v90, 16, v91
	v_pk_fma_f32 v[154:155], v[0:1], v[154:155], v[156:157] op_sel:[1,0,0] op_sel_hi:[0,1,1]
	v_and_b32_e32 v157, 0xffff0000, v91
	v_and_b32_e32 v91, 0xffff0000, v101
	v_lshlrev_b32_e32 v156, 16, v101
	v_pk_mul_f32 v[90:91], v[0:1], v[90:91]
	s_waitcnt vmcnt(45)
	v_lshlrev_b32_e32 v100, 16, v102
	v_pk_fma_f32 v[90:91], v[0:1], v[156:157], v[90:91] op_sel:[1,0,0] op_sel_hi:[0,1,1]
	s_waitcnt vmcnt(44)
	v_lshlrev_b32_e32 v156, 16, v108
	v_and_b32_e32 v157, 0xffff0000, v102
	v_and_b32_e32 v101, 0xffff0000, v108
	v_pk_mul_f32 v[156:157], v[0:1], v[156:157]
	v_lshlrev_b32_e32 v102, 16, v109
	v_pk_fma_f32 v[100:101], v[0:1], v[100:101], v[156:157] op_sel:[1,0,0] op_sel_hi:[0,1,1]
	v_lshlrev_b32_e32 v156, 16, v103
	v_and_b32_e32 v103, 0xffff0000, v103
	v_and_b32_e32 v157, 0xffff0000, v109
	v_pk_mul_f32 v[102:103], v[0:1], v[102:103]
	s_waitcnt vmcnt(40)
	v_lshlrev_b32_e32 v108, 16, v114
	v_pk_fma_f32 v[102:103], v[0:1], v[156:157], v[102:103] op_sel:[1,0,0] op_sel_hi:[0,1,1]
	v_lshlrev_b32_e32 v156, 16, v110
	v_and_b32_e32 v157, 0xffff0000, v114
	v_and_b32_e32 v109, 0xffff0000, v110
	v_pk_mul_f32 v[156:157], v[0:1], v[156:157]
	v_lshlrev_b32_e32 v110, 16, v111
	v_pk_fma_f32 v[108:109], v[0:1], v[108:109], v[156:157] op_sel:[1,0,0] op_sel_hi:[0,1,1]
	v_and_b32_e32 v157, 0xffff0000, v111
	v_and_b32_e32 v111, 0xffff0000, v115
	v_lshlrev_b32_e32 v156, 16, v115
	v_pk_mul_f32 v[110:111], v[0:1], v[110:111]
	s_waitcnt vmcnt(33)
	v_lshlrev_b32_e32 v114, 16, v138
	v_pk_fma_f32 v[110:111], v[0:1], v[156:157], v[110:111] op_sel:[1,0,0] op_sel_hi:[0,1,1]
	v_lshlrev_b32_e32 v156, 16, v118
	v_and_b32_e32 v157, 0xffff0000, v138
	v_and_b32_e32 v115, 0xffff0000, v118
	v_pk_mul_f32 v[156:157], v[0:1], v[156:157]
	v_lshlrev_b32_e32 v118, 16, v119
	v_pk_fma_f32 v[114:115], v[0:1], v[114:115], v[156:157] op_sel:[1,0,0] op_sel_hi:[0,1,1]
	v_and_b32_e32 v157, 0xffff0000, v119
	v_and_b32_e32 v119, 0xffff0000, v139
	v_lshlrev_b32_e32 v156, 16, v139
	v_pk_mul_f32 v[118:119], v[0:1], v[118:119]
	s_waitcnt vmcnt(32)
	v_lshlrev_b32_e32 v138, 16, v140
	v_pk_fma_f32 v[118:119], v[0:1], v[156:157], v[118:119] op_sel:[1,0,0] op_sel_hi:[0,1,1]
	v_lshlrev_b32_e32 v156, 16, v128
	v_and_b32_e32 v157, 0xffff0000, v140
	v_and_b32_e32 v139, 0xffff0000, v128
	v_pk_mul_f32 v[156:157], v[0:1], v[156:157]
	v_lshlrev_b32_e32 v128, 16, v129
	v_pk_fma_f32 v[156:157], v[0:1], v[138:139], v[156:157] op_sel:[1,0,0] op_sel_hi:[0,1,1]
	v_and_b32_e32 v139, 0xffff0000, v129
	v_and_b32_e32 v129, 0xffff0000, v141
	v_lshlrev_b32_e32 v138, 16, v141
	v_pk_mul_f32 v[128:129], v[0:1], v[128:129]
	s_waitcnt vmcnt(27)
	v_lshlrev_b32_e32 v140, 16, v146
	v_and_b32_e32 v141, 0xffff0000, v142
	v_pk_fma_f32 v[128:129], v[0:1], v[138:139], v[128:129] op_sel:[1,0,0] op_sel_hi:[0,1,1]
	v_lshlrev_b32_e32 v138, 16, v142
	v_and_b32_e32 v139, 0xffff0000, v146
	v_pk_mul_f32 v[140:141], v[0:1], v[140:141]
	s_nop 0
	v_pk_fma_f32 v[158:159], v[0:1], v[138:139], v[140:141] op_sel:[1,0,0] op_sel_hi:[0,1,1]
	v_lshlrev_b32_e32 v140, 16, v147
	v_and_b32_e32 v141, 0xffff0000, v143
	v_lshlrev_b32_e32 v138, 16, v143
	v_and_b32_e32 v139, 0xffff0000, v147
	v_pk_mul_f32 v[140:141], v[0:1], v[140:141]
	s_nop 0
	v_pk_fma_f32 v[160:161], v[0:1], v[138:139], v[140:141] op_sel:[1,0,0] op_sel_hi:[0,1,1]
	s_waitcnt vmcnt(26)
	v_lshlrev_b32_e32 v140, 16, v148
	v_and_b32_e32 v141, 0xffff0000, v144
	v_lshlrev_b32_e32 v138, 16, v144
	v_and_b32_e32 v139, 0xffff0000, v148
	v_pk_mul_f32 v[140:141], v[0:1], v[140:141]
	s_nop 0
	v_pk_fma_f32 v[162:163], v[0:1], v[138:139], v[140:141] op_sel:[1,0,0] op_sel_hi:[0,1,1]
	v_lshlrev_b32_e32 v140, 16, v149
	v_and_b32_e32 v141, 0xffff0000, v145
	v_lshlrev_b32_e32 v138, 16, v145
	v_and_b32_e32 v139, 0xffff0000, v149
	v_pk_mul_f32 v[140:141], v[0:1], v[140:141]
	s_nop 0
	v_pk_fma_f32 v[164:165], v[0:1], v[138:139], v[140:141] op_sel:[1,0,0] op_sel_hi:[0,1,1]
	s_waitcnt vmcnt(25)
	v_lshlrev_b32_e32 v140, 16, v150
	s_waitcnt vmcnt(24)
	v_and_b32_e32 v141, 0xffff0000, v152
	v_lshlrev_b32_e32 v138, 16, v152
	v_and_b32_e32 v139, 0xffff0000, v150
	v_pk_mul_f32 v[140:141], v[0:1], v[140:141]
	s_nop 0
	v_pk_fma_f32 v[166:167], v[0:1], v[138:139], v[140:141] op_sel:[1,0,0] op_sel_hi:[0,1,1]
	v_lshlrev_b32_e32 v140, 16, v151
	v_and_b32_e32 v141, 0xffff0000, v153
	v_lshlrev_b32_e32 v138, 16, v153
	v_and_b32_e32 v139, 0xffff0000, v151
	v_pk_mul_f32 v[140:141], v[0:1], v[140:141]
	s_nop 0
	v_pk_fma_f32 v[168:169], v[0:1], v[138:139], v[140:141] op_sel:[1,0,0] op_sel_hi:[0,1,1]
	ds_read_b128 v[138:141], v137
	ds_read_b128 v[142:145], v137 offset:1024
	ds_read_b128 v[146:149], v137 offset:2048
	ds_read_b128 v[150:153], v137 offset:3072
	s_add_i32 s3, s3, 2
	s_waitcnt lgkmcnt(3)
	v_pk_fma_f32 v[88:89], v[90:91], v[140:141], v[88:89]
	v_pk_fma_f32 v[90:91], v[154:155], v[138:139], v[86:87]
	s_waitcnt lgkmcnt(2)
	v_pk_fma_f32 v[86:87], v[100:101], v[142:143], v[96:97]
	v_pk_fma_f32 v[0:1], v[102:103], v[144:145], v[98:99]
	v_mov_b32_e32 v98, v91
	v_mov_b32_e32 v99, v87
	v_mov_b32_e32 v96, v90
	v_mov_b32_e32 v97, v86
	v_pk_mul_f32 v[98:99], v[98:99], v[98:99]
	v_mov_b32_e32 v100, v89
	v_mov_b32_e32 v101, v1
	v_pk_fma_f32 v[96:97], v[96:97], v[96:97], v[98:99]
	v_mov_b32_e32 v98, v88
	v_mov_b32_e32 v99, v0
	v_pk_mul_f32 v[100:101], v[100:101], v[100:101]
	s_add_i32 s5, s5, 4
	v_pk_fma_f32 v[98:99], v[98:99], v[98:99], v[100:101]
	s_add_u32 s10, s10, 0x12000
	v_pk_add_f32 v[154:155], v[96:97], v[98:99]
	s_waitcnt lgkmcnt(1)
	v_pk_fma_f32 v[96:97], v[108:109], v[146:147], v[56:57]
	v_pk_fma_f32 v[98:99], v[110:111], v[148:149], v[58:59]
	v_pk_mul_f32 v[100:101], v[96:97], v[96:97]
	v_pk_mul_f32 v[56:57], v[98:99], v[98:99]
	s_addc_u32 s11, s11, 0
	v_pk_mov_b32 v[102:103], v[100:101], v[56:57] op_sel:[1,0]
	v_mov_b32_e32 v101, v57
	ds_read_b128 v[56:59], v137 offset:4096
	v_pk_add_f32 v[170:171], v[102:103], v[100:101]
	s_waitcnt lgkmcnt(1)
	v_pk_fma_f32 v[100:101], v[118:119], v[152:153], v[54:55]
	v_pk_fma_f32 v[102:103], v[114:115], v[150:151], v[52:53]
	ds_read_b128 v[52:55], v137 offset:5120
	s_waitcnt lgkmcnt(1)
	v_pk_fma_f32 v[110:111], v[156:157], v[56:57], v[48:49]
	v_pk_fma_f32 v[108:109], v[128:129], v[58:59], v[50:51]
	v_mul_f32_e32 v50, v110, v110
	v_pk_add_f32 v[48:49], v[154:155], v[154:155] op_sel:[0,1] op_sel_hi:[1,0]
	v_mul_f32_e32 v114, v111, v111
	v_mov_b32_e32 v49, v50
	v_pk_add_f32 v[50:51], v[170:171], v[170:171] op_sel:[0,1] op_sel_hi:[1,0]
	v_mul_f32_e32 v115, v108, v108
	v_mov_b32_e32 v51, v114
	v_pk_add_f32 v[48:49], v[48:49], v[50:51]
	v_mul_f32_e32 v50, v103, v103
	v_pk_fma_f32 v[50:51], v[102:103], v[102:103], v[50:51] op_sel_hi:[1,1,0]
	v_mul_f32_e32 v114, v101, v101
	v_mul_f32_e32 v118, v109, v109
	v_mov_b32_e32 v51, v115
	v_pk_fma_f32 v[114:115], v[100:101], v[100:101], v[114:115] op_sel_hi:[1,1,0]
	s_add_u32 s14, s14, 0x4000
	v_mov_b32_e32 v115, v118
	v_pk_add_f32 v[50:51], v[50:51], v[114:115]
	s_waitcnt lgkmcnt(0)
	v_pk_fma_f32 v[114:115], v[158:159], v[52:53], v[44:45]
	v_pk_add_f32 v[128:129], v[48:49], v[50:51]
	v_pk_fma_f32 v[118:119], v[160:161], v[54:55], v[46:47]
	ds_read_b128 v[48:51], v137 offset:6144
	ds_read_b128 v[44:47], v137 offset:7168
	v_pk_mul_f32 v[154:155], v[118:119], v[118:119]
	v_pk_mul_f32 v[156:157], v[114:115], v[114:115]
	v_pk_add_f32 v[128:129], v[128:129], v[128:129] op_sel:[0,1] op_sel_hi:[1,0]
	v_pk_mov_b32 v[158:159], v[156:157], v[154:155] op_sel:[1,0]
	v_mov_b32_e32 v157, v155
	v_pk_add_f32 v[154:155], v[158:159], v[156:157]
	s_waitcnt lgkmcnt(0)
	v_pk_fma_f32 v[36:37], v[166:167], v[44:45], v[36:37]
	v_pk_add_f32 v[154:155], v[154:155], v[154:155] op_sel:[0,1] op_sel_hi:[1,0]
	v_mul_f32_e32 v156, v36, v36
	v_mul_f32_e32 v157, v37, v37
	v_pk_fma_f32 v[42:43], v[164:165], v[50:51], v[42:43]
	v_pk_fma_f32 v[40:41], v[162:163], v[48:49], v[40:41]
	v_mov_b32_e32 v129, v156
	v_mov_b32_e32 v155, v157
	v_pk_fma_f32 v[38:39], v[168:169], v[46:47], v[38:39]
	v_pk_add_f32 v[128:129], v[128:129], v[154:155]
	v_mul_f32_e32 v154, v41, v41
	v_mul_f32_e32 v156, v43, v43
	v_mul_f32_e32 v158, v38, v38
	v_mul_f32_e32 v159, v39, v39
	v_pk_fma_f32 v[154:155], v[40:41], v[40:41], v[154:155] op_sel_hi:[1,1,0]
	v_pk_fma_f32 v[156:157], v[42:43], v[42:43], v[156:157] op_sel_hi:[1,1,0]
	v_mov_b32_e32 v155, v158
	v_mov_b32_e32 v157, v159
	v_pk_add_f32 v[154:155], v[154:155], v[156:157]
	s_waitcnt vmcnt(21)
	v_lshlrev_b32_e32 v156, 16, v124
	s_waitcnt vmcnt(20)
	v_and_b32_e32 v157, 0xffff0000, v126
	v_pk_add_f32 v[128:129], v[128:129], v[154:155]
	v_lshlrev_b32_e32 v154, 16, v126
	v_and_b32_e32 v155, 0xffff0000, v124
	v_pk_mul_f32 v[156:157], v[2:3], v[156:157]
	v_lshlrev_b32_e32 v124, 16, v125
	v_pk_fma_f32 v[154:155], v[2:3], v[154:155], v[156:157] op_sel:[1,0,0] op_sel_hi:[0,1,1]
	v_and_b32_e32 v157, 0xffff0000, v125
	v_and_b32_e32 v125, 0xffff0000, v127
	v_lshlrev_b32_e32 v156, 16, v127
	v_pk_mul_f32 v[124:125], v[2:3], v[124:125]
	s_waitcnt vmcnt(15)
	v_lshlrev_b32_e32 v126, 16, v122
	v_pk_fma_f32 v[124:125], v[2:3], v[156:157], v[124:125] op_sel:[1,0,0] op_sel_hi:[0,1,1]
	v_and_b32_e32 v127, 0xffff0000, v120
	v_pk_fma_f32 v[34:35], v[124:125], v[140:141], v[34:35]
	v_lshlrev_b32_e32 v124, 16, v120
	v_and_b32_e32 v125, 0xffff0000, v122
	v_pk_mul_f32 v[126:127], v[2:3], v[126:127]
	v_lshlrev_b32_e32 v120, 16, v123
	v_pk_fma_f32 v[124:125], v[2:3], v[124:125], v[126:127] op_sel:[1,0,0] op_sel_hi:[0,1,1]
	v_lshlrev_b32_e32 v126, 16, v121
	v_and_b32_e32 v121, 0xffff0000, v121
	v_and_b32_e32 v127, 0xffff0000, v123
	v_pk_mul_f32 v[120:121], v[2:3], v[120:121]
	v_pk_fma_f32 v[32:33], v[154:155], v[138:139], v[32:33]
	v_pk_fma_f32 v[120:121], v[2:3], v[126:127], v[120:121] op_sel:[1,0,0] op_sel_hi:[0,1,1]
	v_pk_fma_f32 v[28:29], v[124:125], v[142:143], v[28:29]
	v_pk_fma_f32 v[30:31], v[120:121], v[144:145], v[30:31]
	v_mov_b32_e32 v122, v33
	v_mov_b32_e32 v123, v29
	v_mov_b32_e32 v120, v32
	v_mov_b32_e32 v121, v28
	v_pk_mul_f32 v[122:123], v[122:123], v[122:123]
	v_mov_b32_e32 v124, v35
	v_mov_b32_e32 v125, v31
	v_pk_fma_f32 v[120:121], v[120:121], v[120:121], v[122:123]
	v_mov_b32_e32 v122, v34
	v_mov_b32_e32 v123, v30
	v_pk_mul_f32 v[124:125], v[124:125], v[124:125]
	s_addc_u32 s15, s15, 0
	v_pk_fma_f32 v[122:123], v[122:123], v[122:123], v[124:125]
	s_waitcnt vmcnt(14)
	v_lshlrev_b32_e32 v124, 16, v116
	v_and_b32_e32 v125, 0xffff0000, v112
	v_pk_add_f32 v[120:121], v[120:121], v[122:123]
	v_lshlrev_b32_e32 v122, 16, v112
	v_and_b32_e32 v123, 0xffff0000, v116
	v_pk_mul_f32 v[124:125], v[2:3], v[124:125]
	v_lshlrev_b32_e32 v112, 16, v117
	v_pk_fma_f32 v[122:123], v[2:3], v[122:123], v[124:125] op_sel:[1,0,0] op_sel_hi:[0,1,1]
	v_lshlrev_b32_e32 v124, 16, v113
	v_and_b32_e32 v113, 0xffff0000, v113
	v_and_b32_e32 v125, 0xffff0000, v117
	v_pk_mul_f32 v[112:113], v[2:3], v[112:113]
	v_pk_fma_f32 v[24:25], v[122:123], v[146:147], v[24:25]
	v_pk_fma_f32 v[112:113], v[2:3], v[124:125], v[112:113] op_sel:[1,0,0] op_sel_hi:[0,1,1]
	v_pk_fma_f32 v[26:27], v[112:113], v[148:149], v[26:27]
	v_pk_mul_f32 v[116:117], v[24:25], v[24:25]
	v_pk_mul_f32 v[112:113], v[26:27], v[26:27]
	s_add_u32 s16, s16, 0x4000
	v_pk_mov_b32 v[122:123], v[116:117], v[112:113] op_sel:[1,0]
	v_mov_b32_e32 v117, v113
	v_pk_add_f32 v[112:113], v[122:123], v[116:117]
	s_waitcnt vmcnt(13)
	v_lshlrev_b32_e32 v122, 16, v104
	s_waitcnt vmcnt(9)
	v_and_b32_e32 v123, 0xffff0000, v106
	v_lshlrev_b32_e32 v116, 16, v106
	v_and_b32_e32 v117, 0xffff0000, v104
	v_pk_mul_f32 v[122:123], v[2:3], v[122:123]
	v_lshlrev_b32_e32 v104, 16, v105
	v_pk_fma_f32 v[116:117], v[2:3], v[116:117], v[122:123] op_sel:[1,0,0] op_sel_hi:[0,1,1]
	v_and_b32_e32 v123, 0xffff0000, v105
	v_and_b32_e32 v105, 0xffff0000, v107
	v_lshlrev_b32_e32 v122, 16, v107
	v_pk_mul_f32 v[104:105], v[2:3], v[104:105]
	v_lshlrev_b32_e32 v106, 16, v92
	v_pk_fma_f32 v[104:105], v[2:3], v[122:123], v[104:105] op_sel:[1,0,0] op_sel_hi:[0,1,1]
	s_waitcnt vmcnt(8)
	v_and_b32_e32 v107, 0xffff0000, v94
	v_pk_fma_f32 v[22:23], v[104:105], v[152:153], v[22:23]
	v_lshlrev_b32_e32 v104, 16, v94
	v_and_b32_e32 v105, 0xffff0000, v92
	v_pk_mul_f32 v[106:107], v[2:3], v[106:107]
	v_lshlrev_b32_e32 v92, 16, v93
	v_pk_fma_f32 v[104:105], v[2:3], v[104:105], v[106:107] op_sel:[1,0,0] op_sel_hi:[0,1,1]
	v_and_b32_e32 v107, 0xffff0000, v93
	v_and_b32_e32 v93, 0xffff0000, v95
	v_lshlrev_b32_e32 v106, 16, v95
	v_pk_mul_f32 v[92:93], v[2:3], v[92:93]
	v_pk_fma_f32 v[16:17], v[104:105], v[56:57], v[16:17]
	v_pk_fma_f32 v[92:93], v[2:3], v[106:107], v[92:93] op_sel:[1,0,0] op_sel_hi:[0,1,1]
	v_pk_fma_f32 v[18:19], v[92:93], v[58:59], v[18:19]
	v_mul_f32_e32 v58, v16, v16
	v_pk_add_f32 v[56:57], v[120:121], v[120:121] op_sel:[0,1] op_sel_hi:[1,0]
	v_mul_f32_e32 v92, v17, v17
	v_mov_b32_e32 v57, v58
	v_pk_add_f32 v[58:59], v[112:113], v[112:113] op_sel:[0,1] op_sel_hi:[1,0]
	v_pk_fma_f32 v[20:21], v[116:117], v[150:151], v[20:21]
	v_mov_b32_e32 v59, v92
	v_pk_add_f32 v[56:57], v[56:57], v[58:59]
	v_mul_f32_e32 v58, v21, v21
	v_mul_f32_e32 v93, v18, v18
	v_pk_fma_f32 v[58:59], v[20:21], v[20:21], v[58:59] op_sel_hi:[1,1,0]
	v_mul_f32_e32 v92, v23, v23
	v_mul_f32_e32 v94, v19, v19
	v_mov_b32_e32 v59, v93
	v_pk_fma_f32 v[92:93], v[22:23], v[22:23], v[92:93] op_sel_hi:[1,1,0]
	s_addc_u32 s17, s17, 0
	v_mov_b32_e32 v93, v94
	v_pk_add_f32 v[58:59], v[58:59], v[92:93]
	s_waitcnt vmcnt(3)
	v_lshlrev_b32_e32 v92, 16, v84
	v_and_b32_e32 v93, 0xffff0000, v82
	v_pk_add_f32 v[56:57], v[56:57], v[58:59]
	v_lshlrev_b32_e32 v58, 16, v82
	v_and_b32_e32 v59, 0xffff0000, v84
	v_pk_mul_f32 v[92:93], v[2:3], v[92:93]
	v_lshlrev_b32_e32 v82, 16, v85
	v_pk_fma_f32 v[58:59], v[2:3], v[58:59], v[92:93] op_sel:[1,0,0] op_sel_hi:[0,1,1]
	v_lshlrev_b32_e32 v92, 16, v83
	v_and_b32_e32 v83, 0xffff0000, v83
	v_and_b32_e32 v93, 0xffff0000, v85
	v_pk_mul_f32 v[82:83], v[2:3], v[82:83]
	v_pk_fma_f32 v[12:13], v[58:59], v[52:53], v[12:13]
	v_pk_fma_f32 v[82:83], v[2:3], v[92:93], v[82:83] op_sel:[1,0,0] op_sel_hi:[0,1,1]
	v_pk_fma_f32 v[14:15], v[82:83], v[54:55], v[14:15]
	v_pk_mul_f32 v[54:55], v[12:13], v[12:13]
	v_pk_mul_f32 v[52:53], v[14:15], v[14:15]
	s_add_u32 s18, s18, 0x12000
	v_pk_mov_b32 v[58:59], v[54:55], v[52:53] op_sel:[1,0]
	v_mov_b32_e32 v55, v53
	v_pk_add_f32 v[52:53], v[58:59], v[54:55]
	s_waitcnt vmcnt(2)
	v_lshlrev_b32_e32 v58, 16, v80
	v_and_b32_e32 v59, 0xffff0000, v78
	v_lshlrev_b32_e32 v54, 16, v78
	v_and_b32_e32 v55, 0xffff0000, v80
	v_pk_mul_f32 v[58:59], v[2:3], v[58:59]
	v_lshlrev_b32_e32 v78, 16, v81
	v_pk_fma_f32 v[54:55], v[2:3], v[54:55], v[58:59] op_sel:[1,0,0] op_sel_hi:[0,1,1]
	v_lshlrev_b32_e32 v58, 16, v79
	v_and_b32_e32 v79, 0xffff0000, v79
	v_and_b32_e32 v59, 0xffff0000, v81
	v_pk_mul_f32 v[78:79], v[2:3], v[78:79]
	v_pk_fma_f32 v[92:93], v[54:55], v[48:49], v[8:9]
	v_pk_fma_f32 v[58:59], v[2:3], v[58:59], v[78:79] op_sel:[1,0,0] op_sel_hi:[0,1,1]
	s_waitcnt vmcnt(1)
	v_lshlrev_b32_e32 v48, 16, v74
	s_waitcnt vmcnt(0)
	v_and_b32_e32 v49, 0xffff0000, v76
	v_pk_fma_f32 v[10:11], v[58:59], v[50:51], v[10:11]
	v_lshlrev_b32_e32 v8, 16, v76
	v_and_b32_e32 v9, 0xffff0000, v74
	v_pk_mul_f32 v[48:49], v[2:3], v[48:49]
	v_lshlrev_b32_e32 v50, 16, v75
	v_and_b32_e32 v51, 0xffff0000, v77
	v_pk_fma_f32 v[8:9], v[2:3], v[8:9], v[48:49] op_sel:[1,0,0] op_sel_hi:[0,1,1]
	v_lshlrev_b32_e32 v48, 16, v77
	v_and_b32_e32 v49, 0xffff0000, v75
	v_pk_mul_f32 v[50:51], v[2:3], v[50:51]
	v_pk_fma_f32 v[104:105], v[44:45], v[8:9], v[4:5]
	v_pk_fma_f32 v[2:3], v[2:3], v[48:49], v[50:51] op_sel:[1,0,0] op_sel_hi:[0,1,1]
	v_pk_fma_f32 v[94:95], v[46:47], v[2:3], v[6:7]
	v_mul_f32_e32 v4, v104, v104
	v_pk_add_f32 v[2:3], v[56:57], v[56:57] op_sel:[0,1] op_sel_hi:[1,0]
	v_mul_f32_e32 v6, v105, v105
	v_mov_b32_e32 v3, v4
	v_pk_add_f32 v[4:5], v[52:53], v[52:53] op_sel:[0,1] op_sel_hi:[1,0]
	v_mul_f32_e32 v7, v94, v94
	v_mov_b32_e32 v5, v6
	v_pk_add_f32 v[2:3], v[2:3], v[4:5]
	v_mul_f32_e32 v4, v93, v93
	v_pk_fma_f32 v[4:5], v[92:93], v[92:93], v[4:5] op_sel_hi:[1,1,0]
	v_mul_f32_e32 v6, v11, v11
	v_mul_f32_e32 v8, v95, v95
	v_mov_b32_e32 v5, v7
	v_pk_fma_f32 v[6:7], v[10:11], v[10:11], v[6:7] op_sel_hi:[1,1,0]
	s_addc_u32 s19, s19, 0
	v_mov_b32_e32 v7, v8
	v_pk_add_f32 v[4:5], v[4:5], v[6:7]
	s_cmp_gt_u32 s3, 5
	v_pk_add_f32 v[2:3], v[2:3], v[4:5]
	v_mov_b32_e32 v5, v128
	v_mov_b32_e32 v4, v2
	v_mov_b32_e32 v128, v3
	v_pk_add_f32 v[2:3], v[4:5], v[128:129]
	ds_bpermute_b32 v5, v65, v3
	ds_bpermute_b32 v4, v65, v2
	s_waitcnt lgkmcnt(0)
	v_pk_add_f32 v[2:3], v[2:3], v[4:5]
	ds_bpermute_b32 v5, v130, v3
	ds_bpermute_b32 v4, v130, v2
	s_waitcnt lgkmcnt(0)
	v_pk_add_f32 v[2:3], v[2:3], v[4:5]
	ds_bpermute_b32 v5, v131, v3
	ds_bpermute_b32 v4, v131, v2
	s_waitcnt lgkmcnt(0)
	v_pk_add_f32 v[2:3], v[2:3], v[4:5]
	ds_bpermute_b32 v5, v132, v3
	ds_bpermute_b32 v4, v132, v2
	s_waitcnt lgkmcnt(0)
	v_pk_add_f32 v[2:3], v[2:3], v[4:5]
	ds_bpermute_b32 v5, v133, v3
	ds_bpermute_b32 v4, v133, v2
	s_waitcnt lgkmcnt(0)
	v_pk_add_f32 v[52:53], v[2:3], v[4:5]
	ds_bpermute_b32 v55, v134, v53
	ds_bpermute_b32 v54, v134, v52
	ds_read_b128 v[2:5], v137 offset:8192
	ds_read_b128 v[6:9], v137 offset:9216
	ds_read_b128 v[44:47], v137 offset:10240
	ds_read_b128 v[48:51], v137 offset:11264
	s_waitcnt lgkmcnt(4)
	v_pk_add_f32 v[52:53], v[52:53], v[54:55]
	s_nop 0
	v_pk_fma_f32 v[106:107], v[52:53], s[8:9], v[64:65] op_sel_hi:[1,0,0]
	s_nop 0
	v_mul_f32_e32 v52, 0x4b800000, v107
	v_cmp_gt_f32_e32 vcc, s26, v107
	s_nop 1
	v_cndmask_b32_e32 v52, v107, v52, vcc
	v_rsq_f32_e32 v82, v52
	ds_read_b128 v[52:55], v137 offset:12288
	ds_read_b128 v[56:59], v137 offset:13312
	ds_read_b128 v[74:77], v137 offset:14336
	ds_read_b128 v[78:81], v137 offset:15360
	v_mul_f32_e32 v83, 0x45800000, v82
	v_cndmask_b32_e32 v112, v82, v83, vcc
	v_pk_mul_f32 v[82:83], v[90:91], v[112:113] op_sel_hi:[1,0]
	v_pk_mul_f32 v[84:85], v[88:89], v[112:113] op_sel_hi:[1,0]
	s_waitcnt lgkmcnt(7)
	v_pk_mul_f32 v[82:83], v[2:3], v[82:83]
	v_pk_mul_f32 v[84:85], v[4:5], v[84:85]
	global_store_dwordx4 v[72:73], v[82:85], off
	v_pk_mul_f32 v[0:1], v[0:1], v[112:113] op_sel_hi:[1,0]
	v_cmp_gt_f32_e32 vcc, s26, v106
	v_pk_mul_f32 v[82:83], v[86:87], v[112:113] op_sel_hi:[1,0]
	s_waitcnt lgkmcnt(6)
	v_pk_mul_f32 v[84:85], v[8:9], v[0:1]
	v_pk_mul_f32 v[82:83], v[6:7], v[82:83]
	global_store_dwordx4 v[72:73], v[82:85], off offset:1024
	v_pk_mul_f32 v[0:1], v[96:97], v[112:113] op_sel_hi:[1,0]
	s_nop 0
	v_pk_mul_f32 v[82:83], v[98:99], v[112:113] op_sel_hi:[1,0]
	s_waitcnt lgkmcnt(5)
	v_pk_mul_f32 v[84:85], v[46:47], v[82:83]
	v_pk_mul_f32 v[82:83], v[44:45], v[0:1]
	global_store_dwordx4 v[72:73], v[82:85], off offset:2048
	v_pk_mul_f32 v[0:1], v[102:103], v[112:113] op_sel_hi:[1,0]
	s_nop 0
	v_pk_mul_f32 v[82:83], v[100:101], v[112:113] op_sel_hi:[1,0]
	s_waitcnt lgkmcnt(4)
	v_pk_mul_f32 v[84:85], v[50:51], v[82:83]
	v_pk_mul_f32 v[82:83], v[48:49], v[0:1]
	global_store_dwordx4 v[72:73], v[82:85], off offset:3072
	v_pk_mul_f32 v[0:1], v[110:111], v[112:113] op_sel_hi:[1,0]
	v_pk_mul_f32 v[72:73], v[108:109], v[112:113] op_sel_hi:[1,0]
	s_waitcnt lgkmcnt(3)
	v_pk_mul_f32 v[82:83], v[52:53], v[0:1]
	v_pk_mul_f32 v[84:85], v[54:55], v[72:73]
	v_pk_mul_f32 v[0:1], v[114:115], v[112:113] op_sel_hi:[1,0]
	global_store_dwordx4 v[70:71], v[82:85], off
	v_pk_mul_f32 v[72:73], v[118:119], v[112:113] op_sel_hi:[1,0]
	s_waitcnt lgkmcnt(2)
	v_pk_mul_f32 v[82:83], v[56:57], v[0:1]
	v_pk_mul_f32 v[0:1], v[40:41], v[112:113] op_sel_hi:[1,0]
	v_pk_mul_f32 v[40:41], v[42:43], v[112:113] op_sel_hi:[1,0]
	v_pk_mul_f32 v[84:85], v[58:59], v[72:73]
	s_waitcnt lgkmcnt(1)
	v_pk_mul_f32 v[42:43], v[76:77], v[40:41]
	v_pk_mul_f32 v[40:41], v[74:75], v[0:1]
	v_pk_mul_f32 v[0:1], v[36:37], v[112:113] op_sel_hi:[1,0]
	v_pk_mul_f32 v[36:37], v[38:39], v[112:113] op_sel_hi:[1,0]
	v_mul_f32_e32 v38, 0x4b800000, v106
	v_cndmask_b32_e32 v38, v106, v38, vcc
	global_store_dwordx4 v[70:71], v[40:43], off offset:2048
	global_store_dwordx4 v[70:71], v[82:85], off offset:1024
	s_nop 0
	v_rsq_f32_e32 v40, v38
	s_waitcnt lgkmcnt(0)
	v_pk_mul_f32 v[38:39], v[80:81], v[36:37]
	v_pk_mul_f32 v[36:37], v[78:79], v[0:1]
	global_store_dwordx4 v[70:71], v[36:39], off offset:3072
	v_mul_f32_e32 v0, 0x45800000, v40
	s_nop 0
	v_cndmask_b32_e32 v36, v40, v0, vcc
	v_pk_mul_f32 v[0:1], v[32:33], v[36:37] op_sel_hi:[1,0]
	v_pk_mul_f32 v[32:33], v[34:35], v[36:37] op_sel_hi:[1,0]
	v_pk_mul_f32 v[2:3], v[2:3], v[0:1]
	v_pk_mul_f32 v[4:5], v[4:5], v[32:33]
	global_store_dwordx4 v[68:69], v[2:5], off
	v_pk_mul_f32 v[0:1], v[28:29], v[36:37] op_sel_hi:[1,0]
	s_nop 0
	v_pk_mul_f32 v[2:3], v[30:31], v[36:37] op_sel_hi:[1,0]
	v_pk_mul_f32 v[0:1], v[6:7], v[0:1]
	v_pk_mul_f32 v[2:3], v[8:9], v[2:3]
	global_store_dwordx4 v[68:69], v[0:3], off offset:1024
	s_nop 1
	v_pk_mul_f32 v[0:1], v[24:25], v[36:37] op_sel_hi:[1,0]
	v_pk_mul_f32 v[2:3], v[26:27], v[36:37] op_sel_hi:[1,0]
	v_pk_mul_f32 v[0:1], v[44:45], v[0:1]
	v_pk_mul_f32 v[2:3], v[46:47], v[2:3]
	global_store_dwordx4 v[68:69], v[0:3], off offset:2048
	s_nop 1
	v_pk_mul_f32 v[0:1], v[20:21], v[36:37] op_sel_hi:[1,0]
	v_pk_mul_f32 v[2:3], v[22:23], v[36:37] op_sel_hi:[1,0]
	v_pk_mul_f32 v[0:1], v[48:49], v[0:1]
	v_pk_mul_f32 v[2:3], v[50:51], v[2:3]
	global_store_dwordx4 v[68:69], v[0:3], off offset:3072
	s_nop 1
	v_pk_mul_f32 v[0:1], v[16:17], v[36:37] op_sel_hi:[1,0]
	v_pk_mul_f32 v[2:3], v[18:19], v[36:37] op_sel_hi:[1,0]
	v_pk_mul_f32 v[0:1], v[52:53], v[0:1]
	v_pk_mul_f32 v[2:3], v[54:55], v[2:3]
	global_store_dwordx4 v[66:67], v[0:3], off
	s_nop 1
	v_pk_mul_f32 v[0:1], v[12:13], v[36:37] op_sel_hi:[1,0]
	v_pk_mul_f32 v[2:3], v[14:15], v[36:37] op_sel_hi:[1,0]
	v_pk_mul_f32 v[0:1], v[56:57], v[0:1]
	v_pk_mul_f32 v[2:3], v[58:59], v[2:3]
	global_store_dwordx4 v[66:67], v[0:3], off offset:1024
	s_nop 1
	v_pk_mul_f32 v[0:1], v[92:93], v[36:37] op_sel_hi:[1,0]
	v_pk_mul_f32 v[2:3], v[10:11], v[36:37] op_sel_hi:[1,0]
	v_pk_mul_f32 v[0:1], v[74:75], v[0:1]
	v_pk_mul_f32 v[2:3], v[76:77], v[2:3]
	global_store_dwordx4 v[66:67], v[0:3], off offset:2048
	s_nop 1
	v_pk_mul_f32 v[0:1], v[104:105], v[36:37] op_sel_hi:[1,0]
	v_pk_mul_f32 v[2:3], v[94:95], v[36:37] op_sel_hi:[1,0]
	v_pk_mul_f32 v[0:1], v[78:79], v[0:1]
	v_pk_mul_f32 v[2:3], v[80:81], v[2:3]
	global_store_dwordx4 v[66:67], v[0:3], off offset:3072
	s_cbranch_scc0 .LBB0_1492
	s_add_i32 s81, s81, s72
	s_add_i32 s9, s9, s20
	s_add_i32 s4, s4, s21
	s_add_i32 s2, s2, s21
	s_cmpk_gt_i32 s81, 0xff
	s_cbranch_scc0 .LBB0_1489
